# v8 variant: permuted pipelined epilogue stores use the workspace base in SGPRs plus a 32-bit per-lane offset (one address VGPR and one ds_bpermute fewer per store)
# baseline (speedup 1.0000x reference)
.LBB0_174:
	v_mbcnt_lo_u32_b32 v244, -1, 0
	v_mbcnt_hi_u32_b32 v244, -1, v244
	v_lshrrev_b32_e32 v245, 2, v244
	v_and_b32_e32 v244, 3, v244
	v_lshl_add_u32 v244, v244, 4, v245
	v_lshlrev_b32_e32 v244, 2, v244
	s_ashr_i32 s15, s60, 3
	s_add_i32 s62, s15, s75
	s_lshl_b32 s15, s60, 8
	s_and_b32 s15, s15, 0x700
	s_cmp_eq_u32 s62, 0
	v_lshl_add_u32 v174, s28, 8, v1
	s_cselect_b64 s[26:27], -1, 0
	v_or_b32_e32 v82, s15, v209
	s_and_b64 s[26:27], s[50:51], s[26:27]
	v_or_b32_e32 v180, 16, v174
	v_or_b32_e32 v178, 32, v174
	v_or_b32_e32 v176, 48, v174
	s_mov_b64 s[64:65], -1
	s_and_b64 vcc, exec, s[26:27]
	v_lshlrev_b32_e32 v114, 1, v82
	v_ashrrev_i32_e32 v175, 31, v174
	v_ashrrev_i32_e32 v181, 31, v180
	v_ashrrev_i32_e32 v179, 31, v178
	v_ashrrev_i32_e32 v177, 31, v176
	s_cbranch_vccnz .LBB0_177
	v_lshl_add_u32 v158, s14, 10, v210
	ds_read2_b32 v[88:89], v158 offset1:16
	s_ashr_i32 s63, s62, 31
	s_lshl_b64 s[26:27], s[62:63], 25
	s_add_u32 s26, s84, s26
	s_addc_u32 s27, s85, s27
	v_lshl_add_u64 v[90:91], s[26:27], 0, v[114:115]
	v_lshlrev_b64 v[82:83], 12, v[174:175]
	s_waitcnt lgkmcnt(0)
	v_pk_mul_f32 v[84:85], v[144:145], v[88:89] op_sel_hi:[1,0]
	v_lshl_add_u64 v[82:83], v[90:91], 0, v[82:83]
	v_pk_mul_f32 v[86:87], v[146:147], v[88:89] op_sel_hi:[1,0]
	v_cvt_pk_bf16_f32 v84, v84, v85
	v_pk_mul_f32 v[92:93], v[142:143], v[88:89] op_sel_hi:[1,0]
	v_cvt_pk_bf16_f32 v85, v86, v87
	v_pk_mul_f32 v[94:95], v[140:141], v[88:89] op_sel_hi:[1,0]
	v_cvt_pk_bf16_f32 v87, v92, v93
	v_pk_mul_f32 v[92:93], v[134:135], v[88:89] op_sel_hi:[1,0]
	v_cvt_pk_bf16_f32 v86, v94, v95
	ds_bpermute_b32 v232, v244, v84
	ds_bpermute_b32 v233, v244, v85
	ds_bpermute_b32 v234, v244, v86
	ds_bpermute_b32 v235, v244, v87
	ds_bpermute_b32 v236, v244, v82
	v_pk_mul_f32 v[94:95], v[132:133], v[88:89] op_sel_hi:[1,0]
	s_mov_b32 s15, 0x80000
	v_pk_mul_f32 v[84:85], v[136:137], v[88:89] op_sel_hi:[1,0]
	v_pk_mul_f32 v[86:87], v[138:139], v[88:89] op_sel_hi:[1,0]
	v_cvt_pk_bf16_f32 v84, v84, v85
	v_mov_b32_e32 v88, v89
	v_cvt_pk_bf16_f32 v85, v86, v87
	v_cvt_pk_bf16_f32 v86, v94, v95
	v_cvt_pk_bf16_f32 v87, v92, v93
	s_waitcnt lgkmcnt(0)
	v_subrev_u32_e32 v236, s82, v236
	global_store_dwordx4 v236, v[232:235], s[82:83]
	ds_bpermute_b32 v238, v244, v84
	ds_bpermute_b32 v239, v244, v85
	ds_bpermute_b32 v240, v244, v86
	ds_bpermute_b32 v241, v244, v87
	ds_bpermute_b32 v242, v244, v82
	v_pk_mul_f32 v[94:95], v[126:127], v[88:89] op_sel_hi:[1,0]
	v_pk_mul_f32 v[96:97], v[124:125], v[88:89] op_sel_hi:[1,0]
	v_lshlrev_b64 v[84:85], 12, v[180:181]
	v_lshl_add_u64 v[92:93], v[90:91], 0, v[84:85]
	v_pk_mul_f32 v[86:87], v[130:131], v[88:89] op_sel_hi:[1,0]
	v_pk_mul_f32 v[84:85], v[128:129], v[88:89] op_sel_hi:[1,0]
	s_mov_b64 s[16:17], 0x80000
	v_cvt_pk_bf16_f32 v84, v84, v85
	v_cvt_pk_bf16_f32 v85, v86, v87
	v_cvt_pk_bf16_f32 v86, v96, v97
	v_cvt_pk_bf16_f32 v87, v94, v95
	s_waitcnt lgkmcnt(0)
	v_subrev_u32_e32 v242, s82, v242
	global_store_dwordx4 v242, v[238:241], s[82:83] offset:64
	ds_bpermute_b32 v232, v244, v84
	ds_bpermute_b32 v233, v244, v85
	ds_bpermute_b32 v234, v244, v86
	ds_bpermute_b32 v235, v244, v87
	ds_bpermute_b32 v236, v244, v92
	v_pk_mul_f32 v[94:95], v[118:119], v[88:89] op_sel_hi:[1,0]
	s_nop 0
	v_pk_mul_f32 v[86:87], v[122:123], v[88:89] op_sel_hi:[1,0]
	v_pk_mul_f32 v[84:85], v[120:121], v[88:89] op_sel_hi:[1,0]
	v_pk_mul_f32 v[88:89], v[116:117], v[88:89] op_sel_hi:[1,0]
	v_cvt_pk_bf16_f32 v84, v84, v85
	v_cvt_pk_bf16_f32 v85, v86, v87
	v_cvt_pk_bf16_f32 v87, v94, v95
	s_nop 0
	v_cvt_pk_bf16_f32 v86, v88, v89
	ds_read2_b32 v[88:89], v158 offset0:32 offset1:48
	s_waitcnt lgkmcnt(0)
	v_subrev_u32_e32 v236, s82, v236
	global_store_dwordx4 v236, v[232:235], s[82:83]
	ds_bpermute_b32 v238, v244, v84
	ds_bpermute_b32 v239, v244, v85
	ds_bpermute_b32 v240, v244, v86
	ds_bpermute_b32 v241, v244, v87
	ds_bpermute_b32 v242, v244, v92
	s_waitcnt lgkmcnt(0)
	v_pk_mul_f32 v[94:95], v[108:109], v[88:89] op_sel_hi:[1,0]
	v_lshlrev_b64 v[84:85], 12, v[178:179]
	v_lshl_add_u64 v[92:93], v[90:91], 0, v[84:85]
	v_pk_mul_f32 v[84:85], v[110:111], v[88:89] op_sel_hi:[1,0]
	v_pk_mul_f32 v[86:87], v[112:113], v[88:89] op_sel_hi:[1,0]
	v_cvt_pk_bf16_f32 v84, v84, v85
	v_pk_mul_f32 v[96:97], v[106:107], v[88:89] op_sel_hi:[1,0]
	v_cvt_pk_bf16_f32 v85, v86, v87
	v_cvt_pk_bf16_f32 v87, v94, v95
	v_pk_mul_f32 v[94:95], v[100:101], v[88:89] op_sel_hi:[1,0]
	v_cvt_pk_bf16_f32 v86, v96, v97
	s_waitcnt lgkmcnt(0)
	v_subrev_u32_e32 v242, s82, v242
	global_store_dwordx4 v242, v[238:241], s[82:83] offset:64
	ds_bpermute_b32 v232, v244, v84
	ds_bpermute_b32 v233, v244, v85
	ds_bpermute_b32 v234, v244, v86
	ds_bpermute_b32 v235, v244, v87
	ds_bpermute_b32 v236, v244, v92
	v_pk_mul_f32 v[96:97], v[98:99], v[88:89] op_sel_hi:[1,0]
	s_nop 0
	v_pk_mul_f32 v[84:85], v[102:103], v[88:89] op_sel_hi:[1,0]
	v_pk_mul_f32 v[86:87], v[104:105], v[88:89] op_sel_hi:[1,0]
	v_cvt_pk_bf16_f32 v84, v84, v85
	v_mov_b32_e32 v88, v89
	v_cvt_pk_bf16_f32 v85, v86, v87
	v_cvt_pk_bf16_f32 v86, v96, v97
	v_cvt_pk_bf16_f32 v87, v94, v95
	s_waitcnt lgkmcnt(0)
	v_subrev_u32_e32 v236, s82, v236
	global_store_dwordx4 v236, v[232:235], s[82:83]
	ds_bpermute_b32 v238, v244, v84
	ds_bpermute_b32 v239, v244, v85
	ds_bpermute_b32 v240, v244, v86
	ds_bpermute_b32 v241, v244, v87
	ds_bpermute_b32 v242, v244, v92
	v_pk_mul_f32 v[94:95], v[74:75], v[88:89] op_sel_hi:[1,0]
	v_pk_mul_f32 v[92:93], v[76:77], v[88:89] op_sel_hi:[1,0]
	v_lshlrev_b64 v[84:85], 12, v[176:177]
	v_lshl_add_u64 v[90:91], v[90:91], 0, v[84:85]
	v_pk_mul_f32 v[86:87], v[80:81], v[88:89] op_sel_hi:[1,0]
	v_pk_mul_f32 v[84:85], v[78:79], v[88:89] op_sel_hi:[1,0]
	s_nop 0
	v_cvt_pk_bf16_f32 v84, v84, v85
	v_cvt_pk_bf16_f32 v85, v86, v87
	v_cvt_pk_bf16_f32 v86, v94, v95
	ds_read2_b32 v[94:95], v158 offset0:128 offset1:144
	v_cvt_pk_bf16_f32 v87, v92, v93
	s_waitcnt lgkmcnt(0)
	v_subrev_u32_e32 v242, s82, v242
	global_store_dwordx4 v242, v[238:241], s[82:83] offset:64
	ds_bpermute_b32 v232, v244, v84
	ds_bpermute_b32 v233, v244, v85
	ds_bpermute_b32 v234, v244, v86
	ds_bpermute_b32 v235, v244, v87
	ds_bpermute_b32 v236, v244, v90
	v_pk_mul_f32 v[92:93], v[68:69], v[88:89] op_sel_hi:[1,0]
	s_nop 0
	v_pk_mul_f32 v[86:87], v[72:73], v[88:89] op_sel_hi:[1,0]
	v_pk_mul_f32 v[84:85], v[70:71], v[88:89] op_sel_hi:[1,0]
	v_pk_mul_f32 v[88:89], v[66:67], v[88:89] op_sel_hi:[1,0]
	v_cvt_pk_bf16_f32 v84, v84, v85
	v_cvt_pk_bf16_f32 v85, v86, v87
	v_cvt_pk_bf16_f32 v87, v92, v93
	s_waitcnt lgkmcnt(0)
	v_pk_mul_f32 v[92:93], v[58:59], v[94:95] op_sel_hi:[1,0]
	v_cvt_pk_bf16_f32 v86, v88, v89
	s_waitcnt lgkmcnt(0)
	v_subrev_u32_e32 v236, s82, v236
	global_store_dwordx4 v236, v[232:235], s[82:83]
	ds_bpermute_b32 v238, v244, v84
	ds_bpermute_b32 v239, v244, v85
	ds_bpermute_b32 v240, v244, v86
	ds_bpermute_b32 v241, v244, v87
	ds_bpermute_b32 v242, v244, v90
	v_pk_mul_f32 v[90:91], v[60:61], v[94:95] op_sel_hi:[1,0]
	v_lshl_add_u64 v[88:89], v[82:83], 0, s[16:17]
	v_pk_mul_f32 v[86:87], v[64:65], v[94:95] op_sel_hi:[1,0]
	v_pk_mul_f32 v[84:85], v[62:63], v[94:95] op_sel_hi:[1,0]
	s_mov_b64 s[16:17], 0x90000
	v_cvt_pk_bf16_f32 v84, v84, v85
	v_cvt_pk_bf16_f32 v85, v86, v87
	v_cvt_pk_bf16_f32 v87, v90, v91
	v_add_co_u32_e32 v90, vcc, s15, v82
	v_cvt_pk_bf16_f32 v86, v92, v93
	v_pk_mul_f32 v[92:93], v[50:51], v[94:95] op_sel_hi:[1,0]
	s_nop 0
	v_addc_co_u32_e32 v91, vcc, 0, v83, vcc
	s_waitcnt lgkmcnt(0)
	v_subrev_u32_e32 v242, s82, v242
	global_store_dwordx4 v242, v[238:241], s[82:83] offset:64
	ds_bpermute_b32 v232, v244, v84
	ds_bpermute_b32 v233, v244, v85
	ds_bpermute_b32 v234, v244, v86
	ds_bpermute_b32 v235, v244, v87
	ds_bpermute_b32 v236, v244, v90
	v_pk_mul_f32 v[90:91], v[52:53], v[94:95] op_sel_hi:[1,0]
	s_mov_b32 s15, 0x90000
	v_pk_mul_f32 v[86:87], v[56:57], v[94:95] op_sel_hi:[1,0]
	v_pk_mul_f32 v[84:85], v[54:55], v[94:95] op_sel_hi:[1,0]
	s_nop 0
	v_cvt_pk_bf16_f32 v84, v84, v85
	v_cvt_pk_bf16_f32 v85, v86, v87
	v_cvt_pk_bf16_f32 v86, v92, v93
	v_cvt_pk_bf16_f32 v87, v90, v91
	v_mov_b32_e32 v90, v95
	s_waitcnt lgkmcnt(0)
	v_subrev_u32_e32 v236, s82, v236
	global_store_dwordx4 v236, v[232:235], s[82:83]
	ds_bpermute_b32 v238, v244, v84
	ds_bpermute_b32 v239, v244, v85
	ds_bpermute_b32 v240, v244, v86
	ds_bpermute_b32 v241, v244, v87
	ds_bpermute_b32 v242, v244, v88
	v_pk_mul_f32 v[94:95], v[42:43], v[90:91] op_sel_hi:[1,0]
	v_pk_mul_f32 v[92:93], v[44:45], v[90:91] op_sel_hi:[1,0]
	v_pk_mul_f32 v[86:87], v[48:49], v[90:91] op_sel_hi:[1,0]
	v_pk_mul_f32 v[84:85], v[46:47], v[90:91] op_sel_hi:[1,0]
	v_lshl_add_u64 v[88:89], v[82:83], 0, s[16:17]
	v_cvt_pk_bf16_f32 v84, v84, v85
	v_cvt_pk_bf16_f32 v85, v86, v87
	v_cvt_pk_bf16_f32 v86, v94, v95
	ds_read2_b32 v[94:95], v158 offset0:160 offset1:176
	v_cvt_pk_bf16_f32 v87, v92, v93
	v_add_co_u32_e32 v92, vcc, s15, v82
	s_mov_b32 s15, 0xa0000
	s_nop 0
	v_addc_co_u32_e32 v93, vcc, 0, v83, vcc
	s_waitcnt lgkmcnt(0)
	v_subrev_u32_e32 v242, s82, v242
	global_store_dwordx4 v242, v[238:241], s[82:83] offset:64
	ds_bpermute_b32 v232, v244, v84
	ds_bpermute_b32 v233, v244, v85
	ds_bpermute_b32 v234, v244, v86
	ds_bpermute_b32 v235, v244, v87
	ds_bpermute_b32 v236, v244, v92
	v_pk_mul_f32 v[92:93], v[36:37], v[90:91] op_sel_hi:[1,0]
	s_mov_b64 s[16:17], 0xa0000
	v_pk_mul_f32 v[86:87], v[40:41], v[90:91] op_sel_hi:[1,0]
	v_pk_mul_f32 v[84:85], v[38:39], v[90:91] op_sel_hi:[1,0]
	v_pk_mul_f32 v[90:91], v[34:35], v[90:91] op_sel_hi:[1,0]
	v_cvt_pk_bf16_f32 v84, v84, v85
	v_cvt_pk_bf16_f32 v85, v86, v87
	v_cvt_pk_bf16_f32 v87, v92, v93
	s_waitcnt lgkmcnt(0)
	v_pk_mul_f32 v[92:93], v[26:27], v[94:95] op_sel_hi:[1,0]
	v_cvt_pk_bf16_f32 v86, v90, v91
	s_waitcnt lgkmcnt(0)
	v_subrev_u32_e32 v236, s82, v236
	global_store_dwordx4 v236, v[232:235], s[82:83]
	ds_bpermute_b32 v238, v244, v84
	ds_bpermute_b32 v239, v244, v85
	ds_bpermute_b32 v240, v244, v86
	ds_bpermute_b32 v241, v244, v87
	ds_bpermute_b32 v242, v244, v88
	v_pk_mul_f32 v[90:91], v[28:29], v[94:95] op_sel_hi:[1,0]
	v_lshl_add_u64 v[88:89], v[82:83], 0, s[16:17]
	v_pk_mul_f32 v[86:87], v[32:33], v[94:95] op_sel_hi:[1,0]
	v_pk_mul_f32 v[84:85], v[30:31], v[94:95] op_sel_hi:[1,0]
	s_mov_b64 s[16:17], 0xb0000
	v_cvt_pk_bf16_f32 v84, v84, v85
	v_cvt_pk_bf16_f32 v85, v86, v87
	v_cvt_pk_bf16_f32 v87, v90, v91
	v_add_co_u32_e32 v90, vcc, s15, v82
	v_cvt_pk_bf16_f32 v86, v92, v93
	s_mov_b32 s15, 0xb0000
	s_nop 0
	v_addc_co_u32_e32 v91, vcc, 0, v83, vcc
	s_waitcnt lgkmcnt(0)
	v_subrev_u32_e32 v242, s82, v242
	global_store_dwordx4 v242, v[238:241], s[82:83] offset:64
	ds_bpermute_b32 v232, v244, v84
	ds_bpermute_b32 v233, v244, v85
	ds_bpermute_b32 v234, v244, v86
	ds_bpermute_b32 v235, v244, v87
	ds_bpermute_b32 v236, v244, v90
	v_pk_mul_f32 v[90:91], v[20:21], v[94:95] op_sel_hi:[1,0]
	v_pk_mul_f32 v[92:93], v[18:19], v[94:95] op_sel_hi:[1,0]
	v_pk_mul_f32 v[86:87], v[24:25], v[94:95] op_sel_hi:[1,0]
	v_pk_mul_f32 v[84:85], v[22:23], v[94:95] op_sel_hi:[1,0]
	s_nop 0
	v_cvt_pk_bf16_f32 v84, v84, v85
	v_cvt_pk_bf16_f32 v85, v86, v87
	v_cvt_pk_bf16_f32 v87, v90, v91
	v_mov_b32_e32 v90, v95
	v_cvt_pk_bf16_f32 v86, v92, v93
	s_waitcnt lgkmcnt(0)
	v_subrev_u32_e32 v236, s82, v236
	global_store_dwordx4 v236, v[232:235], s[82:83]
	ds_bpermute_b32 v238, v244, v84
	ds_bpermute_b32 v239, v244, v85
	ds_bpermute_b32 v240, v244, v86
	ds_bpermute_b32 v241, v244, v87
	ds_bpermute_b32 v242, v244, v88
	v_lshl_add_u64 v[88:89], v[82:83], 0, s[16:17]
	v_add_co_u32_e32 v82, vcc, s15, v82
	v_pk_mul_f32 v[84:85], v[14:15], v[90:91] op_sel_hi:[1,0]
	v_pk_mul_f32 v[86:87], v[16:17], v[90:91] op_sel_hi:[1,0]
	v_cvt_pk_bf16_f32 v84, v84, v85
	v_addc_co_u32_e32 v83, vcc, 0, v83, vcc
	v_cvt_pk_bf16_f32 v85, v86, v87
	v_pk_mul_f32 v[92:93], v[12:13], v[90:91] op_sel_hi:[1,0]
	v_pk_mul_f32 v[94:95], v[10:11], v[90:91] op_sel_hi:[1,0]
	v_cvt_pk_bf16_f32 v87, v92, v93
	s_nop 0
	v_cvt_pk_bf16_f32 v86, v94, v95
	s_waitcnt lgkmcnt(0)
	v_subrev_u32_e32 v242, s82, v242
	global_store_dwordx4 v242, v[238:241], s[82:83] offset:64
	ds_bpermute_b32 v232, v244, v84
	ds_bpermute_b32 v233, v244, v85
	ds_bpermute_b32 v234, v244, v86
	ds_bpermute_b32 v235, v244, v87
	ds_bpermute_b32 v236, v244, v82
	v_pk_mul_f32 v[82:83], v[6:7], v[90:91] op_sel_hi:[1,0]
	s_nop 0
	v_pk_mul_f32 v[84:85], v[8:9], v[90:91] op_sel_hi:[1,0]
	v_pk_mul_f32 v[86:87], v[4:5], v[90:91] op_sel_hi:[1,0]
	v_pk_mul_f32 v[90:91], v[2:3], v[90:91] op_sel_hi:[1,0]
	v_cvt_pk_bf16_f32 v82, v82, v83
	v_cvt_pk_bf16_f32 v83, v84, v85
	v_cvt_pk_bf16_f32 v85, v86, v87
	s_nop 0
	v_cvt_pk_bf16_f32 v84, v90, v91
	s_waitcnt lgkmcnt(0)
	v_subrev_u32_e32 v236, s82, v236
	global_store_dwordx4 v236, v[232:235], s[82:83]
	ds_bpermute_b32 v238, v244, v82
	ds_bpermute_b32 v239, v244, v83
	ds_bpermute_b32 v240, v244, v84
	ds_bpermute_b32 v241, v244, v85
	ds_bpermute_b32 v242, v244, v88
	s_waitcnt lgkmcnt(0)
	v_subrev_u32_e32 v242, s82, v242
	global_store_dwordx4 v242, v[238:241], s[82:83] offset:64
	s_cbranch_execz .LBB0_178

.LBB0_178:
	s_lshl_b32 s14, s14, 10
	v_add_u32_e32 v213, s14, v211
	ds_read_b32 v82, v213
	s_waitcnt lgkmcnt(0)
	v_pk_mul_f32 v[84:85], v[146:147], v[82:83] op_sel_hi:[1,0]
	v_pk_mul_f32 v[86:87], v[144:145], v[82:83] op_sel_hi:[1,0]
	v_pk_mul_f32 v[84:85], v[84:85], v[84:85]
	v_pk_mul_f32 v[88:89], v[140:141], v[82:83] op_sel_hi:[1,0]
	v_pk_fma_f32 v[84:85], v[86:87], v[86:87], v[84:85]
	v_pk_mul_f32 v[86:87], v[142:143], v[82:83] op_sel_hi:[1,0]
	s_nop 0
	v_pk_mul_f32 v[86:87], v[86:87], v[86:87]
	s_nop 0
	v_pk_fma_f32 v[86:87], v[88:89], v[88:89], v[86:87]
	v_pk_mul_f32 v[88:89], v[136:137], v[82:83] op_sel_hi:[1,0]
	v_pk_add_f32 v[84:85], v[84:85], v[86:87]
	v_pk_mul_f32 v[86:87], v[138:139], v[82:83] op_sel_hi:[1,0]
	s_nop 0
	v_pk_mul_f32 v[86:87], v[86:87], v[86:87]
	s_nop 0
	v_pk_fma_f32 v[86:87], v[88:89], v[88:89], v[86:87]
	s_nop 0
	v_pk_add_f32 v[84:85], v[86:87], v[84:85]
	v_pk_mul_f32 v[86:87], v[134:135], v[82:83] op_sel_hi:[1,0]
	v_pk_mul_f32 v[82:83], v[132:133], v[82:83] op_sel_hi:[1,0]
	v_pk_mul_f32 v[86:87], v[86:87], v[86:87]
	s_nop 0
	v_pk_fma_f32 v[82:83], v[82:83], v[82:83], v[86:87]
	s_nop 0
	v_pk_add_f32 v[82:83], v[82:83], v[84:85]
	s_nop 0
	v_add_f32_e32 v82, v82, v83
	ds_swizzle_b32 v83, v82 offset:swizzle(SWAP,16)
	s_waitcnt lgkmcnt(0)
	v_add_f32_e32 v82, v82, v83
	v_mov_b32_e32 v83, v82
	s_nop 1
	v_permlane32_swap_b32_e32 v82, v83
	s_and_saveexec_b64 s[62:63], s[38:39]
	v_add_f32_e32 v82, v82, v83
	ds_write_b32 v183, v82
	s_or_b64 exec, exec, s[62:63]
	ds_read_b32 v82, v213 offset:64
	s_waitcnt lgkmcnt(0)
	v_pk_mul_f32 v[84:85], v[130:131], v[82:83] op_sel_hi:[1,0]
	v_pk_mul_f32 v[86:87], v[128:129], v[82:83] op_sel_hi:[1,0]
	v_pk_mul_f32 v[84:85], v[84:85], v[84:85]
	v_pk_mul_f32 v[88:89], v[124:125], v[82:83] op_sel_hi:[1,0]
	v_pk_fma_f32 v[84:85], v[86:87], v[86:87], v[84:85]
	v_pk_mul_f32 v[86:87], v[126:127], v[82:83] op_sel_hi:[1,0]
	s_nop 0
	v_pk_mul_f32 v[86:87], v[86:87], v[86:87]
	s_nop 0
	v_pk_fma_f32 v[86:87], v[88:89], v[88:89], v[86:87]
	v_pk_mul_f32 v[88:89], v[120:121], v[82:83] op_sel_hi:[1,0]
	v_pk_add_f32 v[84:85], v[84:85], v[86:87]
	v_pk_mul_f32 v[86:87], v[122:123], v[82:83] op_sel_hi:[1,0]
	s_nop 0
	v_pk_mul_f32 v[86:87], v[86:87], v[86:87]
	s_nop 0
	v_pk_fma_f32 v[86:87], v[88:89], v[88:89], v[86:87]
	s_nop 0
	v_pk_add_f32 v[84:85], v[86:87], v[84:85]
	v_pk_mul_f32 v[86:87], v[118:119], v[82:83] op_sel_hi:[1,0]
	v_pk_mul_f32 v[82:83], v[116:117], v[82:83] op_sel_hi:[1,0]
	v_pk_mul_f32 v[86:87], v[86:87], v[86:87]
	s_nop 0
	v_pk_fma_f32 v[82:83], v[82:83], v[82:83], v[86:87]
	s_nop 0
	v_pk_add_f32 v[82:83], v[82:83], v[84:85]
	s_nop 0
	v_add_f32_e32 v82, v82, v83
	ds_swizzle_b32 v83, v82 offset:swizzle(SWAP,16)
	s_waitcnt lgkmcnt(0)
	v_add_f32_e32 v82, v82, v83
	v_mov_b32_e32 v83, v82
	s_nop 1
	v_permlane32_swap_b32_e32 v82, v83
	s_and_saveexec_b64 s[62:63], s[38:39]
	v_add_f32_e32 v82, v82, v83
	ds_write_b32 v195, v82
	s_or_b64 exec, exec, s[62:63]
	ds_read_b32 v82, v213 offset:128
	s_waitcnt lgkmcnt(0)
	v_pk_mul_f32 v[84:85], v[112:113], v[82:83] op_sel_hi:[1,0]
	v_pk_mul_f32 v[86:87], v[110:111], v[82:83] op_sel_hi:[1,0]
	v_pk_mul_f32 v[84:85], v[84:85], v[84:85]
	v_pk_mul_f32 v[88:89], v[106:107], v[82:83] op_sel_hi:[1,0]
	v_pk_fma_f32 v[84:85], v[86:87], v[86:87], v[84:85]
	v_pk_mul_f32 v[86:87], v[108:109], v[82:83] op_sel_hi:[1,0]
	s_nop 0
	v_pk_mul_f32 v[86:87], v[86:87], v[86:87]
	s_nop 0
	v_pk_fma_f32 v[86:87], v[88:89], v[88:89], v[86:87]
	v_pk_mul_f32 v[88:89], v[102:103], v[82:83] op_sel_hi:[1,0]
	v_pk_add_f32 v[84:85], v[84:85], v[86:87]
	v_pk_mul_f32 v[86:87], v[104:105], v[82:83] op_sel_hi:[1,0]
	s_nop 0
	v_pk_mul_f32 v[86:87], v[86:87], v[86:87]
	s_nop 0
	v_pk_fma_f32 v[86:87], v[88:89], v[88:89], v[86:87]
	s_nop 0
	v_pk_add_f32 v[84:85], v[86:87], v[84:85]
	v_pk_mul_f32 v[86:87], v[100:101], v[82:83] op_sel_hi:[1,0]
	v_pk_mul_f32 v[82:83], v[98:99], v[82:83] op_sel_hi:[1,0]
	v_pk_mul_f32 v[86:87], v[86:87], v[86:87]
	s_nop 0
	v_pk_fma_f32 v[82:83], v[82:83], v[82:83], v[86:87]
	s_nop 0
	v_pk_add_f32 v[82:83], v[82:83], v[84:85]
	s_nop 0
	v_add_f32_e32 v82, v82, v83
	ds_swizzle_b32 v83, v82 offset:swizzle(SWAP,16)
	s_waitcnt lgkmcnt(0)
	v_add_f32_e32 v82, v82, v83
	v_mov_b32_e32 v83, v82
	s_nop 1
	v_permlane32_swap_b32_e32 v82, v83
	s_and_saveexec_b64 s[62:63], s[38:39]
	v_add_f32_e32 v82, v82, v83
	ds_write_b32 v197, v82
	s_or_b64 exec, exec, s[62:63]
	ds_read_b32 v82, v213 offset:192
	s_waitcnt lgkmcnt(0)
	v_pk_mul_f32 v[84:85], v[80:81], v[82:83] op_sel_hi:[1,0]
	v_pk_mul_f32 v[86:87], v[78:79], v[82:83] op_sel_hi:[1,0]
	v_pk_mul_f32 v[84:85], v[84:85], v[84:85]
	v_pk_mul_f32 v[88:89], v[74:75], v[82:83] op_sel_hi:[1,0]
	v_pk_fma_f32 v[84:85], v[86:87], v[86:87], v[84:85]
	v_pk_mul_f32 v[86:87], v[76:77], v[82:83] op_sel_hi:[1,0]
	s_nop 0
	v_pk_mul_f32 v[86:87], v[86:87], v[86:87]
	s_nop 0
	v_pk_fma_f32 v[86:87], v[88:89], v[88:89], v[86:87]
	v_pk_mul_f32 v[88:89], v[70:71], v[82:83] op_sel_hi:[1,0]
	v_pk_add_f32 v[84:85], v[84:85], v[86:87]
	v_pk_mul_f32 v[86:87], v[72:73], v[82:83] op_sel_hi:[1,0]
	s_nop 0
	v_pk_mul_f32 v[86:87], v[86:87], v[86:87]
	s_nop 0
	v_pk_fma_f32 v[86:87], v[88:89], v[88:89], v[86:87]
	s_nop 0
	v_pk_add_f32 v[84:85], v[86:87], v[84:85]
	v_pk_mul_f32 v[86:87], v[68:69], v[82:83] op_sel_hi:[1,0]
	v_pk_mul_f32 v[82:83], v[66:67], v[82:83] op_sel_hi:[1,0]
	v_pk_mul_f32 v[86:87], v[86:87], v[86:87]
	s_nop 0
	v_pk_fma_f32 v[82:83], v[82:83], v[82:83], v[86:87]
	s_nop 0
	v_pk_add_f32 v[82:83], v[82:83], v[84:85]
	s_nop 0
	v_add_f32_e32 v82, v82, v83
	ds_swizzle_b32 v83, v82 offset:swizzle(SWAP,16)
	s_waitcnt lgkmcnt(0)
	v_add_f32_e32 v82, v82, v83
	v_mov_b32_e32 v83, v82
	s_nop 1
	v_permlane32_swap_b32_e32 v82, v83
	s_and_saveexec_b64 s[62:63], s[38:39]
	v_add_f32_e32 v82, v82, v83
	ds_write_b32 v199, v82
	s_or_b64 exec, exec, s[62:63]
	ds_read_b32 v82, v213 offset:512
	s_waitcnt lgkmcnt(0)
	v_pk_mul_f32 v[84:85], v[64:65], v[82:83] op_sel_hi:[1,0]
	v_pk_mul_f32 v[86:87], v[62:63], v[82:83] op_sel_hi:[1,0]
	v_pk_mul_f32 v[84:85], v[84:85], v[84:85]
	v_pk_mul_f32 v[88:89], v[58:59], v[82:83] op_sel_hi:[1,0]
	v_pk_fma_f32 v[84:85], v[86:87], v[86:87], v[84:85]
	v_pk_mul_f32 v[86:87], v[60:61], v[82:83] op_sel_hi:[1,0]
	s_nop 0
	v_pk_mul_f32 v[86:87], v[86:87], v[86:87]
	s_nop 0
	v_pk_fma_f32 v[86:87], v[88:89], v[88:89], v[86:87]
	v_pk_mul_f32 v[88:89], v[54:55], v[82:83] op_sel_hi:[1,0]
	v_pk_add_f32 v[84:85], v[84:85], v[86:87]
	v_pk_mul_f32 v[86:87], v[56:57], v[82:83] op_sel_hi:[1,0]
	s_nop 0
	v_pk_mul_f32 v[86:87], v[86:87], v[86:87]
	s_nop 0
	v_pk_fma_f32 v[86:87], v[88:89], v[88:89], v[86:87]
	s_nop 0
	v_pk_add_f32 v[84:85], v[86:87], v[84:85]
	v_pk_mul_f32 v[86:87], v[52:53], v[82:83] op_sel_hi:[1,0]
	v_pk_mul_f32 v[82:83], v[50:51], v[82:83] op_sel_hi:[1,0]
	v_pk_mul_f32 v[86:87], v[86:87], v[86:87]
	s_nop 0
	v_pk_fma_f32 v[82:83], v[82:83], v[82:83], v[86:87]
	s_nop 0
	v_pk_add_f32 v[82:83], v[82:83], v[84:85]
	s_nop 0
	v_add_f32_e32 v82, v82, v83
	ds_swizzle_b32 v83, v82 offset:swizzle(SWAP,16)
	s_waitcnt lgkmcnt(0)
	v_add_f32_e32 v82, v82, v83
	v_mov_b32_e32 v83, v82
	s_nop 1
	v_permlane32_swap_b32_e32 v82, v83
	s_and_saveexec_b64 s[62:63], s[38:39]
	v_add_f32_e32 v82, v82, v83
	ds_write_b32 v201, v82
	s_or_b64 exec, exec, s[62:63]
	ds_read_b32 v82, v213 offset:576
	s_waitcnt lgkmcnt(0)
	v_pk_mul_f32 v[84:85], v[48:49], v[82:83] op_sel_hi:[1,0]
	v_pk_mul_f32 v[86:87], v[46:47], v[82:83] op_sel_hi:[1,0]
	v_pk_mul_f32 v[84:85], v[84:85], v[84:85]
	v_pk_mul_f32 v[88:89], v[42:43], v[82:83] op_sel_hi:[1,0]
	v_pk_fma_f32 v[84:85], v[86:87], v[86:87], v[84:85]
	v_pk_mul_f32 v[86:87], v[44:45], v[82:83] op_sel_hi:[1,0]
	s_nop 0
	v_pk_mul_f32 v[86:87], v[86:87], v[86:87]
	s_nop 0
	v_pk_fma_f32 v[86:87], v[88:89], v[88:89], v[86:87]
	v_pk_mul_f32 v[88:89], v[38:39], v[82:83] op_sel_hi:[1,0]
	v_pk_add_f32 v[84:85], v[84:85], v[86:87]
	v_pk_mul_f32 v[86:87], v[40:41], v[82:83] op_sel_hi:[1,0]
	s_nop 0
	v_pk_mul_f32 v[86:87], v[86:87], v[86:87]
	s_nop 0
	v_pk_fma_f32 v[86:87], v[88:89], v[88:89], v[86:87]
	s_nop 0
	v_pk_add_f32 v[84:85], v[86:87], v[84:85]
	v_pk_mul_f32 v[86:87], v[36:37], v[82:83] op_sel_hi:[1,0]
	v_pk_mul_f32 v[82:83], v[34:35], v[82:83] op_sel_hi:[1,0]
	v_pk_mul_f32 v[86:87], v[86:87], v[86:87]
	s_nop 0
	v_pk_fma_f32 v[82:83], v[82:83], v[82:83], v[86:87]
	s_nop 0
	v_pk_add_f32 v[82:83], v[82:83], v[84:85]
	s_nop 0
	v_add_f32_e32 v82, v82, v83
	ds_swizzle_b32 v83, v82 offset:swizzle(SWAP,16)
	s_waitcnt lgkmcnt(0)
	v_add_f32_e32 v82, v82, v83
	v_mov_b32_e32 v83, v82
	s_nop 1
	v_permlane32_swap_b32_e32 v82, v83
	s_and_saveexec_b64 s[62:63], s[38:39]
	v_add_f32_e32 v82, v82, v83
	ds_write_b32 v203, v82
	s_or_b64 exec, exec, s[62:63]
	ds_read_b32 v82, v213 offset:640
	s_waitcnt lgkmcnt(0)
	v_pk_mul_f32 v[84:85], v[32:33], v[82:83] op_sel_hi:[1,0]
	v_pk_mul_f32 v[86:87], v[30:31], v[82:83] op_sel_hi:[1,0]
	v_pk_mul_f32 v[84:85], v[84:85], v[84:85]
	v_pk_mul_f32 v[88:89], v[26:27], v[82:83] op_sel_hi:[1,0]
	v_pk_fma_f32 v[84:85], v[86:87], v[86:87], v[84:85]
	v_pk_mul_f32 v[86:87], v[28:29], v[82:83] op_sel_hi:[1,0]
	s_nop 0
	v_pk_mul_f32 v[86:87], v[86:87], v[86:87]
	s_nop 0
	v_pk_fma_f32 v[86:87], v[88:89], v[88:89], v[86:87]
	v_pk_mul_f32 v[88:89], v[22:23], v[82:83] op_sel_hi:[1,0]
	v_pk_add_f32 v[84:85], v[84:85], v[86:87]
	v_pk_mul_f32 v[86:87], v[24:25], v[82:83] op_sel_hi:[1,0]
	s_nop 0
	v_pk_mul_f32 v[86:87], v[86:87], v[86:87]
	s_nop 0
	v_pk_fma_f32 v[86:87], v[88:89], v[88:89], v[86:87]
	s_nop 0
	v_pk_add_f32 v[84:85], v[86:87], v[84:85]
	v_pk_mul_f32 v[86:87], v[20:21], v[82:83] op_sel_hi:[1,0]
	v_pk_mul_f32 v[82:83], v[18:19], v[82:83] op_sel_hi:[1,0]
	v_pk_mul_f32 v[86:87], v[86:87], v[86:87]
	s_nop 0
	v_pk_fma_f32 v[82:83], v[82:83], v[82:83], v[86:87]
	s_nop 0
	v_pk_add_f32 v[82:83], v[82:83], v[84:85]
	s_nop 0
	v_add_f32_e32 v82, v82, v83
	ds_swizzle_b32 v83, v82 offset:swizzle(SWAP,16)
	s_waitcnt lgkmcnt(0)
	v_add_f32_e32 v82, v82, v83
	v_mov_b32_e32 v83, v82
	s_nop 1
	v_permlane32_swap_b32_e32 v82, v83
	s_and_saveexec_b64 s[62:63], s[38:39]
	v_add_f32_e32 v82, v82, v83
	ds_write_b32 v205, v82
	s_or_b64 exec, exec, s[62:63]
	ds_read_b32 v82, v213 offset:704
	s_waitcnt lgkmcnt(0)
	v_pk_mul_f32 v[84:85], v[16:17], v[82:83] op_sel_hi:[1,0]
	v_pk_mul_f32 v[86:87], v[14:15], v[82:83] op_sel_hi:[1,0]
	v_pk_mul_f32 v[84:85], v[84:85], v[84:85]
	v_pk_mul_f32 v[88:89], v[10:11], v[82:83] op_sel_hi:[1,0]
	v_pk_fma_f32 v[84:85], v[86:87], v[86:87], v[84:85]
	v_pk_mul_f32 v[86:87], v[12:13], v[82:83] op_sel_hi:[1,0]
	s_nop 0
	v_pk_mul_f32 v[86:87], v[86:87], v[86:87]
	s_nop 0
	v_pk_fma_f32 v[86:87], v[88:89], v[88:89], v[86:87]
	v_pk_mul_f32 v[88:89], v[6:7], v[82:83] op_sel_hi:[1,0]
	v_pk_add_f32 v[84:85], v[84:85], v[86:87]
	v_pk_mul_f32 v[86:87], v[8:9], v[82:83] op_sel_hi:[1,0]
	s_nop 0
	v_pk_mul_f32 v[86:87], v[86:87], v[86:87]
	s_nop 0
	v_pk_fma_f32 v[86:87], v[88:89], v[88:89], v[86:87]
	s_nop 0
	v_pk_add_f32 v[84:85], v[86:87], v[84:85]
	v_pk_mul_f32 v[86:87], v[4:5], v[82:83] op_sel_hi:[1,0]
	v_pk_mul_f32 v[82:83], v[2:3], v[82:83] op_sel_hi:[1,0]
	v_pk_mul_f32 v[86:87], v[86:87], v[86:87]
	s_nop 0
	v_pk_fma_f32 v[82:83], v[82:83], v[82:83], v[86:87]
	s_nop 0
	v_pk_add_f32 v[82:83], v[82:83], v[84:85]
	s_nop 0
	v_add_f32_e32 v82, v82, v83
	ds_swizzle_b32 v83, v82 offset:swizzle(SWAP,16)
	s_waitcnt lgkmcnt(0)
	v_add_f32_e32 v82, v82, v83
	v_mov_b32_e32 v83, v82
	s_nop 1
	v_permlane32_swap_b32_e32 v82, v83
	s_and_saveexec_b64 s[62:63], s[38:39]
	v_add_f32_e32 v82, v82, v83
	ds_write_b32 v207, v82
	s_or_b64 exec, exec, s[62:63]
	s_waitcnt lgkmcnt(0)
	s_barrier
	global_load_dwordx4 v[94:97], v[168:169], off offset:16
	global_load_dwordx4 v[90:93], v[168:169], off
	global_load_dwordx4 v[82:85], v[168:169], off offset:144
	global_load_dwordx4 v[86:89], v[168:169], off offset:128
	ds_read_b32 v158, v183
	ds_read_b32 v159, v194
	s_lshl_b32 s14, s60, 1
	s_and_b32 s14, s14, 14
	s_lshl_b32 s15, s28, 1
	s_or_b32 s14, s88, s14
	s_waitcnt lgkmcnt(0)
	v_add_f32_e32 v158, v158, v159
	v_fmamk_f32 v158, v158, 0x3c000000, v185
	v_rsq_f32_e32 v160, v158
	ds_read2_b32 v[158:159], v213 offset1:16
	s_and_b32 s15, s15, 0x7fffff0
	s_or_b32 s14, s15, s14
	s_lshl_b32 s15, s28, 2
	s_and_b32 s15, s15, 28
	s_waitcnt lgkmcnt(0)
	v_mul_f32_e32 v158, v158, v160
	v_lshlrev_b64 v[160:161], 12, v[174:175]
	v_lshl_add_u64 v[160:161], s[46:47], 0, v[160:161]
	v_pk_mul_f32 v[144:145], v[144:145], v[158:159] op_sel_hi:[1,0]
	v_pk_mul_f32 v[146:147], v[146:147], v[158:159] op_sel_hi:[1,0]
	v_pk_mul_f32 v[218:219], v[140:141], v[158:159] op_sel_hi:[1,0]
	v_lshl_add_u64 v[160:161], v[160:161], 0, v[114:115]
	v_pk_mul_f32 v[140:141], v[142:143], v[158:159] op_sel_hi:[1,0]
	s_lshl_b32 s14, s14, 5
	s_add_i32 s15, s15, s8
	s_add_i32 s28, s15, s14
	s_ashr_i32 s29, s28, 31
	s_lshl_b64 s[14:15], s[28:29], 9
	s_waitcnt vmcnt(0)
	v_pk_mul_f32 v[142:143], v[94:95], v[218:219]
	v_pk_mul_f32 v[214:215], v[92:93], v[146:147]
	v_pk_mul_f32 v[216:217], v[90:91], v[144:145]
	v_pk_fma_f32 v[218:219], v[90:91], v[144:145], 0 op_sel_hi:[1,1,0]
	v_cvt_pk_bf16_f32 v144, v216, v217
	v_cvt_pk_bf16_f32 v145, v214, v215
	v_pk_mul_f32 v[140:141], v[96:97], v[140:141]
	v_pk_fma_f32 v[220:221], v[92:93], v[146:147], 0 op_sel_hi:[1,1,0]
	v_cvt_pk_bf16_f32 v146, v142, v143
	v_cvt_pk_bf16_f32 v147, v140, v141
	ds_bpermute_b32 v232, v244, v144
	ds_bpermute_b32 v233, v244, v145
	ds_bpermute_b32 v234, v244, v146
	ds_bpermute_b32 v235, v244, v147
	ds_bpermute_b32 v236, v244, v160
	s_nop 1
	v_pk_mul_f32 v[144:145], v[136:137], v[158:159] op_sel_hi:[1,0]
	v_pk_mul_f32 v[136:137], v[138:139], v[158:159] op_sel_hi:[1,0]
	v_pk_mul_f32 v[138:139], v[86:87], v[144:145]
	v_pk_mul_f32 v[144:145], v[132:133], v[158:159] op_sel_hi:[1,0]
	v_pk_mul_f32 v[132:133], v[134:135], v[158:159] op_sel_hi:[1,0]
	v_pk_mul_f32 v[136:137], v[88:89], v[136:137]
	v_pk_mul_f32 v[132:133], v[84:85], v[132:133]
	v_pk_mul_f32 v[134:135], v[82:83], v[144:145]
	v_cvt_pk_bf16_f32 v144, v138, v139
	v_cvt_pk_bf16_f32 v145, v136, v137
	v_cvt_pk_bf16_f32 v147, v132, v133
	s_nop 0
	v_cvt_pk_bf16_f32 v146, v134, v135
	s_waitcnt lgkmcnt(0)
	v_subrev_u32_e32 v236, s82, v236
	global_store_dwordx4 v236, v[232:235], s[82:83]
	ds_bpermute_b32 v238, v244, v144
	ds_bpermute_b32 v239, v244, v145
	ds_bpermute_b32 v240, v244, v146
	ds_bpermute_b32 v241, v244, v147
	ds_bpermute_b32 v242, v244, v160
	ds_read_b32 v144, v195
	ds_read_b32 v145, v196
	v_lshlrev_b64 v[146:147], 12, v[180:181]
	v_lshl_add_u64 v[146:147], s[46:47], 0, v[146:147]
	v_lshl_add_u64 v[146:147], v[146:147], 0, v[114:115]
	s_waitcnt lgkmcnt(0)
	v_add_f32_e32 v144, v144, v145
	v_fmamk_f32 v144, v144, 0x3c000000, v185
	v_rsq_f32_e32 v144, v144
	s_nop 0
	v_mul_f32_e32 v144, v159, v144
	v_pk_mul_f32 v[128:129], v[128:129], v[144:145] op_sel_hi:[1,0]
	v_pk_mul_f32 v[130:131], v[130:131], v[144:145] op_sel_hi:[1,0]
	v_pk_mul_f32 v[160:161], v[90:91], v[128:129]
	v_pk_mul_f32 v[158:159], v[92:93], v[130:131]
	v_pk_mul_f32 v[180:181], v[124:125], v[144:145] op_sel_hi:[1,0]
	v_pk_mul_f32 v[124:125], v[126:127], v[144:145] op_sel_hi:[1,0]
	v_pk_fma_f32 v[214:215], v[90:91], v[128:129], v[218:219]
	v_cvt_pk_bf16_f32 v128, v160, v161
	v_cvt_pk_bf16_f32 v129, v158, v159
	v_pk_mul_f32 v[124:125], v[96:97], v[124:125]
	v_pk_mul_f32 v[126:127], v[94:95], v[180:181]
	v_pk_fma_f32 v[180:181], v[92:93], v[130:131], v[220:221]
	v_cvt_pk_bf16_f32 v130, v126, v127
	v_cvt_pk_bf16_f32 v131, v124, v125
	s_waitcnt lgkmcnt(0)
	v_subrev_u32_e32 v242, s82, v242
	global_store_dwordx4 v242, v[238:241], s[82:83] offset:64
	ds_bpermute_b32 v232, v244, v128
	ds_bpermute_b32 v233, v244, v129
	ds_bpermute_b32 v234, v244, v130
	ds_bpermute_b32 v235, v244, v131
	ds_bpermute_b32 v236, v244, v146
	s_nop 1
	v_pk_mul_f32 v[128:129], v[120:121], v[144:145] op_sel_hi:[1,0]
	v_pk_mul_f32 v[120:121], v[122:123], v[144:145] op_sel_hi:[1,0]
	v_pk_mul_f32 v[122:123], v[86:87], v[128:129]
	v_pk_mul_f32 v[128:129], v[116:117], v[144:145] op_sel_hi:[1,0]
	v_pk_mul_f32 v[116:117], v[118:119], v[144:145] op_sel_hi:[1,0]
	v_pk_mul_f32 v[120:121], v[88:89], v[120:121]
	v_pk_mul_f32 v[116:117], v[84:85], v[116:117]
	v_pk_mul_f32 v[118:119], v[82:83], v[128:129]
	v_cvt_pk_bf16_f32 v128, v122, v123
	v_cvt_pk_bf16_f32 v129, v120, v121
	v_cvt_pk_bf16_f32 v131, v116, v117
	s_nop 0
	v_cvt_pk_bf16_f32 v130, v118, v119
	s_waitcnt lgkmcnt(0)
	v_subrev_u32_e32 v236, s82, v236
	global_store_dwordx4 v236, v[232:235], s[82:83]
	ds_bpermute_b32 v238, v244, v128
	ds_bpermute_b32 v239, v244, v129
	ds_bpermute_b32 v240, v244, v130
	ds_bpermute_b32 v241, v244, v131
	ds_bpermute_b32 v242, v244, v146
	ds_read_b32 v128, v197
	ds_read_b32 v129, v198
	s_waitcnt lgkmcnt(0)
	v_add_f32_e32 v128, v128, v129
	v_fmamk_f32 v128, v128, 0x3c000000, v185
	v_rsq_f32_e32 v130, v128
	ds_read2_b32 v[128:129], v213 offset0:32 offset1:48
	s_waitcnt lgkmcnt(0)
	v_mul_f32_e32 v128, v128, v130
	v_lshlrev_b64 v[130:131], 12, v[178:179]
	v_pk_mul_f32 v[110:111], v[110:111], v[128:129] op_sel_hi:[1,0]
	v_lshl_add_u64 v[130:131], s[46:47], 0, v[130:131]
	v_pk_mul_f32 v[112:113], v[112:113], v[128:129] op_sel_hi:[1,0]
	v_pk_mul_f32 v[144:145], v[90:91], v[110:111]
	v_lshl_add_u64 v[130:131], v[130:131], 0, v[114:115]
	v_pk_mul_f32 v[146:147], v[92:93], v[112:113]
	v_pk_mul_f32 v[158:159], v[106:107], v[128:129] op_sel_hi:[1,0]
	v_pk_mul_f32 v[106:107], v[108:109], v[128:129] op_sel_hi:[1,0]
	v_cvt_pk_bf16_f32 v144, v144, v145
	v_cvt_pk_bf16_f32 v145, v146, v147
	v_pk_mul_f32 v[108:109], v[94:95], v[158:159]
	v_pk_mul_f32 v[106:107], v[96:97], v[106:107]
	v_cvt_pk_bf16_f32 v146, v108, v109
	v_pk_fma_f32 v[110:111], v[90:91], v[110:111], v[214:215]
	v_cvt_pk_bf16_f32 v147, v106, v107
	s_waitcnt lgkmcnt(0)
	v_subrev_u32_e32 v242, s82, v242
	global_store_dwordx4 v242, v[238:241], s[82:83] offset:64
	ds_bpermute_b32 v232, v244, v144
	ds_bpermute_b32 v233, v244, v145
	ds_bpermute_b32 v234, v244, v146
	ds_bpermute_b32 v235, v244, v147
	ds_bpermute_b32 v236, v244, v130
	v_pk_fma_f32 v[112:113], v[92:93], v[112:113], v[180:181]
	s_nop 0
	v_pk_mul_f32 v[144:145], v[102:103], v[128:129] op_sel_hi:[1,0]
	v_pk_mul_f32 v[102:103], v[104:105], v[128:129] op_sel_hi:[1,0]
	v_pk_mul_f32 v[104:105], v[86:87], v[144:145]
	v_pk_mul_f32 v[144:145], v[98:99], v[128:129] op_sel_hi:[1,0]
	v_pk_mul_f32 v[98:99], v[100:101], v[128:129] op_sel_hi:[1,0]
	v_pk_mul_f32 v[102:103], v[88:89], v[102:103]
	v_pk_mul_f32 v[98:99], v[84:85], v[98:99]
	v_pk_mul_f32 v[100:101], v[82:83], v[144:145]
	v_cvt_pk_bf16_f32 v144, v104, v105
	v_cvt_pk_bf16_f32 v145, v102, v103
	v_cvt_pk_bf16_f32 v147, v98, v99
	s_nop 0
	v_cvt_pk_bf16_f32 v146, v100, v101
	s_waitcnt lgkmcnt(0)
	v_subrev_u32_e32 v236, s82, v236
	global_store_dwordx4 v236, v[232:235], s[82:83]
	ds_bpermute_b32 v238, v244, v144
	ds_bpermute_b32 v239, v244, v145
	ds_bpermute_b32 v240, v244, v146
	ds_bpermute_b32 v241, v244, v147
	ds_bpermute_b32 v242, v244, v130
	ds_read_b32 v128, v199
	ds_read_b32 v130, v200
	s_waitcnt lgkmcnt(0)
	v_add_f32_e32 v128, v128, v130
	v_fmamk_f32 v128, v128, 0x3c000000, v185
	v_rsq_f32_e32 v128, v128
	v_lshlrev_b64 v[130:131], 12, v[176:177]
	v_lshl_add_u64 v[130:131], s[46:47], 0, v[130:131]
	v_lshl_add_u64 v[130:131], v[130:131], 0, v[114:115]
	v_mul_f32_e32 v128, v129, v128
	v_pk_mul_f32 v[144:145], v[78:79], v[128:129] op_sel_hi:[1,0]
	v_pk_mul_f32 v[80:81], v[80:81], v[128:129] op_sel_hi:[1,0]
	v_pk_mul_f32 v[74:75], v[74:75], v[128:129] op_sel_hi:[1,0]
	v_pk_mul_f32 v[76:77], v[76:77], v[128:129] op_sel_hi:[1,0]
	v_pk_mul_f32 v[146:147], v[92:93], v[80:81]
	v_pk_mul_f32 v[158:159], v[90:91], v[144:145]
	v_pk_mul_f32 v[76:77], v[96:97], v[76:77]
	v_pk_mul_f32 v[78:79], v[94:95], v[74:75]
	v_pk_fma_f32 v[160:161], v[92:93], v[80:81], v[112:113]
	v_pk_fma_f32 v[80:81], v[90:91], v[144:145], v[110:111]
	v_cvt_pk_bf16_f32 v110, v158, v159
	v_cvt_pk_bf16_f32 v111, v146, v147
	v_cvt_pk_bf16_f32 v112, v78, v79
	v_cvt_pk_bf16_f32 v113, v76, v77
	v_pk_mul_f32 v[70:71], v[70:71], v[128:129] op_sel_hi:[1,0]
	v_pk_mul_f32 v[72:73], v[72:73], v[128:129] op_sel_hi:[1,0]
	v_pk_mul_f32 v[66:67], v[66:67], v[128:129] op_sel_hi:[1,0]
	v_pk_mul_f32 v[68:69], v[68:69], v[128:129] op_sel_hi:[1,0]
	s_waitcnt lgkmcnt(0)
	v_subrev_u32_e32 v242, s82, v242
	global_store_dwordx4 v242, v[238:241], s[82:83] offset:64
	ds_bpermute_b32 v232, v244, v110
	ds_bpermute_b32 v233, v244, v111
	ds_bpermute_b32 v234, v244, v112
	ds_bpermute_b32 v235, v244, v113
	ds_bpermute_b32 v236, v244, v130
	v_pk_mul_f32 v[72:73], v[88:89], v[72:73]
	v_pk_mul_f32 v[74:75], v[86:87], v[70:71]
	v_pk_mul_f32 v[68:69], v[84:85], v[68:69]
	v_pk_mul_f32 v[70:71], v[82:83], v[66:67]
	v_cvt_pk_bf16_f32 v110, v74, v75
	v_cvt_pk_bf16_f32 v111, v72, v73
	v_cvt_pk_bf16_f32 v113, v68, v69
	v_lshl_add_u64 v[66:67], v[166:167], 0, s[14:15]
	v_cvt_pk_bf16_f32 v112, v70, v71
	s_waitcnt lgkmcnt(0)
	v_subrev_u32_e32 v236, s82, v236
	global_store_dwordx4 v236, v[232:235], s[82:83]
	ds_bpermute_b32 v238, v244, v110
	ds_bpermute_b32 v239, v244, v111
	ds_bpermute_b32 v240, v244, v112
	ds_bpermute_b32 v241, v244, v113
	ds_bpermute_b32 v242, v244, v130
	ds_swizzle_b32 v110, v80 offset:swizzle(SWAP,1)
	ds_swizzle_b32 v111, v81 offset:swizzle(SWAP,1)
	ds_swizzle_b32 v112, v160 offset:swizzle(SWAP,1)
	ds_swizzle_b32 v113, v161 offset:swizzle(SWAP,1)
	s_waitcnt lgkmcnt(2)
	v_pk_add_f32 v[80:81], v[80:81], v[110:111]
	ds_swizzle_b32 v110, v80 offset:swizzle(SWAP,2)
	s_waitcnt lgkmcnt(1)
	v_pk_add_f32 v[112:113], v[160:161], v[112:113]
	ds_swizzle_b32 v111, v81 offset:swizzle(SWAP,2)
	ds_swizzle_b32 v128, v112 offset:swizzle(SWAP,2)
	ds_swizzle_b32 v129, v113 offset:swizzle(SWAP,2)
	s_waitcnt lgkmcnt(2)
	v_pk_add_f32 v[80:81], v[80:81], v[110:111]
	ds_swizzle_b32 v110, v80 offset:swizzle(SWAP,4)
	s_waitcnt lgkmcnt(1)
	v_pk_add_f32 v[112:113], v[112:113], v[128:129]
	ds_swizzle_b32 v111, v81 offset:swizzle(SWAP,4)
	ds_swizzle_b32 v128, v112 offset:swizzle(SWAP,4)
	ds_swizzle_b32 v129, v113 offset:swizzle(SWAP,4)
	s_waitcnt lgkmcnt(2)
	v_pk_add_f32 v[80:81], v[80:81], v[110:111]
	ds_swizzle_b32 v110, v80 offset:swizzle(SWAP,8)
	s_waitcnt lgkmcnt(1)
	v_pk_add_f32 v[112:113], v[112:113], v[128:129]
	ds_swizzle_b32 v111, v81 offset:swizzle(SWAP,8)
	ds_swizzle_b32 v128, v112 offset:swizzle(SWAP,8)
	ds_swizzle_b32 v129, v113 offset:swizzle(SWAP,8)
	s_waitcnt lgkmcnt(0)
	v_subrev_u32_e32 v242, s82, v242
	global_store_dwordx4 v242, v[238:241], s[82:83] offset:64
	s_and_saveexec_b64 s[60:61], s[40:41]
	s_cbranch_execz .LBB0_196
	s_waitcnt lgkmcnt(0)
	v_pk_add_f32 v[112:113], v[112:113], v[128:129]
	v_pk_add_f32 v[110:111], v[80:81], v[110:111]
	global_store_dwordx4 v[66:67], v[110:113], off

.LBB0_202:
	s_or_b64 exec, exec, s[60:61]
	ds_read_b32 v66, v201
	ds_read_b32 v67, v202
	ds_read2_b32 v[68:69], v213 offset0:128 offset1:144
	s_mov_b64 s[14:15], 0x80000
	s_waitcnt lgkmcnt(1)
	v_add_f32_e32 v66, v66, v67
	v_fmamk_f32 v66, v66, 0x3c000000, v185
	v_rsq_f32_e32 v66, v66
	s_waitcnt lgkmcnt(0)
	v_mul_f32_e32 v68, v68, v66
	v_lshlrev_b64 v[66:67], 12, v[174:175]
	v_lshl_add_u64 v[66:67], s[46:47], 0, v[66:67]
	v_lshl_add_u64 v[66:67], v[66:67], 0, v[114:115]
	v_pk_mul_f32 v[64:65], v[64:65], v[68:69] op_sel_hi:[1,0]
	v_lshl_add_u64 v[70:71], v[66:67], 0, s[14:15]
	v_pk_mul_f32 v[62:63], v[62:63], v[68:69] op_sel_hi:[1,0]
	v_pk_mul_f32 v[72:73], v[92:93], v[64:65]
	v_pk_mul_f32 v[76:77], v[58:59], v[68:69] op_sel_hi:[1,0]
	s_mov_b32 s14, 0x80000
	v_pk_mul_f32 v[74:75], v[90:91], v[62:63]
	v_pk_mul_f32 v[58:59], v[60:61], v[68:69] op_sel_hi:[1,0]
	v_pk_mul_f32 v[60:61], v[94:95], v[76:77]
	v_pk_fma_f32 v[76:77], v[90:91], v[62:63], 0 op_sel_hi:[1,1,0]
	v_cvt_pk_bf16_f32 v63, v72, v73
	v_add_co_u32_e32 v72, vcc, s14, v66
	v_cvt_pk_bf16_f32 v62, v74, v75
	v_pk_mul_f32 v[58:59], v[96:97], v[58:59]
	s_nop 0
	v_addc_co_u32_e32 v73, vcc, 0, v67, vcc
	v_pk_fma_f32 v[78:79], v[92:93], v[64:65], 0 op_sel_hi:[1,1,0]
	v_cvt_pk_bf16_f32 v64, v60, v61
	v_cvt_pk_bf16_f32 v65, v58, v59
	ds_bpermute_b32 v232, v244, v62
	ds_bpermute_b32 v233, v244, v63
	ds_bpermute_b32 v234, v244, v64
	ds_bpermute_b32 v235, v244, v65
	ds_bpermute_b32 v236, v244, v72
	s_mov_b64 s[14:15], 0x90000
	s_nop 0
	v_pk_mul_f32 v[62:63], v[54:55], v[68:69] op_sel_hi:[1,0]
	v_pk_mul_f32 v[54:55], v[56:57], v[68:69] op_sel_hi:[1,0]
	v_pk_mul_f32 v[56:57], v[86:87], v[62:63]
	v_pk_mul_f32 v[62:63], v[50:51], v[68:69] op_sel_hi:[1,0]
	v_pk_mul_f32 v[50:51], v[52:53], v[68:69] op_sel_hi:[1,0]
	v_pk_mul_f32 v[54:55], v[88:89], v[54:55]
	v_pk_mul_f32 v[50:51], v[84:85], v[50:51]
	v_pk_mul_f32 v[52:53], v[82:83], v[62:63]
	v_cvt_pk_bf16_f32 v62, v56, v57
	v_cvt_pk_bf16_f32 v63, v54, v55
	v_cvt_pk_bf16_f32 v65, v50, v51
	s_nop 0
	v_cvt_pk_bf16_f32 v64, v52, v53
	s_waitcnt lgkmcnt(0)
	v_subrev_u32_e32 v236, s82, v236
	global_store_dwordx4 v236, v[232:235], s[82:83]
	ds_bpermute_b32 v238, v244, v62
	ds_bpermute_b32 v239, v244, v63
	ds_bpermute_b32 v240, v244, v64
	ds_bpermute_b32 v241, v244, v65
	ds_bpermute_b32 v242, v244, v70
	ds_read_b32 v62, v203
	ds_read_b32 v63, v204
	v_lshl_add_u64 v[64:65], v[66:67], 0, s[14:15]
	s_mov_b32 s14, 0x90000
	s_waitcnt lgkmcnt(0)
	v_add_f32_e32 v62, v62, v63
	v_fmamk_f32 v62, v62, 0x3c000000, v185
	v_rsq_f32_e32 v62, v62
	s_nop 0
	v_mul_f32_e32 v62, v69, v62
	v_pk_mul_f32 v[48:49], v[48:49], v[62:63] op_sel_hi:[1,0]
	v_pk_mul_f32 v[46:47], v[46:47], v[62:63] op_sel_hi:[1,0]
	v_pk_mul_f32 v[68:69], v[92:93], v[48:49]
	v_pk_mul_f32 v[70:71], v[90:91], v[46:47]
	v_pk_fma_f32 v[74:75], v[90:91], v[46:47], v[76:77]
	v_cvt_pk_bf16_f32 v47, v68, v69
	v_add_co_u32_e32 v68, vcc, s14, v66
	v_pk_mul_f32 v[72:73], v[42:43], v[62:63] op_sel_hi:[1,0]
	v_pk_mul_f32 v[42:43], v[44:45], v[62:63] op_sel_hi:[1,0]
	v_cvt_pk_bf16_f32 v46, v70, v71
	v_addc_co_u32_e32 v69, vcc, 0, v67, vcc
	v_pk_mul_f32 v[42:43], v[96:97], v[42:43]
	v_pk_mul_f32 v[44:45], v[94:95], v[72:73]
	v_pk_fma_f32 v[72:73], v[92:93], v[48:49], v[78:79]
	v_cvt_pk_bf16_f32 v48, v44, v45
	v_cvt_pk_bf16_f32 v49, v42, v43
	s_waitcnt lgkmcnt(0)
	v_subrev_u32_e32 v242, s82, v242
	global_store_dwordx4 v242, v[238:241], s[82:83] offset:64
	ds_bpermute_b32 v232, v244, v46
	ds_bpermute_b32 v233, v244, v47
	ds_bpermute_b32 v234, v244, v48
	ds_bpermute_b32 v235, v244, v49
	ds_bpermute_b32 v236, v244, v68
	s_mov_b64 s[14:15], 0xa0000
	s_nop 0
	v_pk_mul_f32 v[46:47], v[38:39], v[62:63] op_sel_hi:[1,0]
	v_pk_mul_f32 v[38:39], v[40:41], v[62:63] op_sel_hi:[1,0]
	v_pk_mul_f32 v[40:41], v[86:87], v[46:47]
	v_pk_mul_f32 v[46:47], v[34:35], v[62:63] op_sel_hi:[1,0]
	v_pk_mul_f32 v[34:35], v[36:37], v[62:63] op_sel_hi:[1,0]
	v_pk_mul_f32 v[38:39], v[88:89], v[38:39]
	v_pk_mul_f32 v[34:35], v[84:85], v[34:35]
	v_pk_mul_f32 v[36:37], v[82:83], v[46:47]
	v_cvt_pk_bf16_f32 v46, v40, v41
	v_cvt_pk_bf16_f32 v47, v38, v39
	v_cvt_pk_bf16_f32 v49, v34, v35
	s_nop 0
	v_cvt_pk_bf16_f32 v48, v36, v37
	s_waitcnt lgkmcnt(0)
	v_subrev_u32_e32 v236, s82, v236
	global_store_dwordx4 v236, v[232:235], s[82:83]
	ds_bpermute_b32 v238, v244, v46
	ds_bpermute_b32 v239, v244, v47
	ds_bpermute_b32 v240, v244, v48
	ds_bpermute_b32 v241, v244, v49
	ds_bpermute_b32 v242, v244, v64
	ds_read_b32 v46, v205
	ds_read_b32 v47, v206
	s_waitcnt lgkmcnt(0)
	v_add_f32_e32 v46, v46, v47
	v_fmamk_f32 v46, v46, 0x3c000000, v185
	v_rsq_f32_e32 v48, v46
	ds_read2_b32 v[46:47], v213 offset0:160 offset1:176
	s_waitcnt lgkmcnt(0)
	v_mul_f32_e32 v46, v46, v48
	v_lshl_add_u64 v[48:49], v[66:67], 0, s[14:15]
	v_pk_mul_f32 v[30:31], v[30:31], v[46:47] op_sel_hi:[1,0]
	v_pk_mul_f32 v[68:69], v[26:27], v[46:47] op_sel_hi:[1,0]
	s_mov_b32 s14, 0xa0000
	v_pk_mul_f32 v[32:33], v[32:33], v[46:47] op_sel_hi:[1,0]
	v_pk_mul_f32 v[62:63], v[90:91], v[30:31]
	v_pk_mul_f32 v[26:27], v[28:29], v[46:47] op_sel_hi:[1,0]
	v_pk_mul_f32 v[28:29], v[94:95], v[68:69]
	v_add_co_u32_e32 v68, vcc, s14, v66
	v_pk_mul_f32 v[64:65], v[92:93], v[32:33]
	v_cvt_pk_bf16_f32 v62, v62, v63
	s_nop 0
	v_addc_co_u32_e32 v69, vcc, 0, v67, vcc
	v_cvt_pk_bf16_f32 v63, v64, v65
	v_pk_mul_f32 v[26:27], v[96:97], v[26:27]
	v_cvt_pk_bf16_f32 v64, v28, v29
	s_mov_b64 s[14:15], 0xb0000
	v_cvt_pk_bf16_f32 v65, v26, v27
	s_waitcnt lgkmcnt(0)
	v_subrev_u32_e32 v242, s82, v242
	global_store_dwordx4 v242, v[238:241], s[82:83] offset:64
	ds_bpermute_b32 v232, v244, v62
	ds_bpermute_b32 v233, v244, v63
	ds_bpermute_b32 v234, v244, v64
	ds_bpermute_b32 v235, v244, v65
	ds_bpermute_b32 v236, v244, v68
	v_pk_fma_f32 v[30:31], v[90:91], v[30:31], v[74:75]
	v_pk_fma_f32 v[32:33], v[92:93], v[32:33], v[72:73]
	v_pk_mul_f32 v[62:63], v[22:23], v[46:47] op_sel_hi:[1,0]
	v_pk_mul_f32 v[22:23], v[24:25], v[46:47] op_sel_hi:[1,0]
	v_pk_mul_f32 v[24:25], v[86:87], v[62:63]
	v_pk_mul_f32 v[62:63], v[18:19], v[46:47] op_sel_hi:[1,0]
	v_pk_mul_f32 v[18:19], v[20:21], v[46:47] op_sel_hi:[1,0]
	v_pk_mul_f32 v[22:23], v[88:89], v[22:23]
	v_pk_mul_f32 v[18:19], v[84:85], v[18:19]
	v_pk_mul_f32 v[20:21], v[82:83], v[62:63]
	v_cvt_pk_bf16_f32 v62, v24, v25
	v_cvt_pk_bf16_f32 v63, v22, v23
	v_cvt_pk_bf16_f32 v65, v18, v19
	s_nop 0
	v_cvt_pk_bf16_f32 v64, v20, v21
	s_waitcnt lgkmcnt(0)
	v_subrev_u32_e32 v236, s82, v236
	global_store_dwordx4 v236, v[232:235], s[82:83]
	ds_bpermute_b32 v238, v244, v62
	ds_bpermute_b32 v239, v244, v63
	ds_bpermute_b32 v240, v244, v64
	ds_bpermute_b32 v241, v244, v65
	ds_bpermute_b32 v242, v244, v48
	ds_read_b32 v46, v207
	ds_read_b32 v48, v208
	s_waitcnt lgkmcnt(0)
	v_add_f32_e32 v46, v46, v48
	v_fmamk_f32 v46, v46, 0x3c000000, v185
	v_rsq_f32_e32 v46, v46
	v_lshl_add_u64 v[48:49], v[66:67], 0, s[14:15]
	s_mov_b32 s14, 0xb0000
	v_mul_f32_e32 v46, v47, v46
	v_pk_mul_f32 v[10:11], v[10:11], v[46:47] op_sel_hi:[1,0]
	v_pk_mul_f32 v[62:63], v[14:15], v[46:47] op_sel_hi:[1,0]
	v_pk_mul_f32 v[16:17], v[16:17], v[46:47] op_sel_hi:[1,0]
	v_pk_mul_f32 v[12:13], v[12:13], v[46:47] op_sel_hi:[1,0]
	v_pk_mul_f32 v[14:15], v[94:95], v[10:11]
	v_add_co_u32_e32 v10, vcc, s14, v66
	v_pk_mul_f32 v[64:65], v[92:93], v[16:17]
	v_pk_mul_f32 v[68:69], v[90:91], v[62:63]
	v_pk_mul_f32 v[12:13], v[96:97], v[12:13]
	v_pk_fma_f32 v[70:71], v[92:93], v[16:17], v[32:33]
	v_pk_fma_f32 v[16:17], v[90:91], v[62:63], v[30:31]
	v_cvt_pk_bf16_f32 v30, v68, v69
	v_cvt_pk_bf16_f32 v31, v64, v65
	v_cvt_pk_bf16_f32 v32, v14, v15
	v_cvt_pk_bf16_f32 v33, v12, v13
	v_addc_co_u32_e32 v11, vcc, 0, v67, vcc
	v_pk_mul_f32 v[6:7], v[6:7], v[46:47] op_sel_hi:[1,0]
	v_pk_mul_f32 v[8:9], v[8:9], v[46:47] op_sel_hi:[1,0]
	v_pk_mul_f32 v[2:3], v[2:3], v[46:47] op_sel_hi:[1,0]
	v_pk_mul_f32 v[4:5], v[4:5], v[46:47] op_sel_hi:[1,0]
	s_waitcnt lgkmcnt(0)
	v_subrev_u32_e32 v242, s82, v242
	global_store_dwordx4 v242, v[238:241], s[82:83] offset:64
	ds_bpermute_b32 v232, v244, v30
	ds_bpermute_b32 v233, v244, v31
	ds_bpermute_b32 v234, v244, v32
	ds_bpermute_b32 v235, v244, v33
	ds_bpermute_b32 v236, v244, v10
	v_pk_mul_f32 v[8:9], v[88:89], v[8:9]
	v_pk_mul_f32 v[10:11], v[86:87], v[6:7]
	v_pk_mul_f32 v[4:5], v[84:85], v[4:5]
	v_pk_mul_f32 v[6:7], v[82:83], v[2:3]
	v_cvt_pk_bf16_f32 v30, v10, v11
	v_cvt_pk_bf16_f32 v31, v8, v9
	v_cvt_pk_bf16_f32 v33, v4, v5
	s_add_i32 s14, s28, 2
	v_cvt_pk_bf16_f32 v32, v6, v7
	s_waitcnt lgkmcnt(0)
	v_subrev_u32_e32 v236, s82, v236
	global_store_dwordx4 v236, v[232:235], s[82:83]
	ds_bpermute_b32 v238, v244, v30
	ds_bpermute_b32 v239, v244, v31
	ds_bpermute_b32 v240, v244, v32
	ds_bpermute_b32 v241, v244, v33
	ds_bpermute_b32 v242, v244, v48
	ds_swizzle_b32 v30, v16 offset:swizzle(SWAP,1)
	ds_swizzle_b32 v31, v17 offset:swizzle(SWAP,1)
	ds_swizzle_b32 v32, v70 offset:swizzle(SWAP,1)
	ds_swizzle_b32 v33, v71 offset:swizzle(SWAP,1)
	s_ashr_i32 s15, s14, 31
	s_lshl_b64 s[14:15], s[14:15], 9
	s_waitcnt lgkmcnt(2)
	v_pk_add_f32 v[16:17], v[16:17], v[30:31]
	ds_swizzle_b32 v30, v16 offset:swizzle(SWAP,2)
	s_waitcnt lgkmcnt(1)
	v_pk_add_f32 v[32:33], v[70:71], v[32:33]
	ds_swizzle_b32 v31, v17 offset:swizzle(SWAP,2)
	ds_swizzle_b32 v46, v32 offset:swizzle(SWAP,2)
	ds_swizzle_b32 v47, v33 offset:swizzle(SWAP,2)
	v_lshl_add_u64 v[2:3], v[166:167], 0, s[14:15]
	s_waitcnt lgkmcnt(2)
	v_pk_add_f32 v[16:17], v[16:17], v[30:31]
	ds_swizzle_b32 v30, v16 offset:swizzle(SWAP,4)
	s_waitcnt lgkmcnt(1)
	v_pk_add_f32 v[32:33], v[32:33], v[46:47]
	ds_swizzle_b32 v31, v17 offset:swizzle(SWAP,4)
	ds_swizzle_b32 v46, v32 offset:swizzle(SWAP,4)
	ds_swizzle_b32 v47, v33 offset:swizzle(SWAP,4)
	s_waitcnt lgkmcnt(2)
	v_pk_add_f32 v[16:17], v[16:17], v[30:31]
	ds_swizzle_b32 v30, v16 offset:swizzle(SWAP,8)
	s_waitcnt lgkmcnt(1)
	v_pk_add_f32 v[32:33], v[32:33], v[46:47]
	ds_swizzle_b32 v31, v17 offset:swizzle(SWAP,8)
	ds_swizzle_b32 v46, v32 offset:swizzle(SWAP,8)
	ds_swizzle_b32 v47, v33 offset:swizzle(SWAP,8)
	s_waitcnt lgkmcnt(0)
	v_subrev_u32_e32 v242, s82, v242
	global_store_dwordx4 v242, v[238:241], s[82:83] offset:64
	s_and_saveexec_b64 s[28:29], s[40:41]
	s_cbranch_execz .LBB0_204
	s_waitcnt lgkmcnt(0)
	v_pk_add_f32 v[32:33], v[32:33], v[46:47]
	v_pk_add_f32 v[30:31], v[16:17], v[30:31]
	global_store_dwordx4 v[2:3], v[30:33], off

.LBB0_352:
	s_ashr_i32 s59, s58, 31
	s_lshl_b64 s[14:15], s[58:59], 25
	s_add_u32 s14, s37, s14
	s_addc_u32 s15, s64, s15
	v_lshlrev_b32_e32 v114, 1, v177
	v_ashrrev_i32_e32 v153, 31, v152
	v_lshl_add_u64 v[132:133], s[14:15], 0, v[114:115]
	v_lshlrev_b64 v[136:137], 12, v[152:153]
	v_mov_b32_e32 v155, v154
	v_lshl_add_u64 v[136:137], v[132:133], 0, v[136:137]
	v_cvt_pk_bf16_f32 v166, v166, v167
	v_cvt_pk_bf16_f32 v167, v134, v135
	v_cvt_pk_bf16_f32 v168, v168, v169
	v_cvt_pk_bf16_f32 v169, v138, v139
	v_mov_b32_e32 v158, v154
	v_mov_b32_e32 v159, v154
	v_cndmask_b32_e64 v114, 0, 1, s[56:57]
	ds_bpermute_b32 v232, v244, v166
	ds_bpermute_b32 v233, v244, v167
	ds_bpermute_b32 v234, v244, v168
	ds_bpermute_b32 v235, v244, v169
	ds_bpermute_b32 v236, v244, v136
	v_pk_mul_f32 v[138:139], v[122:123], v[158:159]
	v_pk_mul_f32 v[134:135], v[120:121], v[154:155]
	v_pk_mul_f32 v[166:167], v[118:119], v[158:159]
	v_cmp_ne_u32_e64 s[40:41], 1, v114
	s_andn2_b64 vcc, exec, s[56:57]
	v_pk_mul_f32 v[168:169], v[116:117], v[154:155]
	s_waitcnt lgkmcnt(0)
	v_subrev_u32_e32 v236, s82, v236
	global_store_dwordx4 v236, v[232:235], s[82:83]
	s_cbranch_vccnz .LBB0_354
	v_max_f32_e32 v114, v134, v134
	v_max_f32_e32 v134, 0xc2a00000, v114
	v_max_f32_e32 v114, v168, v168
	v_max_f32_e32 v158, 0xc2a00000, v114
	v_mul_f32_e32 v114, 0xbfb8aa3b, v134
	v_exp_f32_e32 v114, v114
	v_mul_f32_e32 v155, 0xbfb8aa3b, v158
	v_exp_f32_e32 v155, v155
	v_max_f32_e32 v135, v135, v135
	v_add_f32_e32 v114, 1.0, v114
	v_rcp_f32_e32 v160, v114
	v_add_f32_e32 v114, 1.0, v155
	v_max_f32_e32 v135, 0xc2a00000, v135
	v_max_f32_e32 v155, v169, v169
	v_max_f32_e32 v159, 0xc2a00000, v155
	v_mul_f32_e32 v155, 0xbfb8aa3b, v135
	v_exp_f32_e32 v155, v155
	v_mul_f32_e32 v161, 0xbfb8aa3b, v159
	v_exp_f32_e32 v169, v161
	v_max_f32_e32 v138, v138, v138
	v_rcp_f32_e32 v168, v114
	v_add_f32_e32 v114, 1.0, v155
	v_max_f32_e32 v138, 0xc2a00000, v138
	v_max_f32_e32 v155, v166, v166
	v_max_f32_e32 v166, 0xc2a00000, v155
	v_mul_f32_e32 v155, 0xbfb8aa3b, v138
	v_exp_f32_e32 v155, v155
	v_rcp_f32_e32 v161, v114
	v_add_f32_e32 v114, 1.0, v169
	v_mul_f32_e32 v169, 0xbfb8aa3b, v166
	v_exp_f32_e32 v171, v169
	v_max_f32_e32 v139, v139, v139
	v_rcp_f32_e32 v169, v114
	v_add_f32_e32 v114, 1.0, v155
	v_max_f32_e32 v139, 0xc2a00000, v139
	v_max_f32_e32 v155, v167, v167
	v_max_f32_e32 v167, 0xc2a00000, v155
	v_mul_f32_e32 v155, 0xbfb8aa3b, v139
	v_rcp_f32_e32 v170, v114
	v_add_f32_e32 v114, 1.0, v171
	v_exp_f32_e32 v155, v155
	v_mul_f32_e32 v171, 0xbfb8aa3b, v167
	v_exp_f32_e32 v179, v171
	v_rcp_f32_e32 v178, v114
	v_add_f32_e32 v114, 1.0, v155
	v_rcp_f32_e32 v171, v114
	v_add_f32_e32 v114, 1.0, v179
	v_rcp_f32_e32 v179, v114
	v_pk_mul_f32 v[134:135], v[134:135], v[160:161]
	v_pk_mul_f32 v[138:139], v[138:139], v[170:171]
	v_pk_mul_f32 v[168:169], v[158:159], v[168:169]
	v_pk_mul_f32 v[166:167], v[166:167], v[178:179]
.LBB0_354:
	v_cvt_pk_bf16_f32 v178, v134, v135
	ds_read_b32 v134, v176 offset:64
	v_cvt_pk_bf16_f32 v179, v138, v139
	v_cvt_pk_bf16_f32 v180, v168, v169
	v_cvt_pk_bf16_f32 v181, v166, v167
	s_and_b64 vcc, exec, s[40:41]
	s_waitcnt lgkmcnt(0)
	v_pk_mul_f32 v[138:139], v[112:113], v[134:135] op_sel_hi:[1,0]
	v_pk_mul_f32 v[168:169], v[110:111], v[134:135] op_sel_hi:[1,0]
	v_pk_mul_f32 v[166:167], v[108:109], v[134:135] op_sel_hi:[1,0]
	v_pk_mul_f32 v[170:171], v[106:107], v[134:135] op_sel_hi:[1,0]
	ds_bpermute_b32 v238, v244, v178
	ds_bpermute_b32 v239, v244, v179
	ds_bpermute_b32 v240, v244, v180
	ds_bpermute_b32 v241, v244, v181
	ds_bpermute_b32 v242, v244, v136
	s_waitcnt lgkmcnt(0)
	v_subrev_u32_e32 v242, s82, v242
	global_store_dwordx4 v242, v[238:241], s[82:83] offset:64
	s_cbranch_vccnz .LBB0_356
	v_max_f32_e32 v114, v168, v168
	v_max_f32_e32 v136, 0xc2a00000, v114
	v_max_f32_e32 v114, v170, v170
	v_max_f32_e32 v158, 0xc2a00000, v114
	v_mul_f32_e32 v114, 0xbfb8aa3b, v136
	v_exp_f32_e32 v114, v114
	v_mul_f32_e32 v135, 0xbfb8aa3b, v158
	v_exp_f32_e32 v135, v135
	v_add_f32_e32 v114, 1.0, v114
	v_rcp_f32_e32 v160, v114
	v_add_f32_e32 v114, 1.0, v135
	v_max_f32_e32 v135, v169, v169
	v_max_f32_e32 v137, 0xc2a00000, v135
	v_max_f32_e32 v135, v171, v171
	v_max_f32_e32 v159, 0xc2a00000, v135
	v_mul_f32_e32 v135, 0xbfb8aa3b, v137
	v_exp_f32_e32 v135, v135
	v_mul_f32_e32 v155, 0xbfb8aa3b, v159
	v_rcp_f32_e32 v170, v114
	v_exp_f32_e32 v155, v155
	v_add_f32_e32 v114, 1.0, v135
	v_max_f32_e32 v135, v138, v138
	v_max_f32_e32 v138, 0xc2a00000, v135
	v_max_f32_e32 v135, v166, v166
	v_max_f32_e32 v166, 0xc2a00000, v135
	v_mul_f32_e32 v135, 0xbfb8aa3b, v138
	v_exp_f32_e32 v135, v135
	v_rcp_f32_e32 v161, v114
	v_add_f32_e32 v114, 1.0, v155
	v_mul_f32_e32 v155, 0xbfb8aa3b, v166
	v_exp_f32_e32 v155, v155
	v_rcp_f32_e32 v171, v114
	v_add_f32_e32 v114, 1.0, v135
	v_max_f32_e32 v135, v139, v139
	v_max_f32_e32 v139, 0xc2a00000, v135
	v_max_f32_e32 v135, v167, v167
	v_max_f32_e32 v167, 0xc2a00000, v135
	v_mul_f32_e32 v135, 0xbfb8aa3b, v139
	v_rcp_f32_e32 v178, v114
	v_add_f32_e32 v114, 1.0, v155
	v_exp_f32_e32 v135, v135
	v_mul_f32_e32 v155, 0xbfb8aa3b, v167
	v_exp_f32_e32 v155, v155
	v_rcp_f32_e32 v180, v114
	v_add_f32_e32 v114, 1.0, v135
	v_rcp_f32_e32 v179, v114
	v_add_f32_e32 v114, 1.0, v155
	v_rcp_f32_e32 v181, v114
	v_pk_mul_f32 v[168:169], v[136:137], v[160:161]
	v_pk_mul_f32 v[138:139], v[138:139], v[178:179]
	v_pk_mul_f32 v[170:171], v[158:159], v[170:171]
	v_pk_mul_f32 v[166:167], v[166:167], v[180:181]
.LBB0_356:
	v_or_b32_e32 v136, 16, v152
	v_ashrrev_i32_e32 v137, 31, v136
	v_lshlrev_b64 v[136:137], 12, v[136:137]
	v_mov_b32_e32 v135, v134
	v_lshl_add_u64 v[136:137], v[132:133], 0, v[136:137]
	v_cvt_pk_bf16_f32 v168, v168, v169
	v_cvt_pk_bf16_f32 v169, v138, v139
	v_cvt_pk_bf16_f32 v170, v170, v171
	v_cvt_pk_bf16_f32 v171, v166, v167
	v_mov_b32_e32 v158, v134
	v_mov_b32_e32 v159, v134
	ds_bpermute_b32 v232, v244, v168
	ds_bpermute_b32 v233, v244, v169
	ds_bpermute_b32 v234, v244, v170
	ds_bpermute_b32 v235, v244, v171
	ds_bpermute_b32 v236, v244, v136
	v_pk_mul_f32 v[138:139], v[104:105], v[158:159]
	v_pk_mul_f32 v[166:167], v[100:101], v[158:159]
	v_pk_mul_f32 v[168:169], v[102:103], v[134:135]
	s_and_b64 vcc, exec, s[40:41]
	v_pk_mul_f32 v[170:171], v[98:99], v[134:135]
	s_waitcnt lgkmcnt(0)
	v_subrev_u32_e32 v236, s82, v236
	global_store_dwordx4 v236, v[232:235], s[82:83]
	s_cbranch_vccnz .LBB0_358
	v_max_f32_e32 v114, v168, v168
	v_max_f32_e32 v134, 0xc2a00000, v114
	v_max_f32_e32 v114, v170, v170
	v_max_f32_e32 v158, 0xc2a00000, v114
	v_mul_f32_e32 v114, 0xbfb8aa3b, v134
	v_exp_f32_e32 v114, v114
	v_mul_f32_e32 v135, 0xbfb8aa3b, v158
	v_exp_f32_e32 v135, v135
	v_max_f32_e32 v155, v171, v171
	v_add_f32_e32 v114, 1.0, v114
	v_rcp_f32_e32 v160, v114
	v_add_f32_e32 v114, 1.0, v135
	v_max_f32_e32 v135, v169, v169
	v_max_f32_e32 v135, 0xc2a00000, v135
	v_max_f32_e32 v159, 0xc2a00000, v155
	v_mul_f32_e32 v155, 0xbfb8aa3b, v135
	v_exp_f32_e32 v155, v155
	v_mul_f32_e32 v161, 0xbfb8aa3b, v159
	v_exp_f32_e32 v168, v161
	v_max_f32_e32 v138, v138, v138
	v_rcp_f32_e32 v170, v114
	v_add_f32_e32 v114, 1.0, v155
	v_max_f32_e32 v138, 0xc2a00000, v138
	v_max_f32_e32 v155, v166, v166
	v_max_f32_e32 v166, 0xc2a00000, v155
	v_mul_f32_e32 v155, 0xbfb8aa3b, v138
	v_exp_f32_e32 v155, v155
	v_rcp_f32_e32 v161, v114
	v_add_f32_e32 v114, 1.0, v168
	v_mul_f32_e32 v168, 0xbfb8aa3b, v166
	v_exp_f32_e32 v168, v168
	v_max_f32_e32 v139, v139, v139
	v_rcp_f32_e32 v171, v114
	v_add_f32_e32 v114, 1.0, v155
	v_max_f32_e32 v139, 0xc2a00000, v139
	v_max_f32_e32 v155, v167, v167
	v_max_f32_e32 v167, 0xc2a00000, v155
	v_mul_f32_e32 v155, 0xbfb8aa3b, v139
	v_rcp_f32_e32 v178, v114
	v_add_f32_e32 v114, 1.0, v168
	v_exp_f32_e32 v155, v155
	v_mul_f32_e32 v168, 0xbfb8aa3b, v167
	v_exp_f32_e32 v168, v168
	v_rcp_f32_e32 v180, v114
	v_add_f32_e32 v114, 1.0, v155
	v_rcp_f32_e32 v179, v114
	v_add_f32_e32 v114, 1.0, v168
	v_rcp_f32_e32 v181, v114
	v_pk_mul_f32 v[168:169], v[134:135], v[160:161]
	v_pk_mul_f32 v[138:139], v[138:139], v[178:179]
	v_pk_mul_f32 v[170:171], v[158:159], v[170:171]
	v_pk_mul_f32 v[166:167], v[166:167], v[180:181]
.LBB0_358:
	ds_read_b32 v134, v176 offset:128
	v_cvt_pk_bf16_f32 v168, v168, v169
	v_cvt_pk_bf16_f32 v169, v138, v139
	v_cvt_pk_bf16_f32 v170, v170, v171
	v_cvt_pk_bf16_f32 v171, v166, v167
	ds_bpermute_b32 v238, v244, v168
	ds_bpermute_b32 v239, v244, v169
	ds_bpermute_b32 v240, v244, v170
	ds_bpermute_b32 v241, v244, v171
	ds_bpermute_b32 v242, v244, v136
	s_waitcnt lgkmcnt(0)
	v_pk_mul_f32 v[138:139], v[96:97], v[134:135] op_sel_hi:[1,0]
	v_pk_mul_f32 v[166:167], v[92:93], v[134:135] op_sel_hi:[1,0]
	v_pk_mul_f32 v[168:169], v[94:95], v[134:135] op_sel_hi:[1,0]
	s_and_b64 vcc, exec, s[40:41]
	v_pk_mul_f32 v[170:171], v[90:91], v[134:135] op_sel_hi:[1,0]
	s_waitcnt lgkmcnt(0)
	v_subrev_u32_e32 v242, s82, v242
	global_store_dwordx4 v242, v[238:241], s[82:83] offset:64
	s_cbranch_vccnz .LBB0_360
	v_max_f32_e32 v114, v168, v168
	v_max_f32_e32 v136, 0xc2a00000, v114
	v_max_f32_e32 v114, v170, v170
	v_max_f32_e32 v158, 0xc2a00000, v114
	v_mul_f32_e32 v114, 0xbfb8aa3b, v136
	v_exp_f32_e32 v114, v114
	v_mul_f32_e32 v135, 0xbfb8aa3b, v158
	v_exp_f32_e32 v135, v135
	v_add_f32_e32 v114, 1.0, v114
	v_rcp_f32_e32 v160, v114
	v_add_f32_e32 v114, 1.0, v135
	v_max_f32_e32 v135, v169, v169
	v_max_f32_e32 v137, 0xc2a00000, v135
	v_max_f32_e32 v135, v171, v171
	v_max_f32_e32 v159, 0xc2a00000, v135
	v_mul_f32_e32 v135, 0xbfb8aa3b, v137
	v_exp_f32_e32 v135, v135
	v_mul_f32_e32 v155, 0xbfb8aa3b, v159
	v_rcp_f32_e32 v170, v114
	v_exp_f32_e32 v155, v155
	v_add_f32_e32 v114, 1.0, v135
	v_max_f32_e32 v135, v138, v138
	v_max_f32_e32 v138, 0xc2a00000, v135
	v_max_f32_e32 v135, v166, v166
	v_max_f32_e32 v166, 0xc2a00000, v135
	v_mul_f32_e32 v135, 0xbfb8aa3b, v138
	v_exp_f32_e32 v135, v135
	v_rcp_f32_e32 v161, v114
	v_add_f32_e32 v114, 1.0, v155
	v_mul_f32_e32 v155, 0xbfb8aa3b, v166
	v_exp_f32_e32 v155, v155
	v_rcp_f32_e32 v171, v114
	v_add_f32_e32 v114, 1.0, v135
	v_max_f32_e32 v135, v139, v139
	v_max_f32_e32 v139, 0xc2a00000, v135
	v_max_f32_e32 v135, v167, v167
	v_max_f32_e32 v167, 0xc2a00000, v135
	v_mul_f32_e32 v135, 0xbfb8aa3b, v139
	v_rcp_f32_e32 v178, v114
	v_add_f32_e32 v114, 1.0, v155
	v_exp_f32_e32 v135, v135
	v_mul_f32_e32 v155, 0xbfb8aa3b, v167
	v_exp_f32_e32 v155, v155
	v_rcp_f32_e32 v180, v114
	v_add_f32_e32 v114, 1.0, v135
	v_rcp_f32_e32 v179, v114
	v_add_f32_e32 v114, 1.0, v155
	v_rcp_f32_e32 v181, v114
	v_pk_mul_f32 v[168:169], v[136:137], v[160:161]
	v_pk_mul_f32 v[138:139], v[138:139], v[178:179]
	v_pk_mul_f32 v[170:171], v[158:159], v[170:171]
	v_pk_mul_f32 v[166:167], v[166:167], v[180:181]
.LBB0_360:
	v_or_b32_e32 v136, 32, v152
	v_ashrrev_i32_e32 v137, 31, v136
	v_lshlrev_b64 v[136:137], 12, v[136:137]
	v_mov_b32_e32 v135, v134
	v_lshl_add_u64 v[136:137], v[132:133], 0, v[136:137]
	v_cvt_pk_bf16_f32 v168, v168, v169
	v_cvt_pk_bf16_f32 v169, v138, v139
	v_cvt_pk_bf16_f32 v170, v170, v171
	v_cvt_pk_bf16_f32 v171, v166, v167
	v_mov_b32_e32 v158, v134
	v_mov_b32_e32 v159, v134
	ds_bpermute_b32 v232, v244, v168
	ds_bpermute_b32 v233, v244, v169
	ds_bpermute_b32 v234, v244, v170
	ds_bpermute_b32 v235, v244, v171
	ds_bpermute_b32 v236, v244, v136
	v_pk_mul_f32 v[138:139], v[88:89], v[158:159]
	v_pk_mul_f32 v[166:167], v[84:85], v[158:159]
	v_pk_mul_f32 v[168:169], v[86:87], v[134:135]
	s_and_b64 vcc, exec, s[40:41]
	v_pk_mul_f32 v[170:171], v[82:83], v[134:135]
	s_waitcnt lgkmcnt(0)
	v_subrev_u32_e32 v236, s82, v236
	global_store_dwordx4 v236, v[232:235], s[82:83]
	s_cbranch_vccnz .LBB0_362
	v_max_f32_e32 v114, v168, v168
	v_max_f32_e32 v134, 0xc2a00000, v114
	v_max_f32_e32 v114, v170, v170
	v_max_f32_e32 v158, 0xc2a00000, v114
	v_mul_f32_e32 v114, 0xbfb8aa3b, v134
	v_exp_f32_e32 v114, v114
	v_mul_f32_e32 v135, 0xbfb8aa3b, v158
	v_exp_f32_e32 v135, v135
	v_max_f32_e32 v155, v171, v171
	v_add_f32_e32 v114, 1.0, v114
	v_rcp_f32_e32 v160, v114
	v_add_f32_e32 v114, 1.0, v135
	v_max_f32_e32 v135, v169, v169
	v_max_f32_e32 v135, 0xc2a00000, v135
	v_max_f32_e32 v159, 0xc2a00000, v155
	v_mul_f32_e32 v155, 0xbfb8aa3b, v135
	v_exp_f32_e32 v155, v155
	v_mul_f32_e32 v161, 0xbfb8aa3b, v159
	v_exp_f32_e32 v168, v161
	v_max_f32_e32 v138, v138, v138
	v_rcp_f32_e32 v170, v114
	v_add_f32_e32 v114, 1.0, v155
	v_max_f32_e32 v138, 0xc2a00000, v138
	v_max_f32_e32 v155, v166, v166
	v_max_f32_e32 v166, 0xc2a00000, v155
	v_mul_f32_e32 v155, 0xbfb8aa3b, v138
	v_exp_f32_e32 v155, v155
	v_rcp_f32_e32 v161, v114
	v_add_f32_e32 v114, 1.0, v168
	v_mul_f32_e32 v168, 0xbfb8aa3b, v166
	v_exp_f32_e32 v168, v168
	v_max_f32_e32 v139, v139, v139
	v_rcp_f32_e32 v171, v114
	v_add_f32_e32 v114, 1.0, v155
	v_max_f32_e32 v139, 0xc2a00000, v139
	v_max_f32_e32 v155, v167, v167
	v_max_f32_e32 v167, 0xc2a00000, v155
	v_mul_f32_e32 v155, 0xbfb8aa3b, v139
	v_rcp_f32_e32 v178, v114
	v_add_f32_e32 v114, 1.0, v168
	v_exp_f32_e32 v155, v155
	v_mul_f32_e32 v168, 0xbfb8aa3b, v167
	v_exp_f32_e32 v168, v168
	v_rcp_f32_e32 v180, v114
	v_add_f32_e32 v114, 1.0, v155
	v_rcp_f32_e32 v179, v114
	v_add_f32_e32 v114, 1.0, v168
	v_rcp_f32_e32 v181, v114
	v_pk_mul_f32 v[168:169], v[134:135], v[160:161]
	v_pk_mul_f32 v[138:139], v[138:139], v[178:179]
	v_pk_mul_f32 v[170:171], v[158:159], v[170:171]
	v_pk_mul_f32 v[166:167], v[166:167], v[180:181]
.LBB0_362:
	ds_read_b32 v134, v176 offset:192
	v_cvt_pk_bf16_f32 v168, v168, v169
	v_cvt_pk_bf16_f32 v169, v138, v139
	v_cvt_pk_bf16_f32 v170, v170, v171
	v_cvt_pk_bf16_f32 v171, v166, v167
	ds_bpermute_b32 v238, v244, v168
	ds_bpermute_b32 v239, v244, v169
	ds_bpermute_b32 v240, v244, v170
	ds_bpermute_b32 v241, v244, v171
	ds_bpermute_b32 v242, v244, v136
	s_waitcnt lgkmcnt(0)
	v_pk_mul_f32 v[138:139], v[80:81], v[134:135] op_sel_hi:[1,0]
	v_pk_mul_f32 v[166:167], v[76:77], v[134:135] op_sel_hi:[1,0]
	v_pk_mul_f32 v[168:169], v[78:79], v[134:135] op_sel_hi:[1,0]
	s_and_b64 vcc, exec, s[40:41]
	v_pk_mul_f32 v[170:171], v[74:75], v[134:135] op_sel_hi:[1,0]
	s_waitcnt lgkmcnt(0)
	v_subrev_u32_e32 v242, s82, v242
	global_store_dwordx4 v242, v[238:241], s[82:83] offset:64
	s_cbranch_vccnz .LBB0_364
	v_max_f32_e32 v114, v168, v168
	v_max_f32_e32 v136, 0xc2a00000, v114
	v_max_f32_e32 v114, v170, v170
	v_max_f32_e32 v158, 0xc2a00000, v114
	v_mul_f32_e32 v114, 0xbfb8aa3b, v136
	v_exp_f32_e32 v114, v114
	v_mul_f32_e32 v135, 0xbfb8aa3b, v158
	v_exp_f32_e32 v135, v135
	v_add_f32_e32 v114, 1.0, v114
	v_rcp_f32_e32 v160, v114
	v_add_f32_e32 v114, 1.0, v135
	v_max_f32_e32 v135, v169, v169
	v_max_f32_e32 v137, 0xc2a00000, v135
	v_max_f32_e32 v135, v171, v171
	v_max_f32_e32 v159, 0xc2a00000, v135
	v_mul_f32_e32 v135, 0xbfb8aa3b, v137
	v_exp_f32_e32 v135, v135
	v_mul_f32_e32 v155, 0xbfb8aa3b, v159
	v_rcp_f32_e32 v170, v114
	v_exp_f32_e32 v155, v155
	v_add_f32_e32 v114, 1.0, v135
	v_max_f32_e32 v135, v138, v138
	v_max_f32_e32 v138, 0xc2a00000, v135
	v_max_f32_e32 v135, v166, v166
	v_max_f32_e32 v166, 0xc2a00000, v135
	v_mul_f32_e32 v135, 0xbfb8aa3b, v138
	v_exp_f32_e32 v135, v135
	v_rcp_f32_e32 v161, v114
	v_add_f32_e32 v114, 1.0, v155
	v_mul_f32_e32 v155, 0xbfb8aa3b, v166
	v_exp_f32_e32 v155, v155
	v_rcp_f32_e32 v171, v114
	v_add_f32_e32 v114, 1.0, v135
	v_max_f32_e32 v135, v139, v139
	v_max_f32_e32 v139, 0xc2a00000, v135
	v_max_f32_e32 v135, v167, v167
	v_max_f32_e32 v167, 0xc2a00000, v135
	v_mul_f32_e32 v135, 0xbfb8aa3b, v139
	v_rcp_f32_e32 v178, v114
	v_add_f32_e32 v114, 1.0, v155
	v_exp_f32_e32 v135, v135
	v_mul_f32_e32 v155, 0xbfb8aa3b, v167
	v_exp_f32_e32 v155, v155
	v_rcp_f32_e32 v180, v114
	v_add_f32_e32 v114, 1.0, v135
	v_rcp_f32_e32 v179, v114
	v_add_f32_e32 v114, 1.0, v155
	v_rcp_f32_e32 v181, v114
	v_pk_mul_f32 v[168:169], v[136:137], v[160:161]
	v_pk_mul_f32 v[138:139], v[138:139], v[178:179]
	v_pk_mul_f32 v[170:171], v[158:159], v[170:171]
	v_pk_mul_f32 v[166:167], v[166:167], v[180:181]
.LBB0_364:
	v_or_b32_e32 v136, 48, v152
	v_ashrrev_i32_e32 v137, 31, v136
	v_lshlrev_b64 v[136:137], 12, v[136:137]
	v_mov_b32_e32 v135, v134
	v_lshl_add_u64 v[136:137], v[132:133], 0, v[136:137]
	v_cvt_pk_bf16_f32 v168, v168, v169
	v_cvt_pk_bf16_f32 v169, v138, v139
	v_cvt_pk_bf16_f32 v170, v170, v171
	v_cvt_pk_bf16_f32 v171, v166, v167
	v_mov_b32_e32 v158, v134
	v_mov_b32_e32 v159, v134
	ds_bpermute_b32 v232, v244, v168
	ds_bpermute_b32 v233, v244, v169
	ds_bpermute_b32 v234, v244, v170
	ds_bpermute_b32 v235, v244, v171
	ds_bpermute_b32 v236, v244, v136
	v_pk_mul_f32 v[138:139], v[72:73], v[158:159]
	v_pk_mul_f32 v[166:167], v[68:69], v[158:159]
	v_pk_mul_f32 v[168:169], v[70:71], v[134:135]
	s_and_b64 vcc, exec, s[40:41]
	v_pk_mul_f32 v[170:171], v[66:67], v[134:135]
	s_waitcnt lgkmcnt(0)
	v_subrev_u32_e32 v236, s82, v236
	global_store_dwordx4 v236, v[232:235], s[82:83]
	s_cbranch_vccnz .LBB0_366
	v_max_f32_e32 v114, v168, v168
	v_max_f32_e32 v134, 0xc2a00000, v114
	v_max_f32_e32 v114, v170, v170
	v_max_f32_e32 v158, 0xc2a00000, v114
	v_mul_f32_e32 v114, 0xbfb8aa3b, v134
	v_exp_f32_e32 v114, v114
	v_mul_f32_e32 v135, 0xbfb8aa3b, v158
	v_exp_f32_e32 v135, v135
	v_max_f32_e32 v155, v171, v171
	v_add_f32_e32 v114, 1.0, v114
	v_rcp_f32_e32 v160, v114
	v_add_f32_e32 v114, 1.0, v135
	v_max_f32_e32 v135, v169, v169
	v_max_f32_e32 v135, 0xc2a00000, v135
	v_max_f32_e32 v159, 0xc2a00000, v155
	v_mul_f32_e32 v155, 0xbfb8aa3b, v135
	v_exp_f32_e32 v155, v155
	v_mul_f32_e32 v161, 0xbfb8aa3b, v159
	v_exp_f32_e32 v168, v161
	v_max_f32_e32 v138, v138, v138
	v_rcp_f32_e32 v170, v114
	v_add_f32_e32 v114, 1.0, v155
	v_max_f32_e32 v138, 0xc2a00000, v138
	v_max_f32_e32 v155, v166, v166
	v_max_f32_e32 v166, 0xc2a00000, v155
	v_mul_f32_e32 v155, 0xbfb8aa3b, v138
	v_exp_f32_e32 v155, v155
	v_rcp_f32_e32 v161, v114
	v_add_f32_e32 v114, 1.0, v168
	v_mul_f32_e32 v168, 0xbfb8aa3b, v166
	v_exp_f32_e32 v168, v168
	v_max_f32_e32 v139, v139, v139
	v_rcp_f32_e32 v171, v114
	v_add_f32_e32 v114, 1.0, v155
	v_max_f32_e32 v139, 0xc2a00000, v139
	v_max_f32_e32 v155, v167, v167
	v_max_f32_e32 v167, 0xc2a00000, v155
	v_mul_f32_e32 v155, 0xbfb8aa3b, v139
	v_rcp_f32_e32 v178, v114
	v_add_f32_e32 v114, 1.0, v168
	v_exp_f32_e32 v155, v155
	v_mul_f32_e32 v168, 0xbfb8aa3b, v167
	v_exp_f32_e32 v168, v168
	v_rcp_f32_e32 v180, v114
	v_add_f32_e32 v114, 1.0, v155
	v_rcp_f32_e32 v179, v114
	v_add_f32_e32 v114, 1.0, v168
	v_rcp_f32_e32 v181, v114
	v_pk_mul_f32 v[168:169], v[134:135], v[160:161]
	v_pk_mul_f32 v[138:139], v[138:139], v[178:179]
	v_pk_mul_f32 v[170:171], v[158:159], v[170:171]
	v_pk_mul_f32 v[166:167], v[166:167], v[180:181]
.LBB0_366:
	ds_read_b32 v134, v176 offset:512
	v_cvt_pk_bf16_f32 v168, v168, v169
	v_cvt_pk_bf16_f32 v169, v138, v139
	v_cvt_pk_bf16_f32 v170, v170, v171
	v_cvt_pk_bf16_f32 v171, v166, v167
	ds_bpermute_b32 v238, v244, v168
	ds_bpermute_b32 v239, v244, v169
	ds_bpermute_b32 v240, v244, v170
	ds_bpermute_b32 v241, v244, v171
	ds_bpermute_b32 v242, v244, v136
	s_waitcnt lgkmcnt(0)
	v_pk_mul_f32 v[138:139], v[64:65], v[134:135] op_sel_hi:[1,0]
	v_pk_mul_f32 v[166:167], v[60:61], v[134:135] op_sel_hi:[1,0]
	v_pk_mul_f32 v[168:169], v[62:63], v[134:135] op_sel_hi:[1,0]
	s_and_b64 vcc, exec, s[40:41]
	v_pk_mul_f32 v[170:171], v[58:59], v[134:135] op_sel_hi:[1,0]
	s_waitcnt lgkmcnt(0)
	v_subrev_u32_e32 v242, s82, v242
	global_store_dwordx4 v242, v[238:241], s[82:83] offset:64
	s_cbranch_vccnz .LBB0_368
	v_max_f32_e32 v114, v168, v168
	v_max_f32_e32 v136, 0xc2a00000, v114
	v_max_f32_e32 v114, v170, v170
	v_max_f32_e32 v158, 0xc2a00000, v114
	v_mul_f32_e32 v114, 0xbfb8aa3b, v136
	v_exp_f32_e32 v114, v114
	v_mul_f32_e32 v135, 0xbfb8aa3b, v158
	v_exp_f32_e32 v135, v135
	v_add_f32_e32 v114, 1.0, v114
	v_rcp_f32_e32 v160, v114
	v_add_f32_e32 v114, 1.0, v135
	v_max_f32_e32 v135, v169, v169
	v_max_f32_e32 v137, 0xc2a00000, v135
	v_max_f32_e32 v135, v171, v171
	v_max_f32_e32 v159, 0xc2a00000, v135
	v_mul_f32_e32 v135, 0xbfb8aa3b, v137
	v_exp_f32_e32 v135, v135
	v_mul_f32_e32 v155, 0xbfb8aa3b, v159
	v_rcp_f32_e32 v170, v114
	v_exp_f32_e32 v155, v155
	v_add_f32_e32 v114, 1.0, v135
	v_max_f32_e32 v135, v138, v138
	v_max_f32_e32 v138, 0xc2a00000, v135
	v_max_f32_e32 v135, v166, v166
	v_max_f32_e32 v166, 0xc2a00000, v135
	v_mul_f32_e32 v135, 0xbfb8aa3b, v138
	v_exp_f32_e32 v135, v135
	v_rcp_f32_e32 v161, v114
	v_add_f32_e32 v114, 1.0, v155
	v_mul_f32_e32 v155, 0xbfb8aa3b, v166
	v_exp_f32_e32 v155, v155
	v_rcp_f32_e32 v171, v114
	v_add_f32_e32 v114, 1.0, v135
	v_max_f32_e32 v135, v139, v139
	v_max_f32_e32 v139, 0xc2a00000, v135
	v_max_f32_e32 v135, v167, v167
	v_max_f32_e32 v167, 0xc2a00000, v135
	v_mul_f32_e32 v135, 0xbfb8aa3b, v139
	v_rcp_f32_e32 v178, v114
	v_add_f32_e32 v114, 1.0, v155
	v_exp_f32_e32 v135, v135
	v_mul_f32_e32 v155, 0xbfb8aa3b, v167
	v_exp_f32_e32 v155, v155
	v_rcp_f32_e32 v180, v114
	v_add_f32_e32 v114, 1.0, v135
	v_rcp_f32_e32 v179, v114
	v_add_f32_e32 v114, 1.0, v155
	v_rcp_f32_e32 v181, v114
	v_pk_mul_f32 v[168:169], v[136:137], v[160:161]
	v_pk_mul_f32 v[138:139], v[138:139], v[178:179]
	v_pk_mul_f32 v[170:171], v[158:159], v[170:171]
	v_pk_mul_f32 v[166:167], v[166:167], v[180:181]
.LBB0_368:
	v_lshlrev_b64 v[136:137], 12, v[152:153]
	v_lshl_add_u64 v[136:137], v[132:133], 0, v[136:137]
	s_mov_b32 s14, 0x80000
	v_cvt_pk_bf16_f32 v168, v168, v169
	v_cvt_pk_bf16_f32 v169, v138, v139
	v_add_co_u32_e32 v138, vcc, s14, v136
	v_mov_b32_e32 v135, v134
	v_cvt_pk_bf16_f32 v170, v170, v171
	v_cvt_pk_bf16_f32 v171, v166, v167
	s_nop 0
	v_addc_co_u32_e32 v139, vcc, 0, v137, vcc
	v_mov_b32_e32 v158, v134
	v_mov_b32_e32 v159, v134
	ds_bpermute_b32 v232, v244, v168
	ds_bpermute_b32 v233, v244, v169
	ds_bpermute_b32 v234, v244, v170
	ds_bpermute_b32 v235, v244, v171
	ds_bpermute_b32 v236, v244, v138
	v_pk_mul_f32 v[138:139], v[56:57], v[158:159]
	v_pk_mul_f32 v[166:167], v[52:53], v[158:159]
	v_pk_mul_f32 v[168:169], v[54:55], v[134:135]
	s_and_b64 vcc, exec, s[40:41]
	v_pk_mul_f32 v[170:171], v[50:51], v[134:135]
	s_waitcnt lgkmcnt(0)
	v_subrev_u32_e32 v236, s82, v236
	global_store_dwordx4 v236, v[232:235], s[82:83]
	s_cbranch_vccnz .LBB0_370
	v_max_f32_e32 v114, v168, v168
	v_max_f32_e32 v134, 0xc2a00000, v114
	v_max_f32_e32 v114, v170, v170
	v_max_f32_e32 v158, 0xc2a00000, v114
	v_mul_f32_e32 v114, 0xbfb8aa3b, v134
	v_exp_f32_e32 v114, v114
	v_mul_f32_e32 v135, 0xbfb8aa3b, v158
	v_exp_f32_e32 v135, v135
	v_max_f32_e32 v155, v171, v171
	v_add_f32_e32 v114, 1.0, v114
	v_rcp_f32_e32 v160, v114
	v_add_f32_e32 v114, 1.0, v135
	v_max_f32_e32 v135, v169, v169
	v_max_f32_e32 v135, 0xc2a00000, v135
	v_max_f32_e32 v159, 0xc2a00000, v155
	v_mul_f32_e32 v155, 0xbfb8aa3b, v135
	v_exp_f32_e32 v155, v155
	v_mul_f32_e32 v161, 0xbfb8aa3b, v159
	v_exp_f32_e32 v168, v161
	v_max_f32_e32 v138, v138, v138
	v_rcp_f32_e32 v170, v114
	v_add_f32_e32 v114, 1.0, v155
	v_max_f32_e32 v138, 0xc2a00000, v138
	v_max_f32_e32 v155, v166, v166
	v_max_f32_e32 v166, 0xc2a00000, v155
	v_mul_f32_e32 v155, 0xbfb8aa3b, v138
	v_exp_f32_e32 v155, v155
	v_rcp_f32_e32 v161, v114
	v_add_f32_e32 v114, 1.0, v168
	v_mul_f32_e32 v168, 0xbfb8aa3b, v166
	v_exp_f32_e32 v168, v168
	v_max_f32_e32 v139, v139, v139
	v_rcp_f32_e32 v171, v114
	v_add_f32_e32 v114, 1.0, v155
	v_max_f32_e32 v139, 0xc2a00000, v139
	v_max_f32_e32 v155, v167, v167
	v_max_f32_e32 v167, 0xc2a00000, v155
	v_mul_f32_e32 v155, 0xbfb8aa3b, v139
	v_rcp_f32_e32 v178, v114
	v_add_f32_e32 v114, 1.0, v168
	v_exp_f32_e32 v155, v155
	v_mul_f32_e32 v168, 0xbfb8aa3b, v167
	v_exp_f32_e32 v168, v168
	v_rcp_f32_e32 v180, v114
	v_add_f32_e32 v114, 1.0, v155
	v_rcp_f32_e32 v179, v114
	v_add_f32_e32 v114, 1.0, v168
	v_rcp_f32_e32 v181, v114
	v_pk_mul_f32 v[168:169], v[134:135], v[160:161]
	v_pk_mul_f32 v[138:139], v[138:139], v[178:179]
	v_pk_mul_f32 v[170:171], v[158:159], v[170:171]
	v_pk_mul_f32 v[166:167], v[166:167], v[180:181]
.LBB0_370:
	ds_read_b32 v134, v176 offset:576
	s_mov_b64 s[14:15], 0x80000
	v_lshl_add_u64 v[158:159], v[136:137], 0, s[14:15]
	v_cvt_pk_bf16_f32 v137, v138, v139
	v_cvt_pk_bf16_f32 v138, v170, v171
	v_cvt_pk_bf16_f32 v139, v166, v167
	v_cvt_pk_bf16_f32 v136, v168, v169
	ds_bpermute_b32 v238, v244, v136
	ds_bpermute_b32 v239, v244, v137
	ds_bpermute_b32 v240, v244, v138
	ds_bpermute_b32 v241, v244, v139
	ds_bpermute_b32 v242, v244, v158
	s_waitcnt lgkmcnt(0)
	v_pk_mul_f32 v[168:169], v[46:47], v[134:135] op_sel_hi:[1,0]
	v_pk_mul_f32 v[166:167], v[44:45], v[134:135] op_sel_hi:[1,0]
	v_pk_mul_f32 v[138:139], v[48:49], v[134:135] op_sel_hi:[1,0]
	s_and_b64 vcc, exec, s[40:41]
	v_pk_mul_f32 v[170:171], v[42:43], v[134:135] op_sel_hi:[1,0]
	s_waitcnt lgkmcnt(0)
	v_subrev_u32_e32 v242, s82, v242
	global_store_dwordx4 v242, v[238:241], s[82:83] offset:64
	s_cbranch_vccnz .LBB0_372
	v_max_f32_e32 v114, v168, v168
	v_max_f32_e32 v136, 0xc2a00000, v114
	v_max_f32_e32 v114, v170, v170
	v_max_f32_e32 v158, 0xc2a00000, v114
	v_mul_f32_e32 v114, 0xbfb8aa3b, v136
	v_exp_f32_e32 v114, v114
	v_mul_f32_e32 v135, 0xbfb8aa3b, v158
	v_exp_f32_e32 v135, v135
	v_add_f32_e32 v114, 1.0, v114
	v_rcp_f32_e32 v160, v114
	v_add_f32_e32 v114, 1.0, v135
	v_max_f32_e32 v135, v169, v169
	v_max_f32_e32 v137, 0xc2a00000, v135
	v_max_f32_e32 v135, v171, v171
	v_max_f32_e32 v159, 0xc2a00000, v135
	v_mul_f32_e32 v135, 0xbfb8aa3b, v137
	v_exp_f32_e32 v135, v135
	v_mul_f32_e32 v155, 0xbfb8aa3b, v159
	v_rcp_f32_e32 v170, v114
	v_exp_f32_e32 v155, v155
	v_add_f32_e32 v114, 1.0, v135
	v_max_f32_e32 v135, v138, v138
	v_max_f32_e32 v138, 0xc2a00000, v135
	v_max_f32_e32 v135, v166, v166
	v_max_f32_e32 v166, 0xc2a00000, v135
	v_mul_f32_e32 v135, 0xbfb8aa3b, v138
	v_exp_f32_e32 v135, v135
	v_rcp_f32_e32 v161, v114
	v_add_f32_e32 v114, 1.0, v155
	v_mul_f32_e32 v155, 0xbfb8aa3b, v166
	v_exp_f32_e32 v155, v155
	v_rcp_f32_e32 v171, v114
	v_add_f32_e32 v114, 1.0, v135
	v_max_f32_e32 v135, v139, v139
	v_max_f32_e32 v139, 0xc2a00000, v135
	v_max_f32_e32 v135, v167, v167
	v_max_f32_e32 v167, 0xc2a00000, v135
	v_mul_f32_e32 v135, 0xbfb8aa3b, v139
	v_rcp_f32_e32 v178, v114
	v_add_f32_e32 v114, 1.0, v155
	v_exp_f32_e32 v135, v135
	v_mul_f32_e32 v155, 0xbfb8aa3b, v167
	v_exp_f32_e32 v155, v155
	v_rcp_f32_e32 v180, v114
	v_add_f32_e32 v114, 1.0, v135
	v_rcp_f32_e32 v179, v114
	v_add_f32_e32 v114, 1.0, v155
	v_rcp_f32_e32 v181, v114
	v_pk_mul_f32 v[168:169], v[136:137], v[160:161]
	v_pk_mul_f32 v[138:139], v[138:139], v[178:179]
	v_pk_mul_f32 v[170:171], v[158:159], v[170:171]
	v_pk_mul_f32 v[166:167], v[166:167], v[180:181]
.LBB0_372:
	v_lshlrev_b64 v[136:137], 12, v[152:153]
	v_lshl_add_u64 v[136:137], v[132:133], 0, v[136:137]
	s_mov_b32 s14, 0x90000
	v_cvt_pk_bf16_f32 v168, v168, v169
	v_cvt_pk_bf16_f32 v169, v138, v139
	v_add_co_u32_e32 v138, vcc, s14, v136
	v_mov_b32_e32 v135, v134
	v_cvt_pk_bf16_f32 v170, v170, v171
	v_cvt_pk_bf16_f32 v171, v166, v167
	s_nop 0
	v_addc_co_u32_e32 v139, vcc, 0, v137, vcc
	v_mov_b32_e32 v158, v134
	v_mov_b32_e32 v159, v134
	ds_bpermute_b32 v232, v244, v168
	ds_bpermute_b32 v233, v244, v169
	ds_bpermute_b32 v234, v244, v170
	ds_bpermute_b32 v235, v244, v171
	ds_bpermute_b32 v236, v244, v138
	v_pk_mul_f32 v[138:139], v[40:41], v[158:159]
	v_pk_mul_f32 v[166:167], v[36:37], v[158:159]
	v_pk_mul_f32 v[168:169], v[38:39], v[134:135]
	s_and_b64 vcc, exec, s[40:41]
	v_pk_mul_f32 v[170:171], v[34:35], v[134:135]
	s_waitcnt lgkmcnt(0)
	v_subrev_u32_e32 v236, s82, v236
	global_store_dwordx4 v236, v[232:235], s[82:83]
	s_cbranch_vccnz .LBB0_374
	v_max_f32_e32 v114, v168, v168
	v_max_f32_e32 v134, 0xc2a00000, v114
	v_max_f32_e32 v114, v170, v170
	v_max_f32_e32 v158, 0xc2a00000, v114
	v_mul_f32_e32 v114, 0xbfb8aa3b, v134
	v_exp_f32_e32 v114, v114
	v_mul_f32_e32 v135, 0xbfb8aa3b, v158
	v_exp_f32_e32 v135, v135
	v_max_f32_e32 v155, v171, v171
	v_add_f32_e32 v114, 1.0, v114
	v_rcp_f32_e32 v160, v114
	v_add_f32_e32 v114, 1.0, v135
	v_max_f32_e32 v135, v169, v169
	v_max_f32_e32 v135, 0xc2a00000, v135
	v_max_f32_e32 v159, 0xc2a00000, v155
	v_mul_f32_e32 v155, 0xbfb8aa3b, v135
	v_exp_f32_e32 v155, v155
	v_mul_f32_e32 v161, 0xbfb8aa3b, v159
	v_exp_f32_e32 v168, v161
	v_max_f32_e32 v138, v138, v138
	v_rcp_f32_e32 v170, v114
	v_add_f32_e32 v114, 1.0, v155
	v_max_f32_e32 v138, 0xc2a00000, v138
	v_max_f32_e32 v155, v166, v166
	v_max_f32_e32 v166, 0xc2a00000, v155
	v_mul_f32_e32 v155, 0xbfb8aa3b, v138
	v_exp_f32_e32 v155, v155
	v_rcp_f32_e32 v161, v114
	v_add_f32_e32 v114, 1.0, v168
	v_mul_f32_e32 v168, 0xbfb8aa3b, v166
	v_exp_f32_e32 v168, v168
	v_max_f32_e32 v139, v139, v139
	v_rcp_f32_e32 v171, v114
	v_add_f32_e32 v114, 1.0, v155
	v_max_f32_e32 v139, 0xc2a00000, v139
	v_max_f32_e32 v155, v167, v167
	v_max_f32_e32 v167, 0xc2a00000, v155
	v_mul_f32_e32 v155, 0xbfb8aa3b, v139
	v_rcp_f32_e32 v178, v114
	v_add_f32_e32 v114, 1.0, v168
	v_exp_f32_e32 v155, v155
	v_mul_f32_e32 v168, 0xbfb8aa3b, v167
	v_exp_f32_e32 v168, v168
	v_rcp_f32_e32 v180, v114
	v_add_f32_e32 v114, 1.0, v155
	v_rcp_f32_e32 v179, v114
	v_add_f32_e32 v114, 1.0, v168
	v_rcp_f32_e32 v181, v114
	v_pk_mul_f32 v[168:169], v[134:135], v[160:161]
	v_pk_mul_f32 v[138:139], v[138:139], v[178:179]
	v_pk_mul_f32 v[170:171], v[158:159], v[170:171]
	v_pk_mul_f32 v[166:167], v[166:167], v[180:181]
.LBB0_374:
	ds_read_b32 v134, v176 offset:640
	s_mov_b64 s[14:15], 0x90000
	v_lshl_add_u64 v[158:159], v[136:137], 0, s[14:15]
	v_cvt_pk_bf16_f32 v137, v138, v139
	v_cvt_pk_bf16_f32 v138, v170, v171
	v_cvt_pk_bf16_f32 v139, v166, v167
	v_cvt_pk_bf16_f32 v136, v168, v169
	ds_bpermute_b32 v238, v244, v136
	ds_bpermute_b32 v239, v244, v137
	ds_bpermute_b32 v240, v244, v138
	ds_bpermute_b32 v241, v244, v139
	ds_bpermute_b32 v242, v244, v158
	s_waitcnt lgkmcnt(0)
	v_pk_mul_f32 v[168:169], v[30:31], v[134:135] op_sel_hi:[1,0]
	v_pk_mul_f32 v[166:167], v[28:29], v[134:135] op_sel_hi:[1,0]
	v_pk_mul_f32 v[138:139], v[32:33], v[134:135] op_sel_hi:[1,0]
	s_and_b64 vcc, exec, s[40:41]
	v_pk_mul_f32 v[170:171], v[26:27], v[134:135] op_sel_hi:[1,0]
	s_waitcnt lgkmcnt(0)
	v_subrev_u32_e32 v242, s82, v242
	global_store_dwordx4 v242, v[238:241], s[82:83] offset:64
	s_cbranch_vccnz .LBB0_376
	v_max_f32_e32 v114, v168, v168
	v_max_f32_e32 v136, 0xc2a00000, v114
	v_max_f32_e32 v114, v170, v170
	v_max_f32_e32 v158, 0xc2a00000, v114
	v_mul_f32_e32 v114, 0xbfb8aa3b, v136
	v_exp_f32_e32 v114, v114
	v_mul_f32_e32 v135, 0xbfb8aa3b, v158
	v_exp_f32_e32 v135, v135
	v_add_f32_e32 v114, 1.0, v114
	v_rcp_f32_e32 v160, v114
	v_add_f32_e32 v114, 1.0, v135
	v_max_f32_e32 v135, v169, v169
	v_max_f32_e32 v137, 0xc2a00000, v135
	v_max_f32_e32 v135, v171, v171
	v_max_f32_e32 v159, 0xc2a00000, v135
	v_mul_f32_e32 v135, 0xbfb8aa3b, v137
	v_exp_f32_e32 v135, v135
	v_mul_f32_e32 v155, 0xbfb8aa3b, v159
	v_rcp_f32_e32 v170, v114
	v_exp_f32_e32 v155, v155
	v_add_f32_e32 v114, 1.0, v135
	v_max_f32_e32 v135, v138, v138
	v_max_f32_e32 v138, 0xc2a00000, v135
	v_max_f32_e32 v135, v166, v166
	v_max_f32_e32 v166, 0xc2a00000, v135
	v_mul_f32_e32 v135, 0xbfb8aa3b, v138
	v_exp_f32_e32 v135, v135
	v_rcp_f32_e32 v161, v114
	v_add_f32_e32 v114, 1.0, v155
	v_mul_f32_e32 v155, 0xbfb8aa3b, v166
	v_exp_f32_e32 v155, v155
	v_rcp_f32_e32 v171, v114
	v_add_f32_e32 v114, 1.0, v135
	v_max_f32_e32 v135, v139, v139
	v_max_f32_e32 v139, 0xc2a00000, v135
	v_max_f32_e32 v135, v167, v167
	v_max_f32_e32 v167, 0xc2a00000, v135
	v_mul_f32_e32 v135, 0xbfb8aa3b, v139
	v_rcp_f32_e32 v178, v114
	v_add_f32_e32 v114, 1.0, v155
	v_exp_f32_e32 v135, v135
	v_mul_f32_e32 v155, 0xbfb8aa3b, v167
	v_exp_f32_e32 v155, v155
	v_rcp_f32_e32 v180, v114
	v_add_f32_e32 v114, 1.0, v135
	v_rcp_f32_e32 v179, v114
	v_add_f32_e32 v114, 1.0, v155
	v_rcp_f32_e32 v181, v114
	v_pk_mul_f32 v[168:169], v[136:137], v[160:161]
	v_pk_mul_f32 v[138:139], v[138:139], v[178:179]
	v_pk_mul_f32 v[170:171], v[158:159], v[170:171]
	v_pk_mul_f32 v[166:167], v[166:167], v[180:181]
.LBB0_376:
	v_lshlrev_b64 v[136:137], 12, v[152:153]
	v_lshl_add_u64 v[136:137], v[132:133], 0, v[136:137]
	s_mov_b32 s14, 0xa0000
	v_cvt_pk_bf16_f32 v168, v168, v169
	v_cvt_pk_bf16_f32 v169, v138, v139
	v_add_co_u32_e32 v138, vcc, s14, v136
	v_mov_b32_e32 v135, v134
	v_cvt_pk_bf16_f32 v170, v170, v171
	v_cvt_pk_bf16_f32 v171, v166, v167
	s_nop 0
	v_addc_co_u32_e32 v139, vcc, 0, v137, vcc
	v_mov_b32_e32 v158, v134
	v_mov_b32_e32 v159, v134
	ds_bpermute_b32 v232, v244, v168
	ds_bpermute_b32 v233, v244, v169
	ds_bpermute_b32 v234, v244, v170
	ds_bpermute_b32 v235, v244, v171
	ds_bpermute_b32 v236, v244, v138
	v_pk_mul_f32 v[138:139], v[24:25], v[158:159]
	v_pk_mul_f32 v[166:167], v[20:21], v[158:159]
	v_pk_mul_f32 v[168:169], v[22:23], v[134:135]
	s_and_b64 vcc, exec, s[40:41]
	v_pk_mul_f32 v[170:171], v[18:19], v[134:135]
	s_waitcnt lgkmcnt(0)
	v_subrev_u32_e32 v236, s82, v236
	global_store_dwordx4 v236, v[232:235], s[82:83]
	s_cbranch_vccnz .LBB0_378
	v_max_f32_e32 v114, v168, v168
	v_max_f32_e32 v134, 0xc2a00000, v114
	v_max_f32_e32 v114, v170, v170
	v_max_f32_e32 v158, 0xc2a00000, v114
	v_mul_f32_e32 v114, 0xbfb8aa3b, v134
	v_exp_f32_e32 v114, v114
	v_mul_f32_e32 v135, 0xbfb8aa3b, v158
	v_exp_f32_e32 v135, v135
	v_max_f32_e32 v155, v171, v171
	v_add_f32_e32 v114, 1.0, v114
	v_rcp_f32_e32 v160, v114
	v_add_f32_e32 v114, 1.0, v135
	v_max_f32_e32 v135, v169, v169
	v_max_f32_e32 v135, 0xc2a00000, v135
	v_max_f32_e32 v159, 0xc2a00000, v155
	v_mul_f32_e32 v155, 0xbfb8aa3b, v135
	v_exp_f32_e32 v155, v155
	v_mul_f32_e32 v161, 0xbfb8aa3b, v159
	v_exp_f32_e32 v168, v161
	v_max_f32_e32 v138, v138, v138
	v_rcp_f32_e32 v170, v114
	v_add_f32_e32 v114, 1.0, v155
	v_max_f32_e32 v138, 0xc2a00000, v138
	v_max_f32_e32 v155, v166, v166
	v_max_f32_e32 v166, 0xc2a00000, v155
	v_mul_f32_e32 v155, 0xbfb8aa3b, v138
	v_exp_f32_e32 v155, v155
	v_rcp_f32_e32 v161, v114
	v_add_f32_e32 v114, 1.0, v168
	v_mul_f32_e32 v168, 0xbfb8aa3b, v166
	v_exp_f32_e32 v168, v168
	v_max_f32_e32 v139, v139, v139
	v_rcp_f32_e32 v171, v114
	v_add_f32_e32 v114, 1.0, v155
	v_max_f32_e32 v139, 0xc2a00000, v139
	v_max_f32_e32 v155, v167, v167
	v_max_f32_e32 v167, 0xc2a00000, v155
	v_mul_f32_e32 v155, 0xbfb8aa3b, v139
	v_rcp_f32_e32 v178, v114
	v_add_f32_e32 v114, 1.0, v168
	v_exp_f32_e32 v155, v155
	v_mul_f32_e32 v168, 0xbfb8aa3b, v167
	v_exp_f32_e32 v168, v168
	v_rcp_f32_e32 v180, v114
	v_add_f32_e32 v114, 1.0, v155
	v_rcp_f32_e32 v179, v114
	v_add_f32_e32 v114, 1.0, v168
	v_rcp_f32_e32 v181, v114
	v_pk_mul_f32 v[168:169], v[134:135], v[160:161]
	v_pk_mul_f32 v[138:139], v[138:139], v[178:179]
	v_pk_mul_f32 v[170:171], v[158:159], v[170:171]
	v_pk_mul_f32 v[166:167], v[166:167], v[180:181]
.LBB0_378:
	ds_read_b32 v134, v176 offset:704
	s_mov_b64 s[14:15], 0xa0000
	v_lshl_add_u64 v[158:159], v[136:137], 0, s[14:15]
	v_cvt_pk_bf16_f32 v136, v168, v169
	v_cvt_pk_bf16_f32 v137, v138, v139
	v_cvt_pk_bf16_f32 v138, v170, v171
	v_cvt_pk_bf16_f32 v139, v166, v167
	ds_bpermute_b32 v238, v244, v136
	ds_bpermute_b32 v239, v244, v137
	ds_bpermute_b32 v240, v244, v138
	ds_bpermute_b32 v241, v244, v139
	ds_bpermute_b32 v242, v244, v158
	s_waitcnt lgkmcnt(0)
	v_pk_mul_f32 v[166:167], v[14:15], v[134:135] op_sel_hi:[1,0]
	s_and_b64 vcc, exec, s[40:41]
	v_pk_mul_f32 v[136:137], v[16:17], v[134:135] op_sel_hi:[1,0]
	v_pk_mul_f32 v[138:139], v[12:13], v[134:135] op_sel_hi:[1,0]
	v_pk_mul_f32 v[168:169], v[10:11], v[134:135] op_sel_hi:[1,0]
	s_waitcnt lgkmcnt(0)
	v_subrev_u32_e32 v242, s82, v242
	global_store_dwordx4 v242, v[238:241], s[82:83] offset:64
	s_cbranch_vccnz .LBB0_380
	v_max_f32_e32 v114, v166, v166
	v_max_f32_e32 v158, 0xc2a00000, v114
	v_max_f32_e32 v114, v168, v168
	v_max_f32_e32 v160, 0xc2a00000, v114
	v_mul_f32_e32 v114, 0xbfb8aa3b, v158
	v_exp_f32_e32 v114, v114
	v_mul_f32_e32 v135, 0xbfb8aa3b, v160
	v_exp_f32_e32 v135, v135
	v_add_f32_e32 v114, 1.0, v114
	v_rcp_f32_e32 v166, v114
	v_add_f32_e32 v114, 1.0, v135
	v_max_f32_e32 v135, v167, v167
	v_max_f32_e32 v159, 0xc2a00000, v135
	v_max_f32_e32 v135, v169, v169
	v_max_f32_e32 v161, 0xc2a00000, v135
	v_mul_f32_e32 v135, 0xbfb8aa3b, v159
	v_exp_f32_e32 v135, v135
	v_mul_f32_e32 v155, 0xbfb8aa3b, v161
	v_rcp_f32_e32 v168, v114
	v_exp_f32_e32 v155, v155
	v_add_f32_e32 v114, 1.0, v135
	v_max_f32_e32 v135, v136, v136
	v_max_f32_e32 v136, 0xc2a00000, v135
	v_max_f32_e32 v135, v138, v138
	v_max_f32_e32 v138, 0xc2a00000, v135
	v_mul_f32_e32 v135, 0xbfb8aa3b, v136
	v_exp_f32_e32 v135, v135
	v_rcp_f32_e32 v167, v114
	v_add_f32_e32 v114, 1.0, v155
	v_mul_f32_e32 v155, 0xbfb8aa3b, v138
	v_exp_f32_e32 v155, v155
	v_rcp_f32_e32 v169, v114
	v_add_f32_e32 v114, 1.0, v135
	v_max_f32_e32 v135, v137, v137
	v_max_f32_e32 v137, 0xc2a00000, v135
	v_max_f32_e32 v135, v139, v139
	v_max_f32_e32 v139, 0xc2a00000, v135
	v_mul_f32_e32 v135, 0xbfb8aa3b, v137
	v_rcp_f32_e32 v170, v114
	v_add_f32_e32 v114, 1.0, v155
	v_exp_f32_e32 v135, v135
	v_mul_f32_e32 v155, 0xbfb8aa3b, v139
	v_exp_f32_e32 v155, v155
	v_rcp_f32_e32 v178, v114
	v_add_f32_e32 v114, 1.0, v135
	v_rcp_f32_e32 v171, v114
	v_add_f32_e32 v114, 1.0, v155
	v_rcp_f32_e32 v179, v114
	v_pk_mul_f32 v[166:167], v[158:159], v[166:167]
	v_pk_mul_f32 v[136:137], v[136:137], v[170:171]
	v_pk_mul_f32 v[168:169], v[160:161], v[168:169]
	v_pk_mul_f32 v[138:139], v[138:139], v[178:179]
.LBB0_380:
	v_lshlrev_b64 v[158:159], 12, v[152:153]
	v_lshl_add_u64 v[132:133], v[132:133], 0, v[158:159]
	s_mov_b32 s14, 0xb0000
	v_cvt_pk_bf16_f32 v166, v166, v167
	v_cvt_pk_bf16_f32 v167, v136, v137
	v_add_co_u32_e32 v136, vcc, s14, v132
	v_mov_b32_e32 v135, v134
	s_nop 0
	v_addc_co_u32_e32 v137, vcc, 0, v133, vcc
	v_cvt_pk_bf16_f32 v168, v168, v169
	v_cvt_pk_bf16_f32 v169, v138, v139
	ds_bpermute_b32 v232, v244, v166
	ds_bpermute_b32 v233, v244, v167
	ds_bpermute_b32 v234, v244, v168
	ds_bpermute_b32 v235, v244, v169
	ds_bpermute_b32 v236, v244, v136
	v_mov_b32_e32 v136, v134
	v_mov_b32_e32 v137, v134
	v_pk_mul_f32 v[138:139], v[8:9], v[136:137]
	v_pk_mul_f32 v[168:169], v[6:7], v[134:135]
	v_pk_mul_f32 v[166:167], v[4:5], v[136:137]
	s_and_b64 vcc, exec, s[40:41]
	v_pk_mul_f32 v[134:135], v[2:3], v[134:135]
	s_waitcnt lgkmcnt(0)
	v_subrev_u32_e32 v236, s82, v236
	global_store_dwordx4 v236, v[232:235], s[82:83]
	s_cbranch_vccnz .LBB0_382
	v_max_f32_e32 v114, v168, v168
	v_max_f32_e32 v136, 0xc2a00000, v114
	v_max_f32_e32 v114, v134, v134
	v_max_f32_e32 v134, 0xc2a00000, v114
	v_mul_f32_e32 v114, 0xbfb8aa3b, v136
	v_exp_f32_e32 v114, v114
	v_mul_f32_e32 v137, 0xbfb8aa3b, v134
	v_exp_f32_e32 v137, v137
	v_max_f32_e32 v135, v135, v135
	v_add_f32_e32 v114, 1.0, v114
	v_rcp_f32_e32 v158, v114
	v_add_f32_e32 v114, 1.0, v137
	v_max_f32_e32 v137, v169, v169
	v_max_f32_e32 v137, 0xc2a00000, v137
	v_mul_f32_e32 v153, 0xbfb8aa3b, v137
	v_exp_f32_e32 v153, v153
	v_max_f32_e32 v135, 0xc2a00000, v135
	v_mul_f32_e32 v155, 0xbfb8aa3b, v135
	v_exp_f32_e32 v155, v155
	v_max_f32_e32 v138, v138, v138
	v_rcp_f32_e32 v160, v114
	v_add_f32_e32 v114, 1.0, v153
	v_max_f32_e32 v138, 0xc2a00000, v138
	v_max_f32_e32 v153, v166, v166
	v_max_f32_e32 v166, 0xc2a00000, v153
	v_mul_f32_e32 v153, 0xbfb8aa3b, v138
	v_exp_f32_e32 v153, v153
	v_rcp_f32_e32 v159, v114
	v_add_f32_e32 v114, 1.0, v155
	v_mul_f32_e32 v155, 0xbfb8aa3b, v166
	v_exp_f32_e32 v155, v155
	v_max_f32_e32 v139, v139, v139
	v_rcp_f32_e32 v161, v114
	v_add_f32_e32 v114, 1.0, v153
	v_max_f32_e32 v139, 0xc2a00000, v139
	v_max_f32_e32 v153, v167, v167
	v_max_f32_e32 v167, 0xc2a00000, v153
	v_mul_f32_e32 v153, 0xbfb8aa3b, v139
	v_rcp_f32_e32 v170, v114
	v_add_f32_e32 v114, 1.0, v155
	v_exp_f32_e32 v153, v153
	v_mul_f32_e32 v155, 0xbfb8aa3b, v167
	v_exp_f32_e32 v155, v155
	v_rcp_f32_e32 v178, v114
	v_add_f32_e32 v114, 1.0, v153
	v_rcp_f32_e32 v171, v114
	v_add_f32_e32 v114, 1.0, v155
	v_rcp_f32_e32 v179, v114
	v_pk_mul_f32 v[168:169], v[136:137], v[158:159]
	v_pk_mul_f32 v[138:139], v[138:139], v[170:171]
	v_pk_mul_f32 v[134:135], v[134:135], v[160:161]
	v_pk_mul_f32 v[166:167], v[166:167], v[178:179]

.LBB0_383:
	s_andn2_b64 vcc, exec, s[38:39]
	s_mov_b64 s[28:29], -1
	ds_bpermute_b32 v238, v244, v132
	ds_bpermute_b32 v239, v244, v133
	ds_bpermute_b32 v240, v244, v134
	ds_bpermute_b32 v241, v244, v135
	ds_bpermute_b32 v242, v244, v136
	s_waitcnt lgkmcnt(0)
	v_subrev_u32_e32 v242, s82, v242
	global_store_dwordx4 v242, v[238:241], s[82:83] offset:64
	s_cbranch_vccnz .LBB0_338
	s_branch .LBB0_386
.LBB0_384:
	s_and_b64 vcc, exec, s[40:41]
	s_cbranch_vccz .LBB0_383
	v_lshlrev_b32_e32 v155, 2, v177
	global_load_dwordx4 v[136:139], v155, s[44:45]
	global_load_dwordx4 v[132:135], v155, s[44:45] offset:16
	s_waitcnt lgkmcnt(0)
	v_mul_f32_e32 v160, v128, v154
	v_mul_f32_e32 v161, v129, v154
	v_mul_f32_e32 v166, v130, v154
	v_mul_f32_e32 v167, v131, v154
	v_mul_f32_e32 v168, v124, v154
	v_mul_f32_e32 v169, v125, v154
	v_mul_f32_e32 v170, v126, v154
	v_mul_f32_e32 v171, v127, v154
	global_load_dwordx4 v[124:127], v155, s[44:45] offset:144
	global_load_dwordx4 v[128:131], v155, s[44:45] offset:128
	v_ashrrev_i32_e32 v153, 31, v152
	v_lshlrev_b64 v[158:159], 12, v[152:153]
	v_max_f32_e32 v153, 0xc2a00000, v160
	v_max_f32_e32 v155, 0xc2a00000, v161
	v_max_f32_e32 v160, 0xc2a00000, v166
	v_max_f32_e32 v161, 0xc2a00000, v167
	v_max_f32_e32 v166, 0xc2a00000, v168
	v_max_f32_e32 v167, 0xc2a00000, v169
	v_max_f32_e32 v168, 0xc2a00000, v170
	v_max_f32_e32 v169, 0xc2a00000, v171
	v_mul_f32_e32 v153, 0xbfb8aa3b, v153
	v_mul_f32_e32 v155, 0xbfb8aa3b, v155
	v_mul_f32_e32 v168, 0xbfb8aa3b, v168
	v_mul_f32_e32 v169, 0xbfb8aa3b, v169
	v_exp_f32_e32 v153, v153
	v_exp_f32_e32 v155, v155
	v_mul_f32_e32 v160, 0xbfb8aa3b, v160
	v_mul_f32_e32 v161, 0xbfb8aa3b, v161
	v_exp_f32_e32 v168, v168
	v_exp_f32_e32 v169, v169
	v_exp_f32_e32 v160, v160
	v_exp_f32_e32 v161, v161
	v_mul_f32_e32 v120, v120, v154
	v_max_f32_e32 v120, 0xc2a00000, v120
	v_add_f32_e32 v153, 1.0, v153
	v_add_f32_e32 v155, 1.0, v155
	v_mul_f32_e32 v121, v121, v154
	v_lshlrev_b32_e32 v114, 1, v177
	v_mul_f32_e32 v166, 0xbfb8aa3b, v166
	v_mul_f32_e32 v167, 0xbfb8aa3b, v167
	v_lshl_add_u64 v[158:159], s[42:43], 0, v[158:159]
	v_add_f32_e32 v168, 1.0, v168
	v_add_f32_e32 v169, 1.0, v169
	v_rcp_f32_e32 v153, v153
	v_rcp_f32_e32 v181, v155
	v_mul_f32_e32 v120, 0xbfb8aa3b, v120
	v_max_f32_e32 v121, 0xc2a00000, v121
	v_exp_f32_e32 v170, v166
	v_exp_f32_e32 v171, v167
	v_lshl_add_u64 v[166:167], v[158:159], 0, v[114:115]
	v_add_f32_e32 v158, 1.0, v160
	v_add_f32_e32 v159, 1.0, v161
	v_rcp_f32_e32 v168, v168
	v_rcp_f32_e32 v182, v169
	v_exp_f32_e32 v120, v120
	v_mul_f32_e32 v121, 0xbfb8aa3b, v121
	v_rcp_f32_e32 v158, v158
	v_rcp_f32_e32 v159, v159
	v_exp_f32_e32 v121, v121
	v_add_f32_e32 v120, 1.0, v120
	v_rcp_f32_e32 v120, v120
	v_mul_f32_e32 v116, v116, v154
	v_add_f32_e32 v121, 1.0, v121
	v_rcp_f32_e32 v121, v121
	v_add_f32_e32 v160, 1.0, v170
	v_add_f32_e32 v161, 1.0, v171
	v_max_f32_e32 v116, 0xc2a00000, v116
	v_mul_f32_e32 v117, v117, v154
	v_rcp_f32_e32 v160, v160
	v_rcp_f32_e32 v161, v161
	v_mul_f32_e32 v116, 0xbfb8aa3b, v116
	v_max_f32_e32 v117, 0xc2a00000, v117
	v_exp_f32_e32 v116, v116
	v_mul_f32_e32 v117, 0xbfb8aa3b, v117
	v_exp_f32_e32 v117, v117
	s_mov_b64 s[14:15], 0x80000
	v_add_f32_e32 v116, 1.0, v116
	v_rcp_f32_e32 v116, v116
	v_add_f32_e32 v117, 1.0, v117
	s_waitcnt vmcnt(0)
	v_sub_f32_e32 v180, 1.0, v136
	v_sub_f32_e32 v179, 1.0, v137
	v_sub_f32_e32 v169, 1.0, v134
	v_sub_f32_e32 v155, 1.0, v135
	v_fma_f32 v153, v180, v153, v136
	v_fma_f32 v181, v179, v181, v137
	v_sub_f32_e32 v178, 1.0, v138
	v_sub_f32_e32 v177, 1.0, v139
	v_fma_f32 v168, v169, v168, v134
	v_fma_f32 v182, v155, v182, v135
	v_log_f32_e32 v153, v153
	v_log_f32_e32 v181, v181
	v_fma_f32 v158, v178, v158, v138
	v_fma_f32 v159, v177, v159, v139
	v_log_f32_e32 v168, v168
	v_log_f32_e32 v182, v182
	v_log_f32_e32 v158, v158
	v_log_f32_e32 v159, v159
	v_cvt_pk_f16_f32 v194, v153, v181
	v_sub_f32_e32 v153, 1.0, v128
	v_cvt_pk_f16_f32 v197, v168, v182
	v_fma_f32 v120, v153, v120, v128
	v_sub_f32_e32 v168, 1.0, v129
	v_cvt_pk_f16_f32 v195, v158, v159
	v_log_f32_e32 v158, v120
	v_fma_f32 v120, v168, v121, v129
	v_log_f32_e32 v159, v120
	v_mul_f32_e32 v120, v122, v154
	v_max_f32_e32 v120, 0xc2a00000, v120
	v_mul_f32_e32 v121, v123, v154
	v_mul_f32_e32 v120, 0xbfb8aa3b, v120
	v_max_f32_e32 v121, 0xc2a00000, v121
	v_exp_f32_e32 v120, v120
	v_mul_f32_e32 v121, 0xbfb8aa3b, v121
	v_exp_f32_e32 v122, v121
	v_sub_f32_e32 v171, 1.0, v132
	v_sub_f32_e32 v170, 1.0, v133
	v_add_f32_e32 v120, 1.0, v120
	v_fma_f32 v160, v171, v160, v132
	v_fma_f32 v161, v170, v161, v133
	v_rcp_f32_e32 v120, v120
	v_add_f32_e32 v122, 1.0, v122
	v_log_f32_e32 v160, v160
	v_log_f32_e32 v161, v161
	v_rcp_f32_e32 v123, v122
	v_sub_f32_e32 v121, 1.0, v130
	v_rcp_f32_e32 v117, v117
	v_fma_f32 v120, v121, v120, v130
	v_sub_f32_e32 v122, 1.0, v131
	v_cvt_pk_f16_f32 v196, v160, v161
	v_log_f32_e32 v160, v120
	v_fma_f32 v120, v122, v123, v131
	v_sub_f32_e32 v123, 1.0, v124
	v_log_f32_e32 v161, v120
	v_fma_f32 v116, v123, v116, v124
	v_sub_f32_e32 v120, 1.0, v125
	v_log_f32_e32 v181, v116
	v_fma_f32 v116, v120, v117, v125
	v_log_f32_e32 v182, v116
	v_mul_f32_e32 v116, v118, v154
	v_max_f32_e32 v116, 0xc2a00000, v116
	v_mul_f32_e32 v117, v119, v154
	v_mul_f32_e32 v116, 0xbfb8aa3b, v116
	v_max_f32_e32 v117, 0xc2a00000, v117
	v_exp_f32_e32 v116, v116
	v_mul_f32_e32 v117, 0xbfb8aa3b, v117
	v_exp_f32_e32 v117, v117
	v_sub_f32_e32 v118, 1.0, v126
	v_add_f32_e32 v116, 1.0, v116
	v_rcp_f32_e32 v116, v116
	v_add_f32_e32 v117, 1.0, v117
	v_rcp_f32_e32 v117, v117
	v_sub_f32_e32 v119, 1.0, v127
	v_fma_f32 v116, v118, v116, v126
	v_log_f32_e32 v154, v116
	v_fma_f32 v116, v119, v117, v127
	v_log_f32_e32 v183, v116
	ds_read2_b32 v[116:117], v176 offset0:16 offset1:32
	ds_bpermute_b32 v232, v244, v194
	ds_bpermute_b32 v233, v244, v195
	ds_bpermute_b32 v234, v244, v196
	ds_bpermute_b32 v235, v244, v197
	ds_bpermute_b32 v236, v244, v166
	s_waitcnt lgkmcnt(0)
	v_mul_f32_e32 v106, v106, v116
	v_max_f32_e32 v106, 0xc2a00000, v106
	v_mul_f32_e32 v106, 0xbfb8aa3b, v106
	v_exp_f32_e32 v106, v106
	v_mul_f32_e32 v110, v110, v116
	v_max_f32_e32 v110, 0xc2a00000, v110
	v_mul_f32_e32 v111, v111, v116
	v_mul_f32_e32 v110, 0xbfb8aa3b, v110
	v_max_f32_e32 v111, 0xc2a00000, v111
	v_mul_f32_e32 v107, v107, v116
	v_exp_f32_e32 v110, v110
	v_mul_f32_e32 v111, 0xbfb8aa3b, v111
	v_add_f32_e32 v106, 1.0, v106
	v_max_f32_e32 v107, 0xc2a00000, v107
	v_exp_f32_e32 v111, v111
	v_rcp_f32_e32 v106, v106
	v_mul_f32_e32 v107, 0xbfb8aa3b, v107
	v_exp_f32_e32 v107, v107
	v_cvt_pk_f16_f32 v194, v158, v159
	v_or_b32_e32 v158, 16, v152
	v_add_f32_e32 v110, 1.0, v110
	v_mul_f32_e32 v112, v112, v116
	v_mul_f32_e32 v113, v113, v116
	v_cvt_pk_f16_f32 v197, v154, v183
	v_ashrrev_i32_e32 v159, 31, v158
	v_rcp_f32_e32 v154, v110
	v_add_f32_e32 v110, 1.0, v111
	v_max_f32_e32 v112, 0xc2a00000, v112
	v_max_f32_e32 v113, 0xc2a00000, v113
	v_fma_f32 v106, v171, v106, v132
	v_cvt_pk_f16_f32 v195, v160, v161
	v_rcp_f32_e32 v160, v110
	v_lshlrev_b64 v[110:111], 12, v[158:159]
	v_mul_f32_e32 v112, 0xbfb8aa3b, v112
	v_mul_f32_e32 v113, 0xbfb8aa3b, v113
	v_log_f32_e32 v159, v106
	v_add_f32_e32 v106, 1.0, v107
	v_mul_f32_e32 v107, v108, v116
	v_exp_f32_e32 v112, v112
	v_exp_f32_e32 v113, v113
	v_max_f32_e32 v107, 0xc2a00000, v107
	v_mul_f32_e32 v108, v109, v116
	v_mul_f32_e32 v107, 0xbfb8aa3b, v107
	v_max_f32_e32 v108, 0xc2a00000, v108
	v_exp_f32_e32 v107, v107
	v_mul_f32_e32 v108, 0xbfb8aa3b, v108
	v_exp_f32_e32 v108, v108
	v_add_f32_e32 v112, 1.0, v112
	v_add_f32_e32 v113, 1.0, v113
	v_rcp_f32_e32 v112, v112
	v_rcp_f32_e32 v113, v113
	v_mul_f32_e32 v98, v98, v116
	v_rcp_f32_e32 v106, v106
	v_add_f32_e32 v107, 1.0, v107
	v_max_f32_e32 v98, 0xc2a00000, v98
	v_rcp_f32_e32 v107, v107
	v_add_f32_e32 v108, 1.0, v108
	v_mul_f32_e32 v98, 0xbfb8aa3b, v98
	v_rcp_f32_e32 v108, v108
	v_exp_f32_e32 v98, v98
	v_fma_f32 v112, v178, v112, v138
	v_fma_f32 v113, v177, v113, v139
	v_log_f32_e32 v112, v112
	v_log_f32_e32 v113, v113
	v_fma_f32 v106, v170, v106, v133
	v_log_f32_e32 v109, v106
	v_fma_f32 v106, v169, v107, v134
	v_mul_f32_e32 v102, v102, v116
	v_mul_f32_e32 v99, v99, v116
	v_fma_f32 v154, v180, v154, v136
	v_fma_f32 v158, v179, v160, v137
	v_log_f32_e32 v160, v106
	v_fma_f32 v106, v155, v108, v135
	v_max_f32_e32 v102, 0xc2a00000, v102
	v_add_f32_e32 v98, 1.0, v98
	v_max_f32_e32 v99, 0xc2a00000, v99
	v_log_f32_e32 v154, v154
	v_log_f32_e32 v158, v158
	v_log_f32_e32 v161, v106
	v_mul_f32_e32 v102, 0xbfb8aa3b, v102
	v_rcp_f32_e32 v98, v98
	v_mul_f32_e32 v99, 0xbfb8aa3b, v99
	v_cvt_pk_f16_f32 v107, v112, v113
	v_exp_f32_e32 v112, v102
	v_mul_f32_e32 v102, v103, v116
	v_exp_f32_e32 v99, v99
	v_max_f32_e32 v102, 0xc2a00000, v102
	v_lshl_add_u64 v[110:111], s[42:43], 0, v[110:111]
	v_mul_f32_e32 v102, 0xbfb8aa3b, v102
	v_cvt_pk_f16_f32 v106, v154, v158
	v_cvt_pk_f16_f32 v108, v159, v109
	v_cvt_pk_f16_f32 v109, v160, v161
	v_exp_f32_e32 v113, v102
	v_lshl_add_u64 v[102:103], v[110:111], 0, v[114:115]
	v_fma_f32 v98, v123, v98, v124
	s_waitcnt lgkmcnt(0)
	v_subrev_u32_e32 v236, s82, v236
	global_store_dwordx4 v236, v[232:235], s[82:83]
	ds_bpermute_b32 v238, v244, v106
	ds_bpermute_b32 v239, v244, v107
	ds_bpermute_b32 v240, v244, v108
	ds_bpermute_b32 v241, v244, v109
	ds_bpermute_b32 v242, v244, v102
	v_mul_f32_e32 v104, v104, v116
	v_mul_f32_e32 v105, v105, v116
	v_log_f32_e32 v108, v98
	v_add_f32_e32 v98, 1.0, v99
	v_mul_f32_e32 v99, v100, v116
	v_max_f32_e32 v99, 0xc2a00000, v99
	v_mul_f32_e32 v100, v101, v116
	v_max_f32_e32 v104, 0xc2a00000, v104
	v_max_f32_e32 v105, 0xc2a00000, v105
	v_mul_f32_e32 v99, 0xbfb8aa3b, v99
	v_max_f32_e32 v100, 0xc2a00000, v100
	v_mul_f32_e32 v104, 0xbfb8aa3b, v104
	v_mul_f32_e32 v105, 0xbfb8aa3b, v105
	v_exp_f32_e32 v99, v99
	v_mul_f32_e32 v100, 0xbfb8aa3b, v100
	v_exp_f32_e32 v104, v104
	v_exp_f32_e32 v105, v105
	v_exp_f32_e32 v100, v100
	v_rcp_f32_e32 v98, v98
	v_add_f32_e32 v99, 1.0, v99
	v_add_f32_e32 v110, 1.0, v112
	v_add_f32_e32 v111, 1.0, v113
	v_add_f32_e32 v104, 1.0, v104
	v_add_f32_e32 v105, 1.0, v105
	v_rcp_f32_e32 v99, v99
	v_add_f32_e32 v100, 1.0, v100
	v_rcp_f32_e32 v110, v110
	v_rcp_f32_e32 v111, v111
	v_rcp_f32_e32 v104, v104
	v_rcp_f32_e32 v105, v105
	v_rcp_f32_e32 v100, v100
	v_mul_f32_e32 v90, v90, v117
	v_fma_f32 v98, v120, v98, v125
	v_mul_f32_e32 v94, v94, v117
	v_max_f32_e32 v90, 0xc2a00000, v90
	v_log_f32_e32 v101, v98
	v_fma_f32 v98, v118, v99, v126
	v_max_f32_e32 v94, 0xc2a00000, v94
	v_mul_f32_e32 v90, 0xbfb8aa3b, v90
	v_fma_f32 v106, v153, v110, v128
	v_fma_f32 v107, v168, v111, v129
	v_fma_f32 v104, v121, v104, v130
	v_fma_f32 v105, v122, v105, v131
	v_log_f32_e32 v109, v98
	v_fma_f32 v98, v119, v100, v127
	v_mul_f32_e32 v94, 0xbfb8aa3b, v94
	v_exp_f32_e32 v90, v90
	v_log_f32_e32 v106, v106
	v_log_f32_e32 v107, v107
	v_log_f32_e32 v104, v104
	v_log_f32_e32 v105, v105
	v_log_f32_e32 v110, v98
	v_exp_f32_e32 v94, v94
	v_mul_f32_e32 v95, v95, v117
	v_max_f32_e32 v95, 0xc2a00000, v95
	v_mul_f32_e32 v91, v91, v117
	v_mul_f32_e32 v95, 0xbfb8aa3b, v95
	v_add_f32_e32 v90, 1.0, v90
	v_max_f32_e32 v91, 0xc2a00000, v91
	v_cvt_pk_f16_f32 v98, v106, v107
	v_cvt_pk_f16_f32 v99, v104, v105
	v_cvt_pk_f16_f32 v100, v108, v101
	v_cvt_pk_f16_f32 v101, v109, v110
	v_exp_f32_e32 v95, v95
	v_add_f32_e32 v94, 1.0, v94
	v_rcp_f32_e32 v90, v90
	v_mul_f32_e32 v91, 0xbfb8aa3b, v91
	s_waitcnt lgkmcnt(0)
	v_subrev_u32_e32 v242, s82, v242
	global_store_dwordx4 v242, v[238:241], s[82:83]
	ds_bpermute_b32 v232, v244, v98
	ds_bpermute_b32 v233, v244, v99
	ds_bpermute_b32 v234, v244, v100
	ds_bpermute_b32 v235, v244, v101
	ds_bpermute_b32 v236, v244, v102
	v_exp_f32_e32 v91, v91
	v_fma_f32 v90, v171, v90, v132
	v_rcp_f32_e32 v100, v94
	v_or_b32_e32 v98, 32, v152
	v_ashrrev_i32_e32 v99, 31, v98
	v_add_f32_e32 v94, 1.0, v95
	v_rcp_f32_e32 v101, v94
	v_lshlrev_b64 v[94:95], 12, v[98:99]
	v_fma_f32 v98, v180, v100, v136
	v_log_f32_e32 v100, v90
	v_add_f32_e32 v90, 1.0, v91
	v_mul_f32_e32 v91, v92, v117
	v_mul_f32_e32 v96, v96, v117
	v_mul_f32_e32 v97, v97, v117
	v_max_f32_e32 v91, 0xc2a00000, v91
	v_mul_f32_e32 v92, v93, v117
	v_max_f32_e32 v96, 0xc2a00000, v96
	v_max_f32_e32 v97, 0xc2a00000, v97
	v_mul_f32_e32 v91, 0xbfb8aa3b, v91
	v_max_f32_e32 v92, 0xc2a00000, v92
	v_mul_f32_e32 v96, 0xbfb8aa3b, v96
	v_mul_f32_e32 v97, 0xbfb8aa3b, v97
	v_exp_f32_e32 v91, v91
	v_mul_f32_e32 v92, 0xbfb8aa3b, v92
	v_exp_f32_e32 v96, v96
	v_exp_f32_e32 v97, v97
	v_exp_f32_e32 v92, v92
	v_mul_f32_e32 v82, v82, v117
	v_rcp_f32_e32 v90, v90
	v_add_f32_e32 v91, 1.0, v91
	v_max_f32_e32 v82, 0xc2a00000, v82
	v_add_f32_e32 v96, 1.0, v96
	v_add_f32_e32 v97, 1.0, v97
	v_rcp_f32_e32 v91, v91
	v_add_f32_e32 v92, 1.0, v92
	v_mul_f32_e32 v82, 0xbfb8aa3b, v82
	v_rcp_f32_e32 v96, v96
	v_rcp_f32_e32 v97, v97
	v_rcp_f32_e32 v92, v92
	v_exp_f32_e32 v82, v82
	v_fma_f32 v90, v170, v90, v133
	v_log_f32_e32 v93, v90
	v_fma_f32 v90, v169, v91, v134
	v_mul_f32_e32 v83, v83, v117
	v_fma_f32 v99, v179, v101, v137
	v_fma_f32 v96, v178, v96, v138
	v_fma_f32 v97, v177, v97, v139
	v_log_f32_e32 v101, v90
	v_fma_f32 v90, v155, v92, v135
	v_add_f32_e32 v82, 1.0, v82
	v_max_f32_e32 v83, 0xc2a00000, v83
	v_log_f32_e32 v98, v98
	v_log_f32_e32 v99, v99
	v_log_f32_e32 v96, v96
	v_log_f32_e32 v97, v97
	v_log_f32_e32 v102, v90
	v_rcp_f32_e32 v82, v82
	v_mul_f32_e32 v83, 0xbfb8aa3b, v83
	v_exp_f32_e32 v83, v83
	v_lshl_add_u64 v[94:95], s[42:43], 0, v[94:95]
	v_cvt_pk_f16_f32 v90, v98, v99
	v_cvt_pk_f16_f32 v91, v96, v97
	v_cvt_pk_f16_f32 v92, v100, v93
	v_cvt_pk_f16_f32 v93, v101, v102
	v_lshl_add_u64 v[94:95], v[94:95], 0, v[114:115]
	v_fma_f32 v82, v123, v82, v124
	s_waitcnt lgkmcnt(0)
	v_subrev_u32_e32 v236, s82, v236
	global_store_dwordx4 v236, v[232:235], s[82:83] offset:64
	ds_bpermute_b32 v238, v244, v90
	ds_bpermute_b32 v239, v244, v91
	ds_bpermute_b32 v240, v244, v92
	ds_bpermute_b32 v241, v244, v93
	ds_bpermute_b32 v242, v244, v94
	v_mul_f32_e32 v86, v86, v117
	v_mul_f32_e32 v87, v87, v117
	v_log_f32_e32 v90, v82
	v_add_f32_e32 v82, 1.0, v83
	v_mul_f32_e32 v83, v84, v117
	v_max_f32_e32 v83, 0xc2a00000, v83
	v_mul_f32_e32 v84, v85, v117
	v_mul_f32_e32 v83, 0xbfb8aa3b, v83
	v_max_f32_e32 v84, 0xc2a00000, v84
	v_exp_f32_e32 v83, v83
	v_mul_f32_e32 v84, 0xbfb8aa3b, v84
	v_exp_f32_e32 v84, v84
	v_rcp_f32_e32 v82, v82
	v_add_f32_e32 v83, 1.0, v83
	v_rcp_f32_e32 v83, v83
	v_add_f32_e32 v84, 1.0, v84
	v_rcp_f32_e32 v84, v84
	v_mul_f32_e32 v88, v88, v117
	v_mul_f32_e32 v89, v89, v117
	v_max_f32_e32 v86, 0xc2a00000, v86
	v_max_f32_e32 v87, 0xc2a00000, v87
	v_max_f32_e32 v88, 0xc2a00000, v88
	v_max_f32_e32 v89, 0xc2a00000, v89
	v_fma_f32 v82, v120, v82, v125
	v_mul_f32_e32 v86, 0xbfb8aa3b, v86
	v_mul_f32_e32 v87, 0xbfb8aa3b, v87
	v_mul_f32_e32 v88, 0xbfb8aa3b, v88
	v_mul_f32_e32 v89, 0xbfb8aa3b, v89
	v_log_f32_e32 v91, v82
	v_fma_f32 v82, v118, v83, v126
	v_exp_f32_e32 v86, v86
	v_exp_f32_e32 v87, v87
	v_exp_f32_e32 v88, v88
	v_exp_f32_e32 v89, v89
	v_log_f32_e32 v92, v82
	v_fma_f32 v82, v119, v84, v127
	v_log_f32_e32 v93, v82
	ds_read2_b32 v[82:83], v176 offset0:48 offset1:128
	v_add_f32_e32 v86, 1.0, v86
	v_add_f32_e32 v87, 1.0, v87
	v_add_f32_e32 v88, 1.0, v88
	v_add_f32_e32 v89, 1.0, v89
	v_rcp_f32_e32 v86, v86
	v_rcp_f32_e32 v87, v87
	v_rcp_f32_e32 v88, v88
	v_rcp_f32_e32 v89, v89
	s_waitcnt lgkmcnt(0)
	v_mul_f32_e32 v74, v74, v82
	v_mul_f32_e32 v78, v78, v82
	v_max_f32_e32 v74, 0xc2a00000, v74
	v_max_f32_e32 v78, 0xc2a00000, v78
	v_mul_f32_e32 v74, 0xbfb8aa3b, v74
	v_fma_f32 v86, v153, v86, v128
	v_fma_f32 v87, v168, v87, v129
	v_fma_f32 v88, v121, v88, v130
	v_fma_f32 v89, v122, v89, v131
	v_mul_f32_e32 v78, 0xbfb8aa3b, v78
	v_exp_f32_e32 v74, v74
	v_log_f32_e32 v86, v86
	v_log_f32_e32 v87, v87
	v_log_f32_e32 v88, v88
	v_log_f32_e32 v89, v89
	v_exp_f32_e32 v78, v78
	v_mul_f32_e32 v79, v79, v82
	v_max_f32_e32 v79, 0xc2a00000, v79
	v_mul_f32_e32 v75, v75, v82
	v_mul_f32_e32 v79, 0xbfb8aa3b, v79
	v_add_f32_e32 v74, 1.0, v74
	v_max_f32_e32 v75, 0xc2a00000, v75
	v_cvt_pk_f16_f32 v84, v86, v87
	v_cvt_pk_f16_f32 v85, v88, v89
	v_cvt_pk_f16_f32 v86, v90, v91
	v_cvt_pk_f16_f32 v87, v92, v93
	v_exp_f32_e32 v79, v79
	v_add_f32_e32 v78, 1.0, v78
	v_rcp_f32_e32 v74, v74
	v_mul_f32_e32 v75, 0xbfb8aa3b, v75
	s_waitcnt lgkmcnt(0)
	v_subrev_u32_e32 v242, s82, v242
	global_store_dwordx4 v242, v[238:241], s[82:83]
	ds_bpermute_b32 v232, v244, v84
	ds_bpermute_b32 v233, v244, v85
	ds_bpermute_b32 v234, v244, v86
	ds_bpermute_b32 v235, v244, v87
	ds_bpermute_b32 v236, v244, v94
	v_exp_f32_e32 v75, v75
	v_mul_f32_e32 v80, v80, v82
	v_rcp_f32_e32 v86, v78
	v_or_b32_e32 v84, 48, v152
	v_mul_f32_e32 v81, v81, v82
	v_ashrrev_i32_e32 v85, 31, v84
	v_add_f32_e32 v78, 1.0, v79
	v_max_f32_e32 v80, 0xc2a00000, v80
	v_max_f32_e32 v81, 0xc2a00000, v81
	v_fma_f32 v74, v171, v74, v132
	v_rcp_f32_e32 v87, v78
	v_lshlrev_b64 v[78:79], 12, v[84:85]
	v_fma_f32 v84, v180, v86, v136
	v_mul_f32_e32 v80, 0xbfb8aa3b, v80
	v_mul_f32_e32 v81, 0xbfb8aa3b, v81
	v_log_f32_e32 v86, v74
	v_add_f32_e32 v74, 1.0, v75
	v_mul_f32_e32 v75, v76, v82
	v_exp_f32_e32 v80, v80
	v_exp_f32_e32 v81, v81
	v_max_f32_e32 v75, 0xc2a00000, v75
	v_mul_f32_e32 v76, v77, v82
	v_mul_f32_e32 v75, 0xbfb8aa3b, v75
	v_max_f32_e32 v76, 0xc2a00000, v76
	v_exp_f32_e32 v75, v75
	v_mul_f32_e32 v76, 0xbfb8aa3b, v76
	v_exp_f32_e32 v76, v76
	v_add_f32_e32 v80, 1.0, v80
	v_add_f32_e32 v81, 1.0, v81
	v_rcp_f32_e32 v80, v80
	v_rcp_f32_e32 v81, v81
	v_mul_f32_e32 v66, v66, v82
	v_rcp_f32_e32 v74, v74
	v_add_f32_e32 v75, 1.0, v75
	v_max_f32_e32 v66, 0xc2a00000, v66
	v_rcp_f32_e32 v75, v75
	v_add_f32_e32 v76, 1.0, v76
	v_mul_f32_e32 v66, 0xbfb8aa3b, v66
	v_rcp_f32_e32 v76, v76
	v_exp_f32_e32 v66, v66
	v_fma_f32 v80, v178, v80, v138
	v_fma_f32 v81, v177, v81, v139
	v_log_f32_e32 v80, v80
	v_log_f32_e32 v81, v81
	v_fma_f32 v74, v170, v74, v133
	v_log_f32_e32 v77, v74
	v_fma_f32 v74, v169, v75, v134
	v_mul_f32_e32 v70, v70, v82
	v_mul_f32_e32 v67, v67, v82
	v_fma_f32 v85, v179, v87, v137
	v_log_f32_e32 v87, v74
	v_fma_f32 v74, v155, v76, v135
	v_max_f32_e32 v70, 0xc2a00000, v70
	v_add_f32_e32 v66, 1.0, v66
	v_max_f32_e32 v67, 0xc2a00000, v67
	v_log_f32_e32 v84, v84
	v_log_f32_e32 v85, v85
	v_log_f32_e32 v88, v74
	v_mul_f32_e32 v70, 0xbfb8aa3b, v70
	v_rcp_f32_e32 v66, v66
	v_mul_f32_e32 v67, 0xbfb8aa3b, v67
	v_cvt_pk_f16_f32 v75, v80, v81
	v_exp_f32_e32 v80, v70
	v_mul_f32_e32 v70, v71, v82
	v_exp_f32_e32 v67, v67
	v_max_f32_e32 v70, 0xc2a00000, v70
	v_lshl_add_u64 v[78:79], s[42:43], 0, v[78:79]
	v_mul_f32_e32 v70, 0xbfb8aa3b, v70
	v_cvt_pk_f16_f32 v74, v84, v85
	v_cvt_pk_f16_f32 v76, v86, v77
	v_cvt_pk_f16_f32 v77, v87, v88
	v_exp_f32_e32 v81, v70
	v_lshl_add_u64 v[70:71], v[78:79], 0, v[114:115]
	v_fma_f32 v66, v123, v66, v124
	s_waitcnt lgkmcnt(0)
	v_subrev_u32_e32 v236, s82, v236
	global_store_dwordx4 v236, v[232:235], s[82:83] offset:64
	ds_bpermute_b32 v238, v244, v74
	ds_bpermute_b32 v239, v244, v75
	ds_bpermute_b32 v240, v244, v76
	ds_bpermute_b32 v241, v244, v77
	ds_bpermute_b32 v242, v244, v70
	v_mul_f32_e32 v72, v72, v82
	v_mul_f32_e32 v73, v73, v82
	v_log_f32_e32 v76, v66
	v_add_f32_e32 v66, 1.0, v67
	v_mul_f32_e32 v67, v68, v82
	v_max_f32_e32 v67, 0xc2a00000, v67
	v_mul_f32_e32 v68, v69, v82
	v_max_f32_e32 v72, 0xc2a00000, v72
	v_max_f32_e32 v73, 0xc2a00000, v73
	v_mul_f32_e32 v67, 0xbfb8aa3b, v67
	v_max_f32_e32 v68, 0xc2a00000, v68
	v_mul_f32_e32 v72, 0xbfb8aa3b, v72
	v_mul_f32_e32 v73, 0xbfb8aa3b, v73
	v_exp_f32_e32 v67, v67
	v_mul_f32_e32 v68, 0xbfb8aa3b, v68
	v_exp_f32_e32 v72, v72
	v_exp_f32_e32 v73, v73
	v_exp_f32_e32 v68, v68
	v_mul_f32_e32 v58, v58, v83
	v_rcp_f32_e32 v66, v66
	v_add_f32_e32 v67, 1.0, v67
	v_max_f32_e32 v58, 0xc2a00000, v58
	v_add_f32_e32 v78, 1.0, v80
	v_add_f32_e32 v79, 1.0, v81
	v_add_f32_e32 v72, 1.0, v72
	v_add_f32_e32 v73, 1.0, v73
	v_rcp_f32_e32 v67, v67
	v_add_f32_e32 v68, 1.0, v68
	v_mul_f32_e32 v58, 0xbfb8aa3b, v58
	v_rcp_f32_e32 v78, v78
	v_rcp_f32_e32 v79, v79
	v_rcp_f32_e32 v72, v72
	v_rcp_f32_e32 v73, v73
	v_rcp_f32_e32 v68, v68
	v_exp_f32_e32 v58, v58
	v_fma_f32 v66, v120, v66, v125
	v_log_f32_e32 v69, v66
	v_fma_f32 v66, v118, v67, v126
	v_mul_f32_e32 v59, v59, v83
	v_fma_f32 v74, v153, v78, v128
	v_fma_f32 v75, v168, v79, v129
	v_fma_f32 v72, v121, v72, v130
	v_fma_f32 v73, v122, v73, v131
	v_log_f32_e32 v77, v66
	v_fma_f32 v66, v119, v68, v127
	v_add_f32_e32 v58, 1.0, v58
	v_max_f32_e32 v59, 0xc2a00000, v59
	v_log_f32_e32 v74, v74
	v_log_f32_e32 v75, v75
	v_log_f32_e32 v72, v72
	v_log_f32_e32 v73, v73
	v_log_f32_e32 v78, v66
	v_rcp_f32_e32 v58, v58
	v_mul_f32_e32 v59, 0xbfb8aa3b, v59
	v_exp_f32_e32 v59, v59
	v_mul_f32_e32 v64, v64, v83
	v_mul_f32_e32 v65, v65, v83
	v_max_f32_e32 v64, 0xc2a00000, v64
	v_max_f32_e32 v65, 0xc2a00000, v65
	v_cvt_pk_f16_f32 v66, v74, v75
	v_cvt_pk_f16_f32 v67, v72, v73
	v_cvt_pk_f16_f32 v68, v76, v69
	v_mul_f32_e32 v62, v62, v83
	v_mul_f32_e32 v63, v63, v83
	v_cvt_pk_f16_f32 v69, v77, v78
	v_mul_f32_e32 v64, 0xbfb8aa3b, v64
	v_mul_f32_e32 v65, 0xbfb8aa3b, v65
	v_fma_f32 v58, v171, v58, v132
	v_max_f32_e32 v62, 0xc2a00000, v62
	v_max_f32_e32 v63, 0xc2a00000, v63
	s_waitcnt lgkmcnt(0)
	v_subrev_u32_e32 v242, s82, v242
	global_store_dwordx4 v242, v[238:241], s[82:83]
	ds_bpermute_b32 v232, v244, v66
	ds_bpermute_b32 v233, v244, v67
	ds_bpermute_b32 v234, v244, v68
	ds_bpermute_b32 v235, v244, v69
	ds_bpermute_b32 v236, v244, v70
	v_exp_f32_e32 v64, v64
	v_exp_f32_e32 v65, v65
	v_log_f32_e32 v66, v58
	v_add_f32_e32 v58, 1.0, v59
	v_mul_f32_e32 v59, v60, v83
	v_mul_f32_e32 v62, 0xbfb8aa3b, v62
	v_mul_f32_e32 v63, 0xbfb8aa3b, v63
	v_max_f32_e32 v59, 0xc2a00000, v59
	v_mul_f32_e32 v60, v61, v83
	v_exp_f32_e32 v62, v62
	v_exp_f32_e32 v63, v63
	v_mul_f32_e32 v59, 0xbfb8aa3b, v59
	v_max_f32_e32 v60, 0xc2a00000, v60
	v_exp_f32_e32 v59, v59
	v_mul_f32_e32 v60, 0xbfb8aa3b, v60
	v_add_f32_e32 v64, 1.0, v64
	v_add_f32_e32 v65, 1.0, v65
	v_exp_f32_e32 v60, v60
	v_rcp_f32_e32 v64, v64
	v_rcp_f32_e32 v65, v65
	v_add_f32_e32 v62, 1.0, v62
	v_add_f32_e32 v63, 1.0, v63
	v_mul_f32_e32 v50, v50, v83
	v_rcp_f32_e32 v62, v62
	v_rcp_f32_e32 v63, v63
	v_rcp_f32_e32 v58, v58
	v_add_f32_e32 v59, 1.0, v59
	v_max_f32_e32 v50, 0xc2a00000, v50
	v_rcp_f32_e32 v59, v59
	v_add_f32_e32 v60, 1.0, v60
	v_mul_f32_e32 v50, 0xbfb8aa3b, v50
	v_fma_f32 v64, v178, v64, v138
	v_fma_f32 v65, v177, v65, v139
	v_rcp_f32_e32 v60, v60
	v_exp_f32_e32 v50, v50
	v_log_f32_e32 v64, v64
	v_log_f32_e32 v65, v65
	v_fma_f32 v62, v180, v62, v136
	v_fma_f32 v63, v179, v63, v137
	v_fma_f32 v58, v170, v58, v133
	v_mul_f32_e32 v54, v54, v83
	v_log_f32_e32 v62, v62
	v_log_f32_e32 v63, v63
	v_log_f32_e32 v61, v58
	v_fma_f32 v58, v169, v59, v134
	v_max_f32_e32 v54, 0xc2a00000, v54
	v_mul_f32_e32 v51, v51, v83
	v_log_f32_e32 v67, v58
	v_fma_f32 v58, v155, v60, v135
	v_mul_f32_e32 v54, 0xbfb8aa3b, v54
	v_add_f32_e32 v50, 1.0, v50
	v_max_f32_e32 v51, 0xc2a00000, v51
	v_log_f32_e32 v68, v58
	v_cvt_pk_f16_f32 v59, v64, v65
	v_exp_f32_e32 v64, v54
	v_mul_f32_e32 v54, v55, v83
	v_rcp_f32_e32 v50, v50
	v_mul_f32_e32 v51, 0xbfb8aa3b, v51
	v_max_f32_e32 v54, 0xc2a00000, v54
	v_exp_f32_e32 v51, v51
	v_cvt_pk_f16_f32 v58, v62, v63
	v_lshl_add_u64 v[62:63], v[166:167], 0, s[14:15]
	v_mul_f32_e32 v54, 0xbfb8aa3b, v54
	s_mov_b32 s14, 0x80000
	v_exp_f32_e32 v65, v54
	v_add_co_u32_e32 v54, vcc, s14, v166
	v_cvt_pk_f16_f32 v60, v66, v61
	v_cvt_pk_f16_f32 v61, v67, v68
	v_addc_co_u32_e32 v55, vcc, 0, v167, vcc
	v_fma_f32 v50, v123, v50, v124
	s_waitcnt lgkmcnt(0)
	v_subrev_u32_e32 v236, s82, v236
	global_store_dwordx4 v236, v[232:235], s[82:83] offset:64
	ds_bpermute_b32 v238, v244, v58
	ds_bpermute_b32 v239, v244, v59
	ds_bpermute_b32 v240, v244, v60
	ds_bpermute_b32 v241, v244, v61
	ds_bpermute_b32 v242, v244, v54
	v_mul_f32_e32 v56, v56, v83
	v_mul_f32_e32 v57, v57, v83
	v_log_f32_e32 v58, v50
	v_add_f32_e32 v50, 1.0, v51
	v_mul_f32_e32 v51, v52, v83
	v_max_f32_e32 v51, 0xc2a00000, v51
	v_mul_f32_e32 v51, 0xbfb8aa3b, v51
	v_exp_f32_e32 v51, v51
	v_rcp_f32_e32 v50, v50
	v_mul_f32_e32 v52, v53, v83
	v_max_f32_e32 v56, 0xc2a00000, v56
	v_add_f32_e32 v51, 1.0, v51
	v_rcp_f32_e32 v51, v51
	v_fma_f32 v50, v120, v50, v125
	v_log_f32_e32 v59, v50
	v_max_f32_e32 v57, 0xc2a00000, v57
	v_fma_f32 v50, v118, v51, v126
	v_log_f32_e32 v60, v50
	ds_read2_b32 v[50:51], v176 offset0:144 offset1:160
	v_max_f32_e32 v52, 0xc2a00000, v52
	v_mul_f32_e32 v56, 0xbfb8aa3b, v56
	v_mul_f32_e32 v57, 0xbfb8aa3b, v57
	v_mul_f32_e32 v52, 0xbfb8aa3b, v52
	v_exp_f32_e32 v56, v56
	v_exp_f32_e32 v57, v57
	v_exp_f32_e32 v52, v52
	s_waitcnt lgkmcnt(0)
	v_mul_f32_e32 v42, v42, v50
	v_max_f32_e32 v42, 0xc2a00000, v42
	v_add_f32_e32 v64, 1.0, v64
	v_add_f32_e32 v65, 1.0, v65
	v_add_f32_e32 v56, 1.0, v56
	v_add_f32_e32 v57, 1.0, v57
	v_add_f32_e32 v52, 1.0, v52
	v_mul_f32_e32 v42, 0xbfb8aa3b, v42
	v_rcp_f32_e32 v64, v64
	v_rcp_f32_e32 v65, v65
	v_rcp_f32_e32 v56, v56
	v_rcp_f32_e32 v57, v57
	v_rcp_f32_e32 v52, v52
	v_exp_f32_e32 v42, v42
	v_mul_f32_e32 v43, v43, v50
	v_fma_f32 v54, v153, v64, v128
	v_fma_f32 v55, v168, v65, v129
	v_fma_f32 v56, v121, v56, v130
	v_fma_f32 v57, v122, v57, v131
	v_fma_f32 v52, v119, v52, v127
	v_add_f32_e32 v42, 1.0, v42
	v_max_f32_e32 v43, 0xc2a00000, v43
	v_log_f32_e32 v54, v54
	v_log_f32_e32 v55, v55
	v_log_f32_e32 v56, v56
	v_log_f32_e32 v57, v57
	v_log_f32_e32 v61, v52
	v_rcp_f32_e32 v42, v42
	v_mul_f32_e32 v43, 0xbfb8aa3b, v43
	v_exp_f32_e32 v43, v43
	v_mul_f32_e32 v48, v48, v50
	v_mul_f32_e32 v49, v49, v50
	v_max_f32_e32 v48, 0xc2a00000, v48
	v_max_f32_e32 v49, 0xc2a00000, v49
	v_cvt_pk_f16_f32 v52, v54, v55
	v_cvt_pk_f16_f32 v53, v56, v57
	v_cvt_pk_f16_f32 v54, v58, v59
	v_mul_f32_e32 v46, v46, v50
	v_mul_f32_e32 v47, v47, v50
	v_cvt_pk_f16_f32 v55, v60, v61
	v_mul_f32_e32 v48, 0xbfb8aa3b, v48
	v_mul_f32_e32 v49, 0xbfb8aa3b, v49
	v_fma_f32 v42, v171, v42, v132
	v_max_f32_e32 v46, 0xc2a00000, v46
	v_max_f32_e32 v47, 0xc2a00000, v47
	s_waitcnt lgkmcnt(0)
	v_subrev_u32_e32 v242, s82, v242
	global_store_dwordx4 v242, v[238:241], s[82:83]
	ds_bpermute_b32 v232, v244, v52
	ds_bpermute_b32 v233, v244, v53
	ds_bpermute_b32 v234, v244, v54
	ds_bpermute_b32 v235, v244, v55
	ds_bpermute_b32 v236, v244, v62
	v_exp_f32_e32 v48, v48
	v_exp_f32_e32 v49, v49
	v_log_f32_e32 v52, v42
	v_add_f32_e32 v42, 1.0, v43
	v_mul_f32_e32 v43, v44, v50
	v_mul_f32_e32 v46, 0xbfb8aa3b, v46
	v_mul_f32_e32 v47, 0xbfb8aa3b, v47
	v_max_f32_e32 v43, 0xc2a00000, v43
	v_mul_f32_e32 v44, v45, v50
	v_exp_f32_e32 v46, v46
	v_exp_f32_e32 v47, v47
	v_mul_f32_e32 v43, 0xbfb8aa3b, v43
	v_max_f32_e32 v44, 0xc2a00000, v44
	v_exp_f32_e32 v43, v43
	v_mul_f32_e32 v44, 0xbfb8aa3b, v44
	v_add_f32_e32 v48, 1.0, v48
	v_add_f32_e32 v49, 1.0, v49
	v_exp_f32_e32 v44, v44
	v_rcp_f32_e32 v48, v48
	v_rcp_f32_e32 v49, v49
	v_add_f32_e32 v46, 1.0, v46
	v_add_f32_e32 v47, 1.0, v47
	v_mul_f32_e32 v34, v34, v50
	v_rcp_f32_e32 v46, v46
	v_rcp_f32_e32 v47, v47
	v_rcp_f32_e32 v42, v42
	v_add_f32_e32 v43, 1.0, v43
	v_max_f32_e32 v34, 0xc2a00000, v34
	v_rcp_f32_e32 v43, v43
	v_add_f32_e32 v44, 1.0, v44
	v_mul_f32_e32 v34, 0xbfb8aa3b, v34
	v_fma_f32 v48, v178, v48, v138
	v_fma_f32 v49, v177, v49, v139
	v_rcp_f32_e32 v44, v44
	v_exp_f32_e32 v34, v34
	v_log_f32_e32 v48, v48
	v_log_f32_e32 v49, v49
	v_fma_f32 v46, v180, v46, v136
	v_fma_f32 v47, v179, v47, v137
	v_fma_f32 v42, v170, v42, v133
	v_mul_f32_e32 v38, v38, v50
	v_log_f32_e32 v46, v46
	v_log_f32_e32 v47, v47
	v_log_f32_e32 v45, v42
	v_fma_f32 v42, v169, v43, v134
	v_max_f32_e32 v38, 0xc2a00000, v38
	v_mul_f32_e32 v35, v35, v50
	v_log_f32_e32 v53, v42
	v_fma_f32 v42, v155, v44, v135
	v_mul_f32_e32 v38, 0xbfb8aa3b, v38
	v_add_f32_e32 v34, 1.0, v34
	v_max_f32_e32 v35, 0xc2a00000, v35
	v_log_f32_e32 v54, v42
	v_cvt_pk_f16_f32 v43, v48, v49
	v_exp_f32_e32 v48, v38
	v_mul_f32_e32 v38, v39, v50
	v_rcp_f32_e32 v34, v34
	v_mul_f32_e32 v35, 0xbfb8aa3b, v35
	s_mov_b64 s[14:15], 0x90000
	v_max_f32_e32 v38, 0xc2a00000, v38
	v_exp_f32_e32 v35, v35
	v_cvt_pk_f16_f32 v42, v46, v47
	v_lshl_add_u64 v[46:47], v[166:167], 0, s[14:15]
	v_mul_f32_e32 v38, 0xbfb8aa3b, v38
	s_mov_b32 s14, 0x90000
	v_exp_f32_e32 v49, v38
	v_add_co_u32_e32 v38, vcc, s14, v166
	v_cvt_pk_f16_f32 v44, v52, v45
	v_cvt_pk_f16_f32 v45, v53, v54
	v_addc_co_u32_e32 v39, vcc, 0, v167, vcc
	v_fma_f32 v34, v123, v34, v124
	s_waitcnt lgkmcnt(0)
	v_subrev_u32_e32 v236, s82, v236
	global_store_dwordx4 v236, v[232:235], s[82:83] offset:64
	ds_bpermute_b32 v238, v244, v42
	ds_bpermute_b32 v239, v244, v43
	ds_bpermute_b32 v240, v244, v44
	ds_bpermute_b32 v241, v244, v45
	ds_bpermute_b32 v242, v244, v38
	v_mul_f32_e32 v40, v40, v50
	v_mul_f32_e32 v41, v41, v50
	v_log_f32_e32 v42, v34
	v_add_f32_e32 v34, 1.0, v35
	v_mul_f32_e32 v35, v36, v50
	v_max_f32_e32 v35, 0xc2a00000, v35
	v_mul_f32_e32 v36, v37, v50
	v_max_f32_e32 v40, 0xc2a00000, v40
	v_max_f32_e32 v41, 0xc2a00000, v41
	v_mul_f32_e32 v35, 0xbfb8aa3b, v35
	v_max_f32_e32 v36, 0xc2a00000, v36
	v_mul_f32_e32 v40, 0xbfb8aa3b, v40
	v_mul_f32_e32 v41, 0xbfb8aa3b, v41
	v_exp_f32_e32 v35, v35
	v_mul_f32_e32 v36, 0xbfb8aa3b, v36
	v_exp_f32_e32 v40, v40
	v_exp_f32_e32 v41, v41
	v_exp_f32_e32 v36, v36
	v_mul_f32_e32 v26, v26, v51
	v_rcp_f32_e32 v34, v34
	v_add_f32_e32 v35, 1.0, v35
	v_max_f32_e32 v26, 0xc2a00000, v26
	v_add_f32_e32 v48, 1.0, v48
	v_add_f32_e32 v49, 1.0, v49
	v_add_f32_e32 v40, 1.0, v40
	v_add_f32_e32 v41, 1.0, v41
	v_rcp_f32_e32 v35, v35
	v_add_f32_e32 v36, 1.0, v36
	v_mul_f32_e32 v26, 0xbfb8aa3b, v26
	v_rcp_f32_e32 v48, v48
	v_rcp_f32_e32 v49, v49
	v_rcp_f32_e32 v40, v40
	v_rcp_f32_e32 v41, v41
	v_rcp_f32_e32 v36, v36
	v_exp_f32_e32 v26, v26
	v_fma_f32 v34, v120, v34, v125
	v_log_f32_e32 v37, v34
	v_fma_f32 v34, v118, v35, v126
	v_mul_f32_e32 v27, v27, v51
	v_fma_f32 v38, v153, v48, v128
	v_fma_f32 v39, v168, v49, v129
	v_fma_f32 v40, v121, v40, v130
	v_fma_f32 v41, v122, v41, v131
	v_log_f32_e32 v43, v34
	v_fma_f32 v34, v119, v36, v127
	v_add_f32_e32 v26, 1.0, v26
	v_max_f32_e32 v27, 0xc2a00000, v27
	v_log_f32_e32 v38, v38
	v_log_f32_e32 v39, v39
	v_log_f32_e32 v40, v40
	v_log_f32_e32 v41, v41
	v_log_f32_e32 v44, v34
	v_rcp_f32_e32 v26, v26
	v_mul_f32_e32 v27, 0xbfb8aa3b, v27
	v_exp_f32_e32 v27, v27
	v_mul_f32_e32 v32, v32, v51
	v_mul_f32_e32 v33, v33, v51
	v_max_f32_e32 v32, 0xc2a00000, v32
	v_max_f32_e32 v33, 0xc2a00000, v33
	v_cvt_pk_f16_f32 v34, v38, v39
	v_cvt_pk_f16_f32 v35, v40, v41
	v_cvt_pk_f16_f32 v36, v42, v37
	v_mul_f32_e32 v30, v30, v51
	v_mul_f32_e32 v31, v31, v51
	v_cvt_pk_f16_f32 v37, v43, v44
	v_mul_f32_e32 v32, 0xbfb8aa3b, v32
	v_mul_f32_e32 v33, 0xbfb8aa3b, v33
	v_fma_f32 v26, v171, v26, v132
	v_max_f32_e32 v30, 0xc2a00000, v30
	v_max_f32_e32 v31, 0xc2a00000, v31
	s_waitcnt lgkmcnt(0)
	v_subrev_u32_e32 v242, s82, v242
	global_store_dwordx4 v242, v[238:241], s[82:83]
	ds_bpermute_b32 v232, v244, v34
	ds_bpermute_b32 v233, v244, v35
	ds_bpermute_b32 v234, v244, v36
	ds_bpermute_b32 v235, v244, v37
	ds_bpermute_b32 v236, v244, v46
	v_exp_f32_e32 v32, v32
	v_exp_f32_e32 v33, v33
	v_log_f32_e32 v34, v26
	v_add_f32_e32 v26, 1.0, v27
	v_mul_f32_e32 v27, v28, v51
	v_mul_f32_e32 v30, 0xbfb8aa3b, v30
	v_mul_f32_e32 v31, 0xbfb8aa3b, v31
	v_max_f32_e32 v27, 0xc2a00000, v27
	v_mul_f32_e32 v28, v29, v51
	v_exp_f32_e32 v30, v30
	v_exp_f32_e32 v31, v31
	v_mul_f32_e32 v27, 0xbfb8aa3b, v27
	v_max_f32_e32 v28, 0xc2a00000, v28
	v_exp_f32_e32 v27, v27
	v_mul_f32_e32 v28, 0xbfb8aa3b, v28
	v_add_f32_e32 v32, 1.0, v32
	v_add_f32_e32 v33, 1.0, v33
	v_exp_f32_e32 v28, v28
	v_rcp_f32_e32 v32, v32
	v_rcp_f32_e32 v33, v33
	v_add_f32_e32 v30, 1.0, v30
	v_add_f32_e32 v31, 1.0, v31
	v_mul_f32_e32 v18, v18, v51
	v_rcp_f32_e32 v30, v30
	v_rcp_f32_e32 v31, v31
	v_rcp_f32_e32 v26, v26
	v_add_f32_e32 v27, 1.0, v27
	v_max_f32_e32 v18, 0xc2a00000, v18
	v_rcp_f32_e32 v27, v27
	v_add_f32_e32 v28, 1.0, v28
	v_mul_f32_e32 v18, 0xbfb8aa3b, v18
	v_fma_f32 v32, v178, v32, v138
	v_fma_f32 v33, v177, v33, v139
	v_rcp_f32_e32 v28, v28
	v_exp_f32_e32 v18, v18
	v_log_f32_e32 v32, v32
	v_log_f32_e32 v33, v33
	v_fma_f32 v30, v180, v30, v136
	v_fma_f32 v31, v179, v31, v137
	v_fma_f32 v26, v170, v26, v133
	v_mul_f32_e32 v22, v22, v51
	v_log_f32_e32 v30, v30
	v_log_f32_e32 v31, v31
	v_log_f32_e32 v29, v26
	v_fma_f32 v26, v169, v27, v134
	v_max_f32_e32 v22, 0xc2a00000, v22
	v_mul_f32_e32 v19, v19, v51
	v_log_f32_e32 v35, v26
	v_fma_f32 v26, v155, v28, v135
	v_mul_f32_e32 v22, 0xbfb8aa3b, v22
	v_add_f32_e32 v18, 1.0, v18
	v_max_f32_e32 v19, 0xc2a00000, v19
	v_log_f32_e32 v36, v26
	v_cvt_pk_f16_f32 v27, v32, v33
	v_exp_f32_e32 v32, v22
	v_mul_f32_e32 v22, v23, v51
	v_rcp_f32_e32 v18, v18
	v_mul_f32_e32 v19, 0xbfb8aa3b, v19
	s_mov_b64 s[14:15], 0xa0000
	v_max_f32_e32 v22, 0xc2a00000, v22
	v_exp_f32_e32 v19, v19
	v_cvt_pk_f16_f32 v26, v30, v31
	v_lshl_add_u64 v[30:31], v[166:167], 0, s[14:15]
	v_mul_f32_e32 v22, 0xbfb8aa3b, v22
	s_mov_b32 s14, 0xa0000
	v_exp_f32_e32 v33, v22
	v_add_co_u32_e32 v22, vcc, s14, v166
	v_cvt_pk_f16_f32 v28, v34, v29
	v_cvt_pk_f16_f32 v29, v35, v36
	v_addc_co_u32_e32 v23, vcc, 0, v167, vcc
	v_fma_f32 v18, v123, v18, v124
	s_waitcnt lgkmcnt(0)
	v_subrev_u32_e32 v236, s82, v236
	global_store_dwordx4 v236, v[232:235], s[82:83] offset:64
	ds_bpermute_b32 v238, v244, v26
	ds_bpermute_b32 v239, v244, v27
	ds_bpermute_b32 v240, v244, v28
	ds_bpermute_b32 v241, v244, v29
	ds_bpermute_b32 v242, v244, v22
	v_mul_f32_e32 v24, v24, v51
	v_mul_f32_e32 v25, v25, v51
	v_log_f32_e32 v26, v18
	v_add_f32_e32 v18, 1.0, v19
	v_mul_f32_e32 v19, v20, v51
	v_max_f32_e32 v19, 0xc2a00000, v19
	v_mul_f32_e32 v20, v21, v51
	ds_read_b32 v28, v176 offset:704
	v_max_f32_e32 v24, 0xc2a00000, v24
	v_max_f32_e32 v25, 0xc2a00000, v25
	v_mul_f32_e32 v19, 0xbfb8aa3b, v19
	v_max_f32_e32 v20, 0xc2a00000, v20
	v_mul_f32_e32 v24, 0xbfb8aa3b, v24
	v_mul_f32_e32 v25, 0xbfb8aa3b, v25
	v_exp_f32_e32 v19, v19
	v_mul_f32_e32 v20, 0xbfb8aa3b, v20
	v_exp_f32_e32 v24, v24
	v_exp_f32_e32 v25, v25
	v_exp_f32_e32 v20, v20
	s_waitcnt lgkmcnt(0)
	v_mul_f32_e32 v10, v10, v28
	v_rcp_f32_e32 v18, v18
	v_add_f32_e32 v19, 1.0, v19
	v_max_f32_e32 v10, 0xc2a00000, v10
	v_add_f32_e32 v32, 1.0, v32
	v_add_f32_e32 v33, 1.0, v33
	v_add_f32_e32 v24, 1.0, v24
	v_add_f32_e32 v25, 1.0, v25
	v_rcp_f32_e32 v19, v19
	v_add_f32_e32 v20, 1.0, v20
	v_mul_f32_e32 v10, 0xbfb8aa3b, v10
	v_rcp_f32_e32 v32, v32
	v_rcp_f32_e32 v33, v33
	v_rcp_f32_e32 v24, v24
	v_rcp_f32_e32 v25, v25
	v_rcp_f32_e32 v20, v20
	v_exp_f32_e32 v10, v10
	v_fma_f32 v18, v120, v18, v125
	v_log_f32_e32 v21, v18
	v_fma_f32 v18, v118, v19, v126
	v_mul_f32_e32 v11, v11, v28
	v_fma_f32 v22, v153, v32, v128
	v_fma_f32 v23, v168, v33, v129
	v_fma_f32 v24, v121, v24, v130
	v_fma_f32 v25, v122, v25, v131
	v_log_f32_e32 v27, v18
	v_fma_f32 v18, v119, v20, v127
	v_add_f32_e32 v10, 1.0, v10
	v_max_f32_e32 v11, 0xc2a00000, v11
	v_log_f32_e32 v22, v22
	v_log_f32_e32 v23, v23
	v_log_f32_e32 v24, v24
	v_log_f32_e32 v25, v25
	v_log_f32_e32 v29, v18
	v_rcp_f32_e32 v10, v10
	v_mul_f32_e32 v11, 0xbfb8aa3b, v11
	v_mul_f32_e32 v14, v14, v28
	v_mul_f32_e32 v15, v15, v28
	v_exp_f32_e32 v11, v11
	v_max_f32_e32 v14, 0xc2a00000, v14
	v_max_f32_e32 v15, 0xc2a00000, v15
	v_mul_f32_e32 v14, 0xbfb8aa3b, v14
	v_mul_f32_e32 v15, 0xbfb8aa3b, v15
	v_cvt_pk_f16_f32 v18, v22, v23
	v_cvt_pk_f16_f32 v19, v24, v25
	v_cvt_pk_f16_f32 v20, v26, v21
	v_exp_f32_e32 v14, v14
	v_exp_f32_e32 v15, v15
	v_cvt_pk_f16_f32 v21, v27, v29
	v_fma_f32 v10, v171, v10, v132
	s_waitcnt lgkmcnt(0)
	v_subrev_u32_e32 v242, s82, v242
	global_store_dwordx4 v242, v[238:241], s[82:83]
	ds_bpermute_b32 v232, v244, v18
	ds_bpermute_b32 v233, v244, v19
	ds_bpermute_b32 v234, v244, v20
	ds_bpermute_b32 v235, v244, v21
	ds_bpermute_b32 v236, v244, v30
	v_add_f32_e32 v14, 1.0, v14
	v_add_f32_e32 v15, 1.0, v15
	v_log_f32_e32 v18, v10
	v_add_f32_e32 v10, 1.0, v11
	v_mul_f32_e32 v11, v12, v28
	v_max_f32_e32 v11, 0xc2a00000, v11
	v_mul_f32_e32 v11, 0xbfb8aa3b, v11
	v_exp_f32_e32 v11, v11
	v_rcp_f32_e32 v14, v14
	v_rcp_f32_e32 v15, v15
	v_mul_f32_e32 v16, v16, v28
	v_mul_f32_e32 v17, v17, v28
	v_rcp_f32_e32 v10, v10
	v_mul_f32_e32 v12, v13, v28
	v_add_f32_e32 v11, 1.0, v11
	v_fma_f32 v14, v180, v14, v136
	v_fma_f32 v15, v179, v15, v137
	v_max_f32_e32 v16, 0xc2a00000, v16
	v_max_f32_e32 v17, 0xc2a00000, v17
	v_max_f32_e32 v12, 0xc2a00000, v12
	v_rcp_f32_e32 v11, v11
	v_log_f32_e32 v14, v14
	v_mul_f32_e32 v16, 0xbfb8aa3b, v16
	v_mul_f32_e32 v17, 0xbfb8aa3b, v17
	v_log_f32_e32 v15, v15
	v_mul_f32_e32 v12, 0xbfb8aa3b, v12
	v_exp_f32_e32 v16, v16
	v_exp_f32_e32 v17, v17
	v_exp_f32_e32 v12, v12
	v_mul_f32_e32 v6, v6, v28
	v_fma_f32 v10, v170, v10, v133
	v_max_f32_e32 v6, 0xc2a00000, v6
	v_log_f32_e32 v13, v10
	v_fma_f32 v10, v169, v11, v134
	v_mul_f32_e32 v6, 0xbfb8aa3b, v6
	v_log_f32_e32 v19, v10
	v_cvt_pk_f16_f32 v10, v14, v15
	v_exp_f32_e32 v14, v6
	v_mul_f32_e32 v6, v7, v28
	v_mul_f32_e32 v8, v8, v28
	v_mul_f32_e32 v9, v9, v28
	v_mul_f32_e32 v2, v2, v28
	v_mul_f32_e32 v3, v3, v28
	v_mul_f32_e32 v4, v4, v28
	v_mul_f32_e32 v5, v5, v28
	v_add_f32_e32 v16, 1.0, v16
	v_add_f32_e32 v17, 1.0, v17
	v_add_f32_e32 v12, 1.0, v12
	v_max_f32_e32 v6, 0xc2a00000, v6
	v_max_f32_e32 v8, 0xc2a00000, v8
	v_max_f32_e32 v9, 0xc2a00000, v9
	v_max_f32_e32 v2, 0xc2a00000, v2
	v_max_f32_e32 v3, 0xc2a00000, v3
	v_max_f32_e32 v4, 0xc2a00000, v4
	v_max_f32_e32 v5, 0xc2a00000, v5
	v_rcp_f32_e32 v16, v16
	v_rcp_f32_e32 v17, v17
	v_rcp_f32_e32 v12, v12
	v_mul_f32_e32 v6, 0xbfb8aa3b, v6
	v_mul_f32_e32 v8, 0xbfb8aa3b, v8
	v_mul_f32_e32 v9, 0xbfb8aa3b, v9
	v_mul_f32_e32 v2, 0xbfb8aa3b, v2
	v_mul_f32_e32 v3, 0xbfb8aa3b, v3
	v_mul_f32_e32 v4, 0xbfb8aa3b, v4
	v_mul_f32_e32 v5, 0xbfb8aa3b, v5
	v_exp_f32_e32 v15, v6
	v_exp_f32_e32 v8, v8
	v_exp_f32_e32 v9, v9
	v_exp_f32_e32 v2, v2
	v_exp_f32_e32 v3, v3
	v_exp_f32_e32 v4, v4
	v_exp_f32_e32 v5, v5
	v_fma_f32 v16, v178, v16, v138
	v_fmac_f32_e32 v139, v177, v17
	v_fmac_f32_e32 v135, v155, v12
	v_log_f32_e32 v16, v16
	v_log_f32_e32 v17, v139
	v_log_f32_e32 v20, v135
	v_add_f32_e32 v14, 1.0, v14
	v_add_f32_e32 v15, 1.0, v15
	v_add_f32_e32 v8, 1.0, v8
	v_add_f32_e32 v9, 1.0, v9
	v_add_f32_e32 v2, 1.0, v2
	v_add_f32_e32 v3, 1.0, v3
	v_add_f32_e32 v4, 1.0, v4
	v_add_f32_e32 v5, 1.0, v5
	s_mov_b64 s[14:15], 0xb0000
	v_rcp_f32_e32 v14, v14
	v_rcp_f32_e32 v15, v15
	v_rcp_f32_e32 v8, v8
	v_rcp_f32_e32 v9, v9
	v_rcp_f32_e32 v2, v2
	v_rcp_f32_e32 v3, v3
	v_rcp_f32_e32 v4, v4
	v_rcp_f32_e32 v5, v5
	v_lshl_add_u64 v[136:137], v[166:167], 0, s[14:15]
	s_mov_b32 s14, 0xb0000
	v_add_co_u32_e32 v6, vcc, s14, v166
	v_cvt_pk_f16_f32 v11, v16, v17
	v_cvt_pk_f16_f32 v12, v18, v13
	v_cvt_pk_f16_f32 v13, v19, v20
	v_addc_co_u32_e32 v7, vcc, 0, v167, vcc
	s_waitcnt lgkmcnt(0)
	v_subrev_u32_e32 v236, s82, v236
	global_store_dwordx4 v236, v[232:235], s[82:83] offset:64
	ds_bpermute_b32 v238, v244, v10
	ds_bpermute_b32 v239, v244, v11
	ds_bpermute_b32 v240, v244, v12
	ds_bpermute_b32 v241, v244, v13
	ds_bpermute_b32 v242, v244, v6
	v_fma_f32 v6, v153, v14, v128
	v_fma_f32 v7, v168, v15, v129
	v_fma_f32 v8, v121, v8, v130
	v_fmac_f32_e32 v131, v122, v9
	v_fma_f32 v2, v123, v2, v124
	v_fma_f32 v3, v120, v3, v125
	v_fma_f32 v4, v118, v4, v126
	v_fmac_f32_e32 v127, v119, v5
	v_log_f32_e32 v6, v6
	v_log_f32_e32 v7, v7
	v_log_f32_e32 v8, v8
	v_log_f32_e32 v9, v131
	v_log_f32_e32 v2, v2
	v_log_f32_e32 v3, v3
	v_log_f32_e32 v4, v4
	v_log_f32_e32 v5, v127
	v_cvt_pk_f16_f32 v196, v181, v182
	v_cvt_pk_f16_f32 v132, v6, v7
	v_cvt_pk_f16_f32 v133, v8, v9
	v_cvt_pk_f16_f32 v134, v2, v3
	v_cvt_pk_f16_f32 v135, v4, v5
	s_waitcnt lgkmcnt(0)
	v_subrev_u32_e32 v242, s82, v242
	global_store_dwordx4 v242, v[238:241], s[82:83]
	ds_bpermute_b32 v232, v244, v194
	ds_bpermute_b32 v233, v244, v195
	ds_bpermute_b32 v234, v244, v196
	ds_bpermute_b32 v235, v244, v197
	ds_bpermute_b32 v236, v244, v166
	s_andn2_b64 vcc, exec, s[38:39]
	s_mov_b64 s[28:29], -1
	s_waitcnt lgkmcnt(0)
	v_subrev_u32_e32 v236, s82, v236
	global_store_dwordx4 v236, v[232:235], s[82:83] offset:64
	ds_bpermute_b32 v238, v244, v132
	ds_bpermute_b32 v239, v244, v133
	ds_bpermute_b32 v240, v244, v134
	ds_bpermute_b32 v241, v244, v135
	ds_bpermute_b32 v242, v244, v136
	s_waitcnt lgkmcnt(0)
	v_subrev_u32_e32 v242, s82, v242
	global_store_dwordx4 v242, v[238:241], s[82:83] offset:64
	s_cbranch_vccnz .LBB0_338

.LBB0_509:
	s_ashr_i32 s57, s56, 31
	s_lshl_b64 s[14:15], s[56:57], 25
	s_add_u32 s14, s24, s14
	s_addc_u32 s15, s37, s15
	v_lshlrev_b32_e32 v114, 1, v177
	v_ashrrev_i32_e32 v153, 31, v152
	v_lshl_add_u64 v[132:133], s[14:15], 0, v[114:115]
	v_lshlrev_b64 v[136:137], 12, v[152:153]
	v_mov_b32_e32 v155, v154
	v_lshl_add_u64 v[136:137], v[132:133], 0, v[136:137]
	v_cvt_pk_bf16_f32 v166, v166, v167
	v_cvt_pk_bf16_f32 v167, v134, v135
	v_cvt_pk_bf16_f32 v168, v168, v169
	v_cvt_pk_bf16_f32 v169, v138, v139
	v_mov_b32_e32 v158, v154
	v_mov_b32_e32 v159, v154
	v_cndmask_b32_e64 v114, 0, 1, s[54:55]
	ds_bpermute_b32 v232, v244, v166
	ds_bpermute_b32 v233, v244, v167
	ds_bpermute_b32 v234, v244, v168
	ds_bpermute_b32 v235, v244, v169
	ds_bpermute_b32 v236, v244, v136
	v_pk_mul_f32 v[138:139], v[122:123], v[158:159]
	v_pk_mul_f32 v[134:135], v[120:121], v[154:155]
	v_pk_mul_f32 v[166:167], v[118:119], v[158:159]
	v_cmp_ne_u32_e64 s[40:41], 1, v114
	s_andn2_b64 vcc, exec, s[54:55]
	v_pk_mul_f32 v[168:169], v[116:117], v[154:155]
	s_waitcnt lgkmcnt(0)
	v_subrev_u32_e32 v236, s82, v236
	global_store_dwordx4 v236, v[232:235], s[82:83]
	s_cbranch_vccnz .LBB0_511
	v_max_f32_e32 v114, v134, v134
	v_max_f32_e32 v134, 0xc2a00000, v114
	v_max_f32_e32 v114, v168, v168
	v_max_f32_e32 v158, 0xc2a00000, v114
	v_mul_f32_e32 v114, 0xbfb8aa3b, v134
	v_exp_f32_e32 v114, v114
	v_mul_f32_e32 v155, 0xbfb8aa3b, v158
	v_exp_f32_e32 v155, v155
	v_max_f32_e32 v135, v135, v135
	v_add_f32_e32 v114, 1.0, v114
	v_rcp_f32_e32 v160, v114
	v_add_f32_e32 v114, 1.0, v155
	v_max_f32_e32 v135, 0xc2a00000, v135
	v_max_f32_e32 v155, v169, v169
	v_max_f32_e32 v159, 0xc2a00000, v155
	v_mul_f32_e32 v155, 0xbfb8aa3b, v135
	v_exp_f32_e32 v155, v155
	v_mul_f32_e32 v161, 0xbfb8aa3b, v159
	v_exp_f32_e32 v169, v161
	v_max_f32_e32 v138, v138, v138
	v_rcp_f32_e32 v168, v114
	v_add_f32_e32 v114, 1.0, v155
	v_max_f32_e32 v138, 0xc2a00000, v138
	v_max_f32_e32 v155, v166, v166
	v_max_f32_e32 v166, 0xc2a00000, v155
	v_mul_f32_e32 v155, 0xbfb8aa3b, v138
	v_exp_f32_e32 v155, v155
	v_rcp_f32_e32 v161, v114
	v_add_f32_e32 v114, 1.0, v169
	v_mul_f32_e32 v169, 0xbfb8aa3b, v166
	v_exp_f32_e32 v171, v169
	v_max_f32_e32 v139, v139, v139
	v_rcp_f32_e32 v169, v114
	v_add_f32_e32 v114, 1.0, v155
	v_max_f32_e32 v139, 0xc2a00000, v139
	v_max_f32_e32 v155, v167, v167
	v_max_f32_e32 v167, 0xc2a00000, v155
	v_mul_f32_e32 v155, 0xbfb8aa3b, v139
	v_rcp_f32_e32 v170, v114
	v_add_f32_e32 v114, 1.0, v171
	v_exp_f32_e32 v155, v155
	v_mul_f32_e32 v171, 0xbfb8aa3b, v167
	v_exp_f32_e32 v179, v171
	v_rcp_f32_e32 v178, v114
	v_add_f32_e32 v114, 1.0, v155
	v_rcp_f32_e32 v171, v114
	v_add_f32_e32 v114, 1.0, v179
	v_rcp_f32_e32 v179, v114
	v_pk_mul_f32 v[134:135], v[134:135], v[160:161]
	v_pk_mul_f32 v[138:139], v[138:139], v[170:171]
	v_pk_mul_f32 v[168:169], v[158:159], v[168:169]
	v_pk_mul_f32 v[166:167], v[166:167], v[178:179]

.LBB0_541:
	s_and_b64 vcc, exec, s[40:41]
	s_cbranch_vccz .LBB0_540
	v_lshlrev_b32_e32 v155, 2, v177
	global_load_dwordx4 v[136:139], v155, s[42:43]
	global_load_dwordx4 v[132:135], v155, s[42:43] offset:16
	s_waitcnt lgkmcnt(0)
	v_mul_f32_e32 v160, v128, v154
	v_mul_f32_e32 v161, v129, v154
	v_mul_f32_e32 v166, v130, v154
	v_mul_f32_e32 v167, v131, v154
	v_mul_f32_e32 v168, v124, v154
	v_mul_f32_e32 v169, v125, v154
	v_mul_f32_e32 v170, v126, v154
	v_mul_f32_e32 v171, v127, v154
	global_load_dwordx4 v[124:127], v155, s[42:43] offset:144
	global_load_dwordx4 v[128:131], v155, s[42:43] offset:128
	v_ashrrev_i32_e32 v153, 31, v152
	v_lshlrev_b64 v[158:159], 12, v[152:153]
	v_max_f32_e32 v153, 0xc2a00000, v160
	v_max_f32_e32 v155, 0xc2a00000, v161
	v_max_f32_e32 v160, 0xc2a00000, v166
	v_max_f32_e32 v161, 0xc2a00000, v167
	v_max_f32_e32 v166, 0xc2a00000, v168
	v_max_f32_e32 v167, 0xc2a00000, v169
	v_max_f32_e32 v168, 0xc2a00000, v170
	v_max_f32_e32 v169, 0xc2a00000, v171
	v_mul_f32_e32 v153, 0xbfb8aa3b, v153
	v_mul_f32_e32 v155, 0xbfb8aa3b, v155
	v_mul_f32_e32 v168, 0xbfb8aa3b, v168
	v_mul_f32_e32 v169, 0xbfb8aa3b, v169
	v_exp_f32_e32 v153, v153
	v_exp_f32_e32 v155, v155
	v_mul_f32_e32 v160, 0xbfb8aa3b, v160
	v_mul_f32_e32 v161, 0xbfb8aa3b, v161
	v_exp_f32_e32 v168, v168
	v_exp_f32_e32 v169, v169
	v_exp_f32_e32 v160, v160
	v_exp_f32_e32 v161, v161
	v_mul_f32_e32 v120, v120, v154
	v_max_f32_e32 v120, 0xc2a00000, v120
	v_add_f32_e32 v153, 1.0, v153
	v_add_f32_e32 v155, 1.0, v155
	v_mul_f32_e32 v121, v121, v154
	v_lshlrev_b32_e32 v114, 1, v177
	v_mul_f32_e32 v166, 0xbfb8aa3b, v166
	v_mul_f32_e32 v167, 0xbfb8aa3b, v167
	v_lshl_add_u64 v[158:159], s[26:27], 0, v[158:159]
	v_add_f32_e32 v168, 1.0, v168
	v_add_f32_e32 v169, 1.0, v169
	v_rcp_f32_e32 v153, v153
	v_rcp_f32_e32 v181, v155
	v_mul_f32_e32 v120, 0xbfb8aa3b, v120
	v_max_f32_e32 v121, 0xc2a00000, v121
	v_exp_f32_e32 v170, v166
	v_exp_f32_e32 v171, v167
	v_lshl_add_u64 v[166:167], v[158:159], 0, v[114:115]
	v_add_f32_e32 v158, 1.0, v160
	v_add_f32_e32 v159, 1.0, v161
	v_rcp_f32_e32 v168, v168
	v_rcp_f32_e32 v182, v169
	v_exp_f32_e32 v120, v120
	v_mul_f32_e32 v121, 0xbfb8aa3b, v121
	v_rcp_f32_e32 v158, v158
	v_rcp_f32_e32 v159, v159
	v_exp_f32_e32 v121, v121
	v_add_f32_e32 v120, 1.0, v120
	v_rcp_f32_e32 v120, v120
	v_mul_f32_e32 v116, v116, v154
	v_add_f32_e32 v121, 1.0, v121
	v_rcp_f32_e32 v121, v121
	v_add_f32_e32 v160, 1.0, v170
	v_add_f32_e32 v161, 1.0, v171
	v_max_f32_e32 v116, 0xc2a00000, v116
	v_mul_f32_e32 v117, v117, v154
	v_rcp_f32_e32 v160, v160
	v_rcp_f32_e32 v161, v161
	v_mul_f32_e32 v116, 0xbfb8aa3b, v116
	v_max_f32_e32 v117, 0xc2a00000, v117
	v_exp_f32_e32 v116, v116
	v_mul_f32_e32 v117, 0xbfb8aa3b, v117
	v_exp_f32_e32 v117, v117
	s_mov_b64 s[14:15], 0x80000
	v_add_f32_e32 v116, 1.0, v116
	v_rcp_f32_e32 v116, v116
	v_add_f32_e32 v117, 1.0, v117
	s_waitcnt vmcnt(0)
	v_sub_f32_e32 v180, 1.0, v136
	v_sub_f32_e32 v179, 1.0, v137
	v_sub_f32_e32 v169, 1.0, v134
	v_sub_f32_e32 v155, 1.0, v135
	v_fma_f32 v153, v180, v153, v136
	v_fma_f32 v181, v179, v181, v137
	v_sub_f32_e32 v178, 1.0, v138
	v_sub_f32_e32 v177, 1.0, v139
	v_fma_f32 v168, v169, v168, v134
	v_fma_f32 v182, v155, v182, v135
	v_log_f32_e32 v153, v153
	v_log_f32_e32 v181, v181
	v_fma_f32 v158, v178, v158, v138
	v_fma_f32 v159, v177, v159, v139
	v_log_f32_e32 v168, v168
	v_log_f32_e32 v182, v182
	v_log_f32_e32 v158, v158
	v_log_f32_e32 v159, v159
	v_cvt_pk_f16_f32 v194, v153, v181
	v_sub_f32_e32 v153, 1.0, v128
	v_cvt_pk_f16_f32 v197, v168, v182
	v_fma_f32 v120, v153, v120, v128
	v_sub_f32_e32 v168, 1.0, v129
	v_cvt_pk_f16_f32 v195, v158, v159
	v_log_f32_e32 v158, v120
	v_fma_f32 v120, v168, v121, v129
	v_log_f32_e32 v159, v120
	v_mul_f32_e32 v120, v122, v154
	v_max_f32_e32 v120, 0xc2a00000, v120
	v_mul_f32_e32 v121, v123, v154
	v_mul_f32_e32 v120, 0xbfb8aa3b, v120
	v_max_f32_e32 v121, 0xc2a00000, v121
	v_exp_f32_e32 v120, v120
	v_mul_f32_e32 v121, 0xbfb8aa3b, v121
	v_exp_f32_e32 v122, v121
	v_sub_f32_e32 v171, 1.0, v132
	v_sub_f32_e32 v170, 1.0, v133
	v_add_f32_e32 v120, 1.0, v120
	v_fma_f32 v160, v171, v160, v132
	v_fma_f32 v161, v170, v161, v133
	v_rcp_f32_e32 v120, v120
	v_add_f32_e32 v122, 1.0, v122
	v_log_f32_e32 v160, v160
	v_log_f32_e32 v161, v161
	v_rcp_f32_e32 v123, v122
	v_sub_f32_e32 v121, 1.0, v130
	v_rcp_f32_e32 v117, v117
	v_fma_f32 v120, v121, v120, v130
	v_sub_f32_e32 v122, 1.0, v131
	v_cvt_pk_f16_f32 v196, v160, v161
	v_log_f32_e32 v160, v120
	v_fma_f32 v120, v122, v123, v131
	v_sub_f32_e32 v123, 1.0, v124
	v_log_f32_e32 v161, v120
	v_fma_f32 v116, v123, v116, v124
	v_sub_f32_e32 v120, 1.0, v125
	v_log_f32_e32 v181, v116
	v_fma_f32 v116, v120, v117, v125
	v_log_f32_e32 v182, v116
	v_mul_f32_e32 v116, v118, v154
	v_max_f32_e32 v116, 0xc2a00000, v116
	v_mul_f32_e32 v117, v119, v154
	v_mul_f32_e32 v116, 0xbfb8aa3b, v116
	v_max_f32_e32 v117, 0xc2a00000, v117
	v_exp_f32_e32 v116, v116
	v_mul_f32_e32 v117, 0xbfb8aa3b, v117
	v_exp_f32_e32 v117, v117
	v_sub_f32_e32 v118, 1.0, v126
	v_add_f32_e32 v116, 1.0, v116
	v_rcp_f32_e32 v116, v116
	v_add_f32_e32 v117, 1.0, v117
	v_rcp_f32_e32 v117, v117
	v_sub_f32_e32 v119, 1.0, v127
	v_fma_f32 v116, v118, v116, v126
	v_log_f32_e32 v154, v116
	v_fma_f32 v116, v119, v117, v127
	v_log_f32_e32 v183, v116
	ds_read2_b32 v[116:117], v176 offset0:16 offset1:32
	ds_bpermute_b32 v232, v244, v194
	ds_bpermute_b32 v233, v244, v195
	ds_bpermute_b32 v234, v244, v196
	ds_bpermute_b32 v235, v244, v197
	ds_bpermute_b32 v236, v244, v166
	s_waitcnt lgkmcnt(0)
	v_mul_f32_e32 v106, v106, v116
	v_max_f32_e32 v106, 0xc2a00000, v106
	v_mul_f32_e32 v106, 0xbfb8aa3b, v106
	v_exp_f32_e32 v106, v106
	v_mul_f32_e32 v110, v110, v116
	v_max_f32_e32 v110, 0xc2a00000, v110
	v_mul_f32_e32 v111, v111, v116
	v_mul_f32_e32 v110, 0xbfb8aa3b, v110
	v_max_f32_e32 v111, 0xc2a00000, v111
	v_mul_f32_e32 v107, v107, v116
	v_exp_f32_e32 v110, v110
	v_mul_f32_e32 v111, 0xbfb8aa3b, v111
	v_add_f32_e32 v106, 1.0, v106
	v_max_f32_e32 v107, 0xc2a00000, v107
	v_exp_f32_e32 v111, v111
	v_rcp_f32_e32 v106, v106
	v_mul_f32_e32 v107, 0xbfb8aa3b, v107
	v_exp_f32_e32 v107, v107
	v_cvt_pk_f16_f32 v194, v158, v159
	v_or_b32_e32 v158, 16, v152
	v_add_f32_e32 v110, 1.0, v110
	v_mul_f32_e32 v112, v112, v116
	v_mul_f32_e32 v113, v113, v116
	v_cvt_pk_f16_f32 v197, v154, v183
	v_ashrrev_i32_e32 v159, 31, v158
	v_rcp_f32_e32 v154, v110
	v_add_f32_e32 v110, 1.0, v111
	v_max_f32_e32 v112, 0xc2a00000, v112
	v_max_f32_e32 v113, 0xc2a00000, v113
	v_fma_f32 v106, v171, v106, v132
	v_cvt_pk_f16_f32 v195, v160, v161
	v_rcp_f32_e32 v160, v110
	v_lshlrev_b64 v[110:111], 12, v[158:159]
	v_mul_f32_e32 v112, 0xbfb8aa3b, v112
	v_mul_f32_e32 v113, 0xbfb8aa3b, v113
	v_log_f32_e32 v159, v106
	v_add_f32_e32 v106, 1.0, v107
	v_mul_f32_e32 v107, v108, v116
	v_exp_f32_e32 v112, v112
	v_exp_f32_e32 v113, v113
	v_max_f32_e32 v107, 0xc2a00000, v107
	v_mul_f32_e32 v108, v109, v116
	v_mul_f32_e32 v107, 0xbfb8aa3b, v107
	v_max_f32_e32 v108, 0xc2a00000, v108
	v_exp_f32_e32 v107, v107
	v_mul_f32_e32 v108, 0xbfb8aa3b, v108
	v_exp_f32_e32 v108, v108
	v_add_f32_e32 v112, 1.0, v112
	v_add_f32_e32 v113, 1.0, v113
	v_rcp_f32_e32 v112, v112
	v_rcp_f32_e32 v113, v113
	v_mul_f32_e32 v98, v98, v116
	v_rcp_f32_e32 v106, v106
	v_add_f32_e32 v107, 1.0, v107
	v_max_f32_e32 v98, 0xc2a00000, v98
	v_rcp_f32_e32 v107, v107
	v_add_f32_e32 v108, 1.0, v108
	v_mul_f32_e32 v98, 0xbfb8aa3b, v98
	v_rcp_f32_e32 v108, v108
	v_exp_f32_e32 v98, v98
	v_fma_f32 v112, v178, v112, v138
	v_fma_f32 v113, v177, v113, v139
	v_log_f32_e32 v112, v112
	v_log_f32_e32 v113, v113
	v_fma_f32 v106, v170, v106, v133
	v_log_f32_e32 v109, v106
	v_fma_f32 v106, v169, v107, v134
	v_mul_f32_e32 v102, v102, v116
	v_mul_f32_e32 v99, v99, v116
	v_fma_f32 v154, v180, v154, v136
	v_fma_f32 v158, v179, v160, v137
	v_log_f32_e32 v160, v106
	v_fma_f32 v106, v155, v108, v135
	v_max_f32_e32 v102, 0xc2a00000, v102
	v_add_f32_e32 v98, 1.0, v98
	v_max_f32_e32 v99, 0xc2a00000, v99
	v_log_f32_e32 v154, v154
	v_log_f32_e32 v158, v158
	v_log_f32_e32 v161, v106
	v_mul_f32_e32 v102, 0xbfb8aa3b, v102
	v_rcp_f32_e32 v98, v98
	v_mul_f32_e32 v99, 0xbfb8aa3b, v99
	v_cvt_pk_f16_f32 v107, v112, v113
	v_exp_f32_e32 v112, v102
	v_mul_f32_e32 v102, v103, v116
	v_exp_f32_e32 v99, v99
	v_max_f32_e32 v102, 0xc2a00000, v102
	v_lshl_add_u64 v[110:111], s[26:27], 0, v[110:111]
	v_mul_f32_e32 v102, 0xbfb8aa3b, v102
	v_cvt_pk_f16_f32 v106, v154, v158
	v_cvt_pk_f16_f32 v108, v159, v109
	v_cvt_pk_f16_f32 v109, v160, v161
	v_exp_f32_e32 v113, v102
	v_lshl_add_u64 v[102:103], v[110:111], 0, v[114:115]
	v_fma_f32 v98, v123, v98, v124
	s_waitcnt lgkmcnt(0)
	v_subrev_u32_e32 v236, s82, v236
	global_store_dwordx4 v236, v[232:235], s[82:83]
	ds_bpermute_b32 v238, v244, v106
	ds_bpermute_b32 v239, v244, v107
	ds_bpermute_b32 v240, v244, v108
	ds_bpermute_b32 v241, v244, v109
	ds_bpermute_b32 v242, v244, v102
	v_mul_f32_e32 v104, v104, v116
	v_mul_f32_e32 v105, v105, v116
	v_log_f32_e32 v108, v98
	v_add_f32_e32 v98, 1.0, v99
	v_mul_f32_e32 v99, v100, v116
	v_max_f32_e32 v99, 0xc2a00000, v99
	v_mul_f32_e32 v100, v101, v116
	v_max_f32_e32 v104, 0xc2a00000, v104
	v_max_f32_e32 v105, 0xc2a00000, v105
	v_mul_f32_e32 v99, 0xbfb8aa3b, v99
	v_max_f32_e32 v100, 0xc2a00000, v100
	v_mul_f32_e32 v104, 0xbfb8aa3b, v104
	v_mul_f32_e32 v105, 0xbfb8aa3b, v105
	v_exp_f32_e32 v99, v99
	v_mul_f32_e32 v100, 0xbfb8aa3b, v100
	v_exp_f32_e32 v104, v104
	v_exp_f32_e32 v105, v105
	v_exp_f32_e32 v100, v100
	v_rcp_f32_e32 v98, v98
	v_add_f32_e32 v99, 1.0, v99
	v_add_f32_e32 v110, 1.0, v112
	v_add_f32_e32 v111, 1.0, v113
	v_add_f32_e32 v104, 1.0, v104
	v_add_f32_e32 v105, 1.0, v105
	v_rcp_f32_e32 v99, v99
	v_add_f32_e32 v100, 1.0, v100
	v_rcp_f32_e32 v110, v110
	v_rcp_f32_e32 v111, v111
	v_rcp_f32_e32 v104, v104
	v_rcp_f32_e32 v105, v105
	v_rcp_f32_e32 v100, v100
	v_mul_f32_e32 v90, v90, v117
	v_fma_f32 v98, v120, v98, v125
	v_mul_f32_e32 v94, v94, v117
	v_max_f32_e32 v90, 0xc2a00000, v90
	v_log_f32_e32 v101, v98
	v_fma_f32 v98, v118, v99, v126
	v_max_f32_e32 v94, 0xc2a00000, v94
	v_mul_f32_e32 v90, 0xbfb8aa3b, v90
	v_fma_f32 v106, v153, v110, v128
	v_fma_f32 v107, v168, v111, v129
	v_fma_f32 v104, v121, v104, v130
	v_fma_f32 v105, v122, v105, v131
	v_log_f32_e32 v109, v98
	v_fma_f32 v98, v119, v100, v127
	v_mul_f32_e32 v94, 0xbfb8aa3b, v94
	v_exp_f32_e32 v90, v90
	v_log_f32_e32 v106, v106
	v_log_f32_e32 v107, v107
	v_log_f32_e32 v104, v104
	v_log_f32_e32 v105, v105
	v_log_f32_e32 v110, v98
	v_exp_f32_e32 v94, v94
	v_mul_f32_e32 v95, v95, v117
	v_max_f32_e32 v95, 0xc2a00000, v95
	v_mul_f32_e32 v91, v91, v117
	v_mul_f32_e32 v95, 0xbfb8aa3b, v95
	v_add_f32_e32 v90, 1.0, v90
	v_max_f32_e32 v91, 0xc2a00000, v91
	v_cvt_pk_f16_f32 v98, v106, v107
	v_cvt_pk_f16_f32 v99, v104, v105
	v_cvt_pk_f16_f32 v100, v108, v101
	v_cvt_pk_f16_f32 v101, v109, v110
	v_exp_f32_e32 v95, v95
	v_add_f32_e32 v94, 1.0, v94
	v_rcp_f32_e32 v90, v90
	v_mul_f32_e32 v91, 0xbfb8aa3b, v91
	s_waitcnt lgkmcnt(0)
	v_subrev_u32_e32 v242, s82, v242
	global_store_dwordx4 v242, v[238:241], s[82:83]
	ds_bpermute_b32 v232, v244, v98
	ds_bpermute_b32 v233, v244, v99
	ds_bpermute_b32 v234, v244, v100
	ds_bpermute_b32 v235, v244, v101
	ds_bpermute_b32 v236, v244, v102
	v_exp_f32_e32 v91, v91
	v_fma_f32 v90, v171, v90, v132
	v_rcp_f32_e32 v100, v94
	v_or_b32_e32 v98, 32, v152
	v_ashrrev_i32_e32 v99, 31, v98
	v_add_f32_e32 v94, 1.0, v95
	v_rcp_f32_e32 v101, v94
	v_lshlrev_b64 v[94:95], 12, v[98:99]
	v_fma_f32 v98, v180, v100, v136
	v_log_f32_e32 v100, v90
	v_add_f32_e32 v90, 1.0, v91
	v_mul_f32_e32 v91, v92, v117
	v_mul_f32_e32 v96, v96, v117
	v_mul_f32_e32 v97, v97, v117
	v_max_f32_e32 v91, 0xc2a00000, v91
	v_mul_f32_e32 v92, v93, v117
	v_max_f32_e32 v96, 0xc2a00000, v96
	v_max_f32_e32 v97, 0xc2a00000, v97
	v_mul_f32_e32 v91, 0xbfb8aa3b, v91
	v_max_f32_e32 v92, 0xc2a00000, v92
	v_mul_f32_e32 v96, 0xbfb8aa3b, v96
	v_mul_f32_e32 v97, 0xbfb8aa3b, v97
	v_exp_f32_e32 v91, v91
	v_mul_f32_e32 v92, 0xbfb8aa3b, v92
	v_exp_f32_e32 v96, v96
	v_exp_f32_e32 v97, v97
	v_exp_f32_e32 v92, v92
	v_mul_f32_e32 v82, v82, v117
	v_rcp_f32_e32 v90, v90
	v_add_f32_e32 v91, 1.0, v91
	v_max_f32_e32 v82, 0xc2a00000, v82
	v_add_f32_e32 v96, 1.0, v96
	v_add_f32_e32 v97, 1.0, v97
	v_rcp_f32_e32 v91, v91
	v_add_f32_e32 v92, 1.0, v92
	v_mul_f32_e32 v82, 0xbfb8aa3b, v82
	v_rcp_f32_e32 v96, v96
	v_rcp_f32_e32 v97, v97
	v_rcp_f32_e32 v92, v92
	v_exp_f32_e32 v82, v82
	v_fma_f32 v90, v170, v90, v133
	v_log_f32_e32 v93, v90
	v_fma_f32 v90, v169, v91, v134
	v_mul_f32_e32 v83, v83, v117
	v_fma_f32 v99, v179, v101, v137
	v_fma_f32 v96, v178, v96, v138
	v_fma_f32 v97, v177, v97, v139
	v_log_f32_e32 v101, v90
	v_fma_f32 v90, v155, v92, v135
	v_add_f32_e32 v82, 1.0, v82
	v_max_f32_e32 v83, 0xc2a00000, v83
	v_log_f32_e32 v98, v98
	v_log_f32_e32 v99, v99
	v_log_f32_e32 v96, v96
	v_log_f32_e32 v97, v97
	v_log_f32_e32 v102, v90
	v_rcp_f32_e32 v82, v82
	v_mul_f32_e32 v83, 0xbfb8aa3b, v83
	v_exp_f32_e32 v83, v83
	v_lshl_add_u64 v[94:95], s[26:27], 0, v[94:95]
	v_cvt_pk_f16_f32 v90, v98, v99
	v_cvt_pk_f16_f32 v91, v96, v97
	v_cvt_pk_f16_f32 v92, v100, v93
	v_cvt_pk_f16_f32 v93, v101, v102
	v_lshl_add_u64 v[94:95], v[94:95], 0, v[114:115]
	v_fma_f32 v82, v123, v82, v124
	s_waitcnt lgkmcnt(0)
	v_subrev_u32_e32 v236, s82, v236
	global_store_dwordx4 v236, v[232:235], s[82:83] offset:64
	ds_bpermute_b32 v238, v244, v90
	ds_bpermute_b32 v239, v244, v91
	ds_bpermute_b32 v240, v244, v92
	ds_bpermute_b32 v241, v244, v93
	ds_bpermute_b32 v242, v244, v94
	v_mul_f32_e32 v86, v86, v117
	v_mul_f32_e32 v87, v87, v117
	v_log_f32_e32 v90, v82
	v_add_f32_e32 v82, 1.0, v83
	v_mul_f32_e32 v83, v84, v117
	v_max_f32_e32 v83, 0xc2a00000, v83
	v_mul_f32_e32 v84, v85, v117
	v_mul_f32_e32 v83, 0xbfb8aa3b, v83
	v_max_f32_e32 v84, 0xc2a00000, v84
	v_exp_f32_e32 v83, v83
	v_mul_f32_e32 v84, 0xbfb8aa3b, v84
	v_exp_f32_e32 v84, v84
	v_rcp_f32_e32 v82, v82
	v_add_f32_e32 v83, 1.0, v83
	v_rcp_f32_e32 v83, v83
	v_add_f32_e32 v84, 1.0, v84
	v_rcp_f32_e32 v84, v84
	v_mul_f32_e32 v88, v88, v117
	v_mul_f32_e32 v89, v89, v117
	v_max_f32_e32 v86, 0xc2a00000, v86
	v_max_f32_e32 v87, 0xc2a00000, v87
	v_max_f32_e32 v88, 0xc2a00000, v88
	v_max_f32_e32 v89, 0xc2a00000, v89
	v_fma_f32 v82, v120, v82, v125
	v_mul_f32_e32 v86, 0xbfb8aa3b, v86
	v_mul_f32_e32 v87, 0xbfb8aa3b, v87
	v_mul_f32_e32 v88, 0xbfb8aa3b, v88
	v_mul_f32_e32 v89, 0xbfb8aa3b, v89
	v_log_f32_e32 v91, v82
	v_fma_f32 v82, v118, v83, v126
	v_exp_f32_e32 v86, v86
	v_exp_f32_e32 v87, v87
	v_exp_f32_e32 v88, v88
	v_exp_f32_e32 v89, v89
	v_log_f32_e32 v92, v82
	v_fma_f32 v82, v119, v84, v127
	v_log_f32_e32 v93, v82
	ds_read2_b32 v[82:83], v176 offset0:48 offset1:128
	v_add_f32_e32 v86, 1.0, v86
	v_add_f32_e32 v87, 1.0, v87
	v_add_f32_e32 v88, 1.0, v88
	v_add_f32_e32 v89, 1.0, v89
	v_rcp_f32_e32 v86, v86
	v_rcp_f32_e32 v87, v87
	v_rcp_f32_e32 v88, v88
	v_rcp_f32_e32 v89, v89
	s_waitcnt lgkmcnt(0)
	v_mul_f32_e32 v74, v74, v82
	v_mul_f32_e32 v78, v78, v82
	v_max_f32_e32 v74, 0xc2a00000, v74
	v_max_f32_e32 v78, 0xc2a00000, v78
	v_mul_f32_e32 v74, 0xbfb8aa3b, v74
	v_fma_f32 v86, v153, v86, v128
	v_fma_f32 v87, v168, v87, v129
	v_fma_f32 v88, v121, v88, v130
	v_fma_f32 v89, v122, v89, v131
	v_mul_f32_e32 v78, 0xbfb8aa3b, v78
	v_exp_f32_e32 v74, v74
	v_log_f32_e32 v86, v86
	v_log_f32_e32 v87, v87
	v_log_f32_e32 v88, v88
	v_log_f32_e32 v89, v89
	v_exp_f32_e32 v78, v78
	v_mul_f32_e32 v79, v79, v82
	v_max_f32_e32 v79, 0xc2a00000, v79
	v_mul_f32_e32 v75, v75, v82
	v_mul_f32_e32 v79, 0xbfb8aa3b, v79
	v_add_f32_e32 v74, 1.0, v74
	v_max_f32_e32 v75, 0xc2a00000, v75
	v_cvt_pk_f16_f32 v84, v86, v87
	v_cvt_pk_f16_f32 v85, v88, v89
	v_cvt_pk_f16_f32 v86, v90, v91
	v_cvt_pk_f16_f32 v87, v92, v93
	v_exp_f32_e32 v79, v79
	v_add_f32_e32 v78, 1.0, v78
	v_rcp_f32_e32 v74, v74
	v_mul_f32_e32 v75, 0xbfb8aa3b, v75
	s_waitcnt lgkmcnt(0)
	v_subrev_u32_e32 v242, s82, v242
	global_store_dwordx4 v242, v[238:241], s[82:83]
	ds_bpermute_b32 v232, v244, v84
	ds_bpermute_b32 v233, v244, v85
	ds_bpermute_b32 v234, v244, v86
	ds_bpermute_b32 v235, v244, v87
	ds_bpermute_b32 v236, v244, v94
	v_exp_f32_e32 v75, v75
	v_mul_f32_e32 v80, v80, v82
	v_rcp_f32_e32 v86, v78
	v_or_b32_e32 v84, 48, v152
	v_mul_f32_e32 v81, v81, v82
	v_ashrrev_i32_e32 v85, 31, v84
	v_add_f32_e32 v78, 1.0, v79
	v_max_f32_e32 v80, 0xc2a00000, v80
	v_max_f32_e32 v81, 0xc2a00000, v81
	v_fma_f32 v74, v171, v74, v132
	v_rcp_f32_e32 v87, v78
	v_lshlrev_b64 v[78:79], 12, v[84:85]
	v_fma_f32 v84, v180, v86, v136
	v_mul_f32_e32 v80, 0xbfb8aa3b, v80
	v_mul_f32_e32 v81, 0xbfb8aa3b, v81
	v_log_f32_e32 v86, v74
	v_add_f32_e32 v74, 1.0, v75
	v_mul_f32_e32 v75, v76, v82
	v_exp_f32_e32 v80, v80
	v_exp_f32_e32 v81, v81
	v_max_f32_e32 v75, 0xc2a00000, v75
	v_mul_f32_e32 v76, v77, v82
	v_mul_f32_e32 v75, 0xbfb8aa3b, v75
	v_max_f32_e32 v76, 0xc2a00000, v76
	v_exp_f32_e32 v75, v75
	v_mul_f32_e32 v76, 0xbfb8aa3b, v76
	v_exp_f32_e32 v76, v76
	v_add_f32_e32 v80, 1.0, v80
	v_add_f32_e32 v81, 1.0, v81
	v_rcp_f32_e32 v80, v80
	v_rcp_f32_e32 v81, v81
	v_mul_f32_e32 v66, v66, v82
	v_rcp_f32_e32 v74, v74
	v_add_f32_e32 v75, 1.0, v75
	v_max_f32_e32 v66, 0xc2a00000, v66
	v_rcp_f32_e32 v75, v75
	v_add_f32_e32 v76, 1.0, v76
	v_mul_f32_e32 v66, 0xbfb8aa3b, v66
	v_rcp_f32_e32 v76, v76
	v_exp_f32_e32 v66, v66
	v_fma_f32 v80, v178, v80, v138
	v_fma_f32 v81, v177, v81, v139
	v_log_f32_e32 v80, v80
	v_log_f32_e32 v81, v81
	v_fma_f32 v74, v170, v74, v133
	v_log_f32_e32 v77, v74
	v_fma_f32 v74, v169, v75, v134
	v_mul_f32_e32 v70, v70, v82
	v_mul_f32_e32 v67, v67, v82
	v_fma_f32 v85, v179, v87, v137
	v_log_f32_e32 v87, v74
	v_fma_f32 v74, v155, v76, v135
	v_max_f32_e32 v70, 0xc2a00000, v70
	v_add_f32_e32 v66, 1.0, v66
	v_max_f32_e32 v67, 0xc2a00000, v67
	v_log_f32_e32 v84, v84
	v_log_f32_e32 v85, v85
	v_log_f32_e32 v88, v74
	v_mul_f32_e32 v70, 0xbfb8aa3b, v70
	v_rcp_f32_e32 v66, v66
	v_mul_f32_e32 v67, 0xbfb8aa3b, v67
	v_cvt_pk_f16_f32 v75, v80, v81
	v_exp_f32_e32 v80, v70
	v_mul_f32_e32 v70, v71, v82
	v_exp_f32_e32 v67, v67
	v_max_f32_e32 v70, 0xc2a00000, v70
	v_lshl_add_u64 v[78:79], s[26:27], 0, v[78:79]
	v_mul_f32_e32 v70, 0xbfb8aa3b, v70
	v_cvt_pk_f16_f32 v74, v84, v85
	v_cvt_pk_f16_f32 v76, v86, v77
	v_cvt_pk_f16_f32 v77, v87, v88
	v_exp_f32_e32 v81, v70
	v_lshl_add_u64 v[70:71], v[78:79], 0, v[114:115]
	v_fma_f32 v66, v123, v66, v124
	s_waitcnt lgkmcnt(0)
	v_subrev_u32_e32 v236, s82, v236
	global_store_dwordx4 v236, v[232:235], s[82:83] offset:64
	ds_bpermute_b32 v238, v244, v74
	ds_bpermute_b32 v239, v244, v75
	ds_bpermute_b32 v240, v244, v76
	ds_bpermute_b32 v241, v244, v77
	ds_bpermute_b32 v242, v244, v70
	v_mul_f32_e32 v72, v72, v82
	v_mul_f32_e32 v73, v73, v82
	v_log_f32_e32 v76, v66
	v_add_f32_e32 v66, 1.0, v67
	v_mul_f32_e32 v67, v68, v82
	v_max_f32_e32 v67, 0xc2a00000, v67
	v_mul_f32_e32 v68, v69, v82
	v_max_f32_e32 v72, 0xc2a00000, v72
	v_max_f32_e32 v73, 0xc2a00000, v73
	v_mul_f32_e32 v67, 0xbfb8aa3b, v67
	v_max_f32_e32 v68, 0xc2a00000, v68
	v_mul_f32_e32 v72, 0xbfb8aa3b, v72
	v_mul_f32_e32 v73, 0xbfb8aa3b, v73
	v_exp_f32_e32 v67, v67
	v_mul_f32_e32 v68, 0xbfb8aa3b, v68
	v_exp_f32_e32 v72, v72
	v_exp_f32_e32 v73, v73
	v_exp_f32_e32 v68, v68
	v_mul_f32_e32 v58, v58, v83
	v_rcp_f32_e32 v66, v66
	v_add_f32_e32 v67, 1.0, v67
	v_max_f32_e32 v58, 0xc2a00000, v58
	v_add_f32_e32 v78, 1.0, v80
	v_add_f32_e32 v79, 1.0, v81
	v_add_f32_e32 v72, 1.0, v72
	v_add_f32_e32 v73, 1.0, v73
	v_rcp_f32_e32 v67, v67
	v_add_f32_e32 v68, 1.0, v68
	v_mul_f32_e32 v58, 0xbfb8aa3b, v58
	v_rcp_f32_e32 v78, v78
	v_rcp_f32_e32 v79, v79
	v_rcp_f32_e32 v72, v72
	v_rcp_f32_e32 v73, v73
	v_rcp_f32_e32 v68, v68
	v_exp_f32_e32 v58, v58
	v_fma_f32 v66, v120, v66, v125
	v_log_f32_e32 v69, v66
	v_fma_f32 v66, v118, v67, v126
	v_mul_f32_e32 v59, v59, v83
	v_fma_f32 v74, v153, v78, v128
	v_fma_f32 v75, v168, v79, v129
	v_fma_f32 v72, v121, v72, v130
	v_fma_f32 v73, v122, v73, v131
	v_log_f32_e32 v77, v66
	v_fma_f32 v66, v119, v68, v127
	v_add_f32_e32 v58, 1.0, v58
	v_max_f32_e32 v59, 0xc2a00000, v59
	v_log_f32_e32 v74, v74
	v_log_f32_e32 v75, v75
	v_log_f32_e32 v72, v72
	v_log_f32_e32 v73, v73
	v_log_f32_e32 v78, v66
	v_rcp_f32_e32 v58, v58
	v_mul_f32_e32 v59, 0xbfb8aa3b, v59
	v_exp_f32_e32 v59, v59
	v_mul_f32_e32 v64, v64, v83
	v_mul_f32_e32 v65, v65, v83
	v_max_f32_e32 v64, 0xc2a00000, v64
	v_max_f32_e32 v65, 0xc2a00000, v65
	v_cvt_pk_f16_f32 v66, v74, v75
	v_cvt_pk_f16_f32 v67, v72, v73
	v_cvt_pk_f16_f32 v68, v76, v69
	v_mul_f32_e32 v62, v62, v83
	v_mul_f32_e32 v63, v63, v83
	v_cvt_pk_f16_f32 v69, v77, v78
	v_mul_f32_e32 v64, 0xbfb8aa3b, v64
	v_mul_f32_e32 v65, 0xbfb8aa3b, v65
	v_fma_f32 v58, v171, v58, v132
	v_max_f32_e32 v62, 0xc2a00000, v62
	v_max_f32_e32 v63, 0xc2a00000, v63
	s_waitcnt lgkmcnt(0)
	v_subrev_u32_e32 v242, s82, v242
	global_store_dwordx4 v242, v[238:241], s[82:83]
	ds_bpermute_b32 v232, v244, v66
	ds_bpermute_b32 v233, v244, v67
	ds_bpermute_b32 v234, v244, v68
	ds_bpermute_b32 v235, v244, v69
	ds_bpermute_b32 v236, v244, v70
	v_exp_f32_e32 v64, v64
	v_exp_f32_e32 v65, v65
	v_log_f32_e32 v66, v58
	v_add_f32_e32 v58, 1.0, v59
	v_mul_f32_e32 v59, v60, v83
	v_mul_f32_e32 v62, 0xbfb8aa3b, v62
	v_mul_f32_e32 v63, 0xbfb8aa3b, v63
	v_max_f32_e32 v59, 0xc2a00000, v59
	v_mul_f32_e32 v60, v61, v83
	v_exp_f32_e32 v62, v62
	v_exp_f32_e32 v63, v63
	v_mul_f32_e32 v59, 0xbfb8aa3b, v59
	v_max_f32_e32 v60, 0xc2a00000, v60
	v_exp_f32_e32 v59, v59
	v_mul_f32_e32 v60, 0xbfb8aa3b, v60
	v_add_f32_e32 v64, 1.0, v64
	v_add_f32_e32 v65, 1.0, v65
	v_exp_f32_e32 v60, v60
	v_rcp_f32_e32 v64, v64
	v_rcp_f32_e32 v65, v65
	v_add_f32_e32 v62, 1.0, v62
	v_add_f32_e32 v63, 1.0, v63
	v_mul_f32_e32 v50, v50, v83
	v_rcp_f32_e32 v62, v62
	v_rcp_f32_e32 v63, v63
	v_rcp_f32_e32 v58, v58
	v_add_f32_e32 v59, 1.0, v59
	v_max_f32_e32 v50, 0xc2a00000, v50
	v_rcp_f32_e32 v59, v59
	v_add_f32_e32 v60, 1.0, v60
	v_mul_f32_e32 v50, 0xbfb8aa3b, v50
	v_fma_f32 v64, v178, v64, v138
	v_fma_f32 v65, v177, v65, v139
	v_rcp_f32_e32 v60, v60
	v_exp_f32_e32 v50, v50
	v_log_f32_e32 v64, v64
	v_log_f32_e32 v65, v65
	v_fma_f32 v62, v180, v62, v136
	v_fma_f32 v63, v179, v63, v137
	v_fma_f32 v58, v170, v58, v133
	v_mul_f32_e32 v54, v54, v83
	v_log_f32_e32 v62, v62
	v_log_f32_e32 v63, v63
	v_log_f32_e32 v61, v58
	v_fma_f32 v58, v169, v59, v134
	v_max_f32_e32 v54, 0xc2a00000, v54
	v_mul_f32_e32 v51, v51, v83
	v_log_f32_e32 v67, v58
	v_fma_f32 v58, v155, v60, v135
	v_mul_f32_e32 v54, 0xbfb8aa3b, v54
	v_add_f32_e32 v50, 1.0, v50
	v_max_f32_e32 v51, 0xc2a00000, v51
	v_log_f32_e32 v68, v58
	v_cvt_pk_f16_f32 v59, v64, v65
	v_exp_f32_e32 v64, v54
	v_mul_f32_e32 v54, v55, v83
	v_rcp_f32_e32 v50, v50
	v_mul_f32_e32 v51, 0xbfb8aa3b, v51
	v_max_f32_e32 v54, 0xc2a00000, v54
	v_exp_f32_e32 v51, v51
	v_cvt_pk_f16_f32 v58, v62, v63
	v_lshl_add_u64 v[62:63], v[166:167], 0, s[14:15]
	v_mul_f32_e32 v54, 0xbfb8aa3b, v54
	s_mov_b32 s14, 0x80000
	v_exp_f32_e32 v65, v54
	v_add_co_u32_e32 v54, vcc, s14, v166
	v_cvt_pk_f16_f32 v60, v66, v61
	v_cvt_pk_f16_f32 v61, v67, v68
	v_addc_co_u32_e32 v55, vcc, 0, v167, vcc
	v_fma_f32 v50, v123, v50, v124
	s_waitcnt lgkmcnt(0)
	v_subrev_u32_e32 v236, s82, v236
	global_store_dwordx4 v236, v[232:235], s[82:83] offset:64
	ds_bpermute_b32 v238, v244, v58
	ds_bpermute_b32 v239, v244, v59
	ds_bpermute_b32 v240, v244, v60
	ds_bpermute_b32 v241, v244, v61
	ds_bpermute_b32 v242, v244, v54
	v_mul_f32_e32 v56, v56, v83
	v_mul_f32_e32 v57, v57, v83
	v_log_f32_e32 v58, v50
	v_add_f32_e32 v50, 1.0, v51
	v_mul_f32_e32 v51, v52, v83
	v_max_f32_e32 v51, 0xc2a00000, v51
	v_mul_f32_e32 v51, 0xbfb8aa3b, v51
	v_exp_f32_e32 v51, v51
	v_rcp_f32_e32 v50, v50
	v_mul_f32_e32 v52, v53, v83
	v_max_f32_e32 v56, 0xc2a00000, v56
	v_add_f32_e32 v51, 1.0, v51
	v_rcp_f32_e32 v51, v51
	v_fma_f32 v50, v120, v50, v125
	v_log_f32_e32 v59, v50
	v_max_f32_e32 v57, 0xc2a00000, v57
	v_fma_f32 v50, v118, v51, v126
	v_log_f32_e32 v60, v50
	ds_read2_b32 v[50:51], v176 offset0:144 offset1:160
	v_max_f32_e32 v52, 0xc2a00000, v52
	v_mul_f32_e32 v56, 0xbfb8aa3b, v56
	v_mul_f32_e32 v57, 0xbfb8aa3b, v57
	v_mul_f32_e32 v52, 0xbfb8aa3b, v52
	v_exp_f32_e32 v56, v56
	v_exp_f32_e32 v57, v57
	v_exp_f32_e32 v52, v52
	s_waitcnt lgkmcnt(0)
	v_mul_f32_e32 v42, v42, v50
	v_max_f32_e32 v42, 0xc2a00000, v42
	v_add_f32_e32 v64, 1.0, v64
	v_add_f32_e32 v65, 1.0, v65
	v_add_f32_e32 v56, 1.0, v56
	v_add_f32_e32 v57, 1.0, v57
	v_add_f32_e32 v52, 1.0, v52
	v_mul_f32_e32 v42, 0xbfb8aa3b, v42
	v_rcp_f32_e32 v64, v64
	v_rcp_f32_e32 v65, v65
	v_rcp_f32_e32 v56, v56
	v_rcp_f32_e32 v57, v57
	v_rcp_f32_e32 v52, v52
	v_exp_f32_e32 v42, v42
	v_mul_f32_e32 v43, v43, v50
	v_fma_f32 v54, v153, v64, v128
	v_fma_f32 v55, v168, v65, v129
	v_fma_f32 v56, v121, v56, v130
	v_fma_f32 v57, v122, v57, v131
	v_fma_f32 v52, v119, v52, v127
	v_add_f32_e32 v42, 1.0, v42
	v_max_f32_e32 v43, 0xc2a00000, v43
	v_log_f32_e32 v54, v54
	v_log_f32_e32 v55, v55
	v_log_f32_e32 v56, v56
	v_log_f32_e32 v57, v57
	v_log_f32_e32 v61, v52
	v_rcp_f32_e32 v42, v42
	v_mul_f32_e32 v43, 0xbfb8aa3b, v43
	v_exp_f32_e32 v43, v43
	v_mul_f32_e32 v48, v48, v50
	v_mul_f32_e32 v49, v49, v50
	v_max_f32_e32 v48, 0xc2a00000, v48
	v_max_f32_e32 v49, 0xc2a00000, v49
	v_cvt_pk_f16_f32 v52, v54, v55
	v_cvt_pk_f16_f32 v53, v56, v57
	v_cvt_pk_f16_f32 v54, v58, v59
	v_mul_f32_e32 v46, v46, v50
	v_mul_f32_e32 v47, v47, v50
	v_cvt_pk_f16_f32 v55, v60, v61
	v_mul_f32_e32 v48, 0xbfb8aa3b, v48
	v_mul_f32_e32 v49, 0xbfb8aa3b, v49
	v_fma_f32 v42, v171, v42, v132
	v_max_f32_e32 v46, 0xc2a00000, v46
	v_max_f32_e32 v47, 0xc2a00000, v47
	s_waitcnt lgkmcnt(0)
	v_subrev_u32_e32 v242, s82, v242
	global_store_dwordx4 v242, v[238:241], s[82:83]
	ds_bpermute_b32 v232, v244, v52
	ds_bpermute_b32 v233, v244, v53
	ds_bpermute_b32 v234, v244, v54
	ds_bpermute_b32 v235, v244, v55
	ds_bpermute_b32 v236, v244, v62
	v_exp_f32_e32 v48, v48
	v_exp_f32_e32 v49, v49
	v_log_f32_e32 v52, v42
	v_add_f32_e32 v42, 1.0, v43
	v_mul_f32_e32 v43, v44, v50
	v_mul_f32_e32 v46, 0xbfb8aa3b, v46
	v_mul_f32_e32 v47, 0xbfb8aa3b, v47
	v_max_f32_e32 v43, 0xc2a00000, v43
	v_mul_f32_e32 v44, v45, v50
	v_exp_f32_e32 v46, v46
	v_exp_f32_e32 v47, v47
	v_mul_f32_e32 v43, 0xbfb8aa3b, v43
	v_max_f32_e32 v44, 0xc2a00000, v44
	v_exp_f32_e32 v43, v43
	v_mul_f32_e32 v44, 0xbfb8aa3b, v44
	v_add_f32_e32 v48, 1.0, v48
	v_add_f32_e32 v49, 1.0, v49
	v_exp_f32_e32 v44, v44
	v_rcp_f32_e32 v48, v48
	v_rcp_f32_e32 v49, v49
	v_add_f32_e32 v46, 1.0, v46
	v_add_f32_e32 v47, 1.0, v47
	v_mul_f32_e32 v34, v34, v50
	v_rcp_f32_e32 v46, v46
	v_rcp_f32_e32 v47, v47
	v_rcp_f32_e32 v42, v42
	v_add_f32_e32 v43, 1.0, v43
	v_max_f32_e32 v34, 0xc2a00000, v34
	v_rcp_f32_e32 v43, v43
	v_add_f32_e32 v44, 1.0, v44
	v_mul_f32_e32 v34, 0xbfb8aa3b, v34
	v_fma_f32 v48, v178, v48, v138
	v_fma_f32 v49, v177, v49, v139
	v_rcp_f32_e32 v44, v44
	v_exp_f32_e32 v34, v34
	v_log_f32_e32 v48, v48
	v_log_f32_e32 v49, v49
	v_fma_f32 v46, v180, v46, v136
	v_fma_f32 v47, v179, v47, v137
	v_fma_f32 v42, v170, v42, v133
	v_mul_f32_e32 v38, v38, v50
	v_log_f32_e32 v46, v46
	v_log_f32_e32 v47, v47
	v_log_f32_e32 v45, v42
	v_fma_f32 v42, v169, v43, v134
	v_max_f32_e32 v38, 0xc2a00000, v38
	v_mul_f32_e32 v35, v35, v50
	v_log_f32_e32 v53, v42
	v_fma_f32 v42, v155, v44, v135
	v_mul_f32_e32 v38, 0xbfb8aa3b, v38
	v_add_f32_e32 v34, 1.0, v34
	v_max_f32_e32 v35, 0xc2a00000, v35
	v_log_f32_e32 v54, v42
	v_cvt_pk_f16_f32 v43, v48, v49
	v_exp_f32_e32 v48, v38
	v_mul_f32_e32 v38, v39, v50
	v_rcp_f32_e32 v34, v34
	v_mul_f32_e32 v35, 0xbfb8aa3b, v35
	s_mov_b64 s[14:15], 0x90000
	v_max_f32_e32 v38, 0xc2a00000, v38
	v_exp_f32_e32 v35, v35
	v_cvt_pk_f16_f32 v42, v46, v47
	v_lshl_add_u64 v[46:47], v[166:167], 0, s[14:15]
	v_mul_f32_e32 v38, 0xbfb8aa3b, v38
	s_mov_b32 s14, 0x90000
	v_exp_f32_e32 v49, v38
	v_add_co_u32_e32 v38, vcc, s14, v166
	v_cvt_pk_f16_f32 v44, v52, v45
	v_cvt_pk_f16_f32 v45, v53, v54
	v_addc_co_u32_e32 v39, vcc, 0, v167, vcc
	v_fma_f32 v34, v123, v34, v124
	s_waitcnt lgkmcnt(0)
	v_subrev_u32_e32 v236, s82, v236
	global_store_dwordx4 v236, v[232:235], s[82:83] offset:64
	ds_bpermute_b32 v238, v244, v42
	ds_bpermute_b32 v239, v244, v43
	ds_bpermute_b32 v240, v244, v44
	ds_bpermute_b32 v241, v244, v45
	ds_bpermute_b32 v242, v244, v38
	v_mul_f32_e32 v40, v40, v50
	v_mul_f32_e32 v41, v41, v50
	v_log_f32_e32 v42, v34
	v_add_f32_e32 v34, 1.0, v35
	v_mul_f32_e32 v35, v36, v50
	v_max_f32_e32 v35, 0xc2a00000, v35
	v_mul_f32_e32 v36, v37, v50
	v_max_f32_e32 v40, 0xc2a00000, v40
	v_max_f32_e32 v41, 0xc2a00000, v41
	v_mul_f32_e32 v35, 0xbfb8aa3b, v35
	v_max_f32_e32 v36, 0xc2a00000, v36
	v_mul_f32_e32 v40, 0xbfb8aa3b, v40
	v_mul_f32_e32 v41, 0xbfb8aa3b, v41
	v_exp_f32_e32 v35, v35
	v_mul_f32_e32 v36, 0xbfb8aa3b, v36
	v_exp_f32_e32 v40, v40
	v_exp_f32_e32 v41, v41
	v_exp_f32_e32 v36, v36
	v_mul_f32_e32 v26, v26, v51
	v_rcp_f32_e32 v34, v34
	v_add_f32_e32 v35, 1.0, v35
	v_max_f32_e32 v26, 0xc2a00000, v26
	v_add_f32_e32 v48, 1.0, v48
	v_add_f32_e32 v49, 1.0, v49
	v_add_f32_e32 v40, 1.0, v40
	v_add_f32_e32 v41, 1.0, v41
	v_rcp_f32_e32 v35, v35
	v_add_f32_e32 v36, 1.0, v36
	v_mul_f32_e32 v26, 0xbfb8aa3b, v26
	v_rcp_f32_e32 v48, v48
	v_rcp_f32_e32 v49, v49
	v_rcp_f32_e32 v40, v40
	v_rcp_f32_e32 v41, v41
	v_rcp_f32_e32 v36, v36
	v_exp_f32_e32 v26, v26
	v_fma_f32 v34, v120, v34, v125
	v_log_f32_e32 v37, v34
	v_fma_f32 v34, v118, v35, v126
	v_mul_f32_e32 v27, v27, v51
	v_fma_f32 v38, v153, v48, v128
	v_fma_f32 v39, v168, v49, v129
	v_fma_f32 v40, v121, v40, v130
	v_fma_f32 v41, v122, v41, v131
	v_log_f32_e32 v43, v34
	v_fma_f32 v34, v119, v36, v127
	v_add_f32_e32 v26, 1.0, v26
	v_max_f32_e32 v27, 0xc2a00000, v27
	v_log_f32_e32 v38, v38
	v_log_f32_e32 v39, v39
	v_log_f32_e32 v40, v40
	v_log_f32_e32 v41, v41
	v_log_f32_e32 v44, v34
	v_rcp_f32_e32 v26, v26
	v_mul_f32_e32 v27, 0xbfb8aa3b, v27
	v_exp_f32_e32 v27, v27
	v_mul_f32_e32 v32, v32, v51
	v_mul_f32_e32 v33, v33, v51
	v_max_f32_e32 v32, 0xc2a00000, v32
	v_max_f32_e32 v33, 0xc2a00000, v33
	v_cvt_pk_f16_f32 v34, v38, v39
	v_cvt_pk_f16_f32 v35, v40, v41
	v_cvt_pk_f16_f32 v36, v42, v37
	v_mul_f32_e32 v30, v30, v51
	v_mul_f32_e32 v31, v31, v51
	v_cvt_pk_f16_f32 v37, v43, v44
	v_mul_f32_e32 v32, 0xbfb8aa3b, v32
	v_mul_f32_e32 v33, 0xbfb8aa3b, v33
	v_fma_f32 v26, v171, v26, v132
	v_max_f32_e32 v30, 0xc2a00000, v30
	v_max_f32_e32 v31, 0xc2a00000, v31
	s_waitcnt lgkmcnt(0)
	v_subrev_u32_e32 v242, s82, v242
	global_store_dwordx4 v242, v[238:241], s[82:83]
	ds_bpermute_b32 v232, v244, v34
	ds_bpermute_b32 v233, v244, v35
	ds_bpermute_b32 v234, v244, v36
	ds_bpermute_b32 v235, v244, v37
	ds_bpermute_b32 v236, v244, v46
	v_exp_f32_e32 v32, v32
	v_exp_f32_e32 v33, v33
	v_log_f32_e32 v34, v26
	v_add_f32_e32 v26, 1.0, v27
	v_mul_f32_e32 v27, v28, v51
	v_mul_f32_e32 v30, 0xbfb8aa3b, v30
	v_mul_f32_e32 v31, 0xbfb8aa3b, v31
	v_max_f32_e32 v27, 0xc2a00000, v27
	v_mul_f32_e32 v28, v29, v51
	v_exp_f32_e32 v30, v30
	v_exp_f32_e32 v31, v31
	v_mul_f32_e32 v27, 0xbfb8aa3b, v27
	v_max_f32_e32 v28, 0xc2a00000, v28
	v_exp_f32_e32 v27, v27
	v_mul_f32_e32 v28, 0xbfb8aa3b, v28
	v_add_f32_e32 v32, 1.0, v32
	v_add_f32_e32 v33, 1.0, v33
	v_exp_f32_e32 v28, v28
	v_rcp_f32_e32 v32, v32
	v_rcp_f32_e32 v33, v33
	v_add_f32_e32 v30, 1.0, v30
	v_add_f32_e32 v31, 1.0, v31
	v_mul_f32_e32 v18, v18, v51
	v_rcp_f32_e32 v30, v30
	v_rcp_f32_e32 v31, v31
	v_rcp_f32_e32 v26, v26
	v_add_f32_e32 v27, 1.0, v27
	v_max_f32_e32 v18, 0xc2a00000, v18
	v_rcp_f32_e32 v27, v27
	v_add_f32_e32 v28, 1.0, v28
	v_mul_f32_e32 v18, 0xbfb8aa3b, v18
	v_fma_f32 v32, v178, v32, v138
	v_fma_f32 v33, v177, v33, v139
	v_rcp_f32_e32 v28, v28
	v_exp_f32_e32 v18, v18
	v_log_f32_e32 v32, v32
	v_log_f32_e32 v33, v33
	v_fma_f32 v30, v180, v30, v136
	v_fma_f32 v31, v179, v31, v137
	v_fma_f32 v26, v170, v26, v133
	v_mul_f32_e32 v22, v22, v51
	v_log_f32_e32 v30, v30
	v_log_f32_e32 v31, v31
	v_log_f32_e32 v29, v26
	v_fma_f32 v26, v169, v27, v134
	v_max_f32_e32 v22, 0xc2a00000, v22
	v_mul_f32_e32 v19, v19, v51
	v_log_f32_e32 v35, v26
	v_fma_f32 v26, v155, v28, v135
	v_mul_f32_e32 v22, 0xbfb8aa3b, v22
	v_add_f32_e32 v18, 1.0, v18
	v_max_f32_e32 v19, 0xc2a00000, v19
	v_log_f32_e32 v36, v26
	v_cvt_pk_f16_f32 v27, v32, v33
	v_exp_f32_e32 v32, v22
	v_mul_f32_e32 v22, v23, v51
	v_rcp_f32_e32 v18, v18
	v_mul_f32_e32 v19, 0xbfb8aa3b, v19
	s_mov_b64 s[14:15], 0xa0000
	v_max_f32_e32 v22, 0xc2a00000, v22
	v_exp_f32_e32 v19, v19
	v_cvt_pk_f16_f32 v26, v30, v31
	v_lshl_add_u64 v[30:31], v[166:167], 0, s[14:15]
	v_mul_f32_e32 v22, 0xbfb8aa3b, v22
	s_mov_b32 s14, 0xa0000
	v_exp_f32_e32 v33, v22
	v_add_co_u32_e32 v22, vcc, s14, v166
	v_cvt_pk_f16_f32 v28, v34, v29
	v_cvt_pk_f16_f32 v29, v35, v36
	v_addc_co_u32_e32 v23, vcc, 0, v167, vcc
	v_fma_f32 v18, v123, v18, v124
	s_waitcnt lgkmcnt(0)
	v_subrev_u32_e32 v236, s82, v236
	global_store_dwordx4 v236, v[232:235], s[82:83] offset:64
	ds_bpermute_b32 v238, v244, v26
	ds_bpermute_b32 v239, v244, v27
	ds_bpermute_b32 v240, v244, v28
	ds_bpermute_b32 v241, v244, v29
	ds_bpermute_b32 v242, v244, v22
	v_mul_f32_e32 v24, v24, v51
	v_mul_f32_e32 v25, v25, v51
	v_log_f32_e32 v26, v18
	v_add_f32_e32 v18, 1.0, v19
	v_mul_f32_e32 v19, v20, v51
	v_max_f32_e32 v19, 0xc2a00000, v19
	v_mul_f32_e32 v20, v21, v51
	ds_read_b32 v28, v176 offset:704
	v_max_f32_e32 v24, 0xc2a00000, v24
	v_max_f32_e32 v25, 0xc2a00000, v25
	v_mul_f32_e32 v19, 0xbfb8aa3b, v19
	v_max_f32_e32 v20, 0xc2a00000, v20
	v_mul_f32_e32 v24, 0xbfb8aa3b, v24
	v_mul_f32_e32 v25, 0xbfb8aa3b, v25
	v_exp_f32_e32 v19, v19
	v_mul_f32_e32 v20, 0xbfb8aa3b, v20
	v_exp_f32_e32 v24, v24
	v_exp_f32_e32 v25, v25
	v_exp_f32_e32 v20, v20
	s_waitcnt lgkmcnt(0)
	v_mul_f32_e32 v10, v10, v28
	v_rcp_f32_e32 v18, v18
	v_add_f32_e32 v19, 1.0, v19
	v_max_f32_e32 v10, 0xc2a00000, v10
	v_add_f32_e32 v32, 1.0, v32
	v_add_f32_e32 v33, 1.0, v33
	v_add_f32_e32 v24, 1.0, v24
	v_add_f32_e32 v25, 1.0, v25
	v_rcp_f32_e32 v19, v19
	v_add_f32_e32 v20, 1.0, v20
	v_mul_f32_e32 v10, 0xbfb8aa3b, v10
	v_rcp_f32_e32 v32, v32
	v_rcp_f32_e32 v33, v33
	v_rcp_f32_e32 v24, v24
	v_rcp_f32_e32 v25, v25
	v_rcp_f32_e32 v20, v20
	v_exp_f32_e32 v10, v10
	v_fma_f32 v18, v120, v18, v125
	v_log_f32_e32 v21, v18
	v_fma_f32 v18, v118, v19, v126
	v_mul_f32_e32 v11, v11, v28
	v_fma_f32 v22, v153, v32, v128
	v_fma_f32 v23, v168, v33, v129
	v_fma_f32 v24, v121, v24, v130
	v_fma_f32 v25, v122, v25, v131
	v_log_f32_e32 v27, v18
	v_fma_f32 v18, v119, v20, v127
	v_add_f32_e32 v10, 1.0, v10
	v_max_f32_e32 v11, 0xc2a00000, v11
	v_log_f32_e32 v22, v22
	v_log_f32_e32 v23, v23
	v_log_f32_e32 v24, v24
	v_log_f32_e32 v25, v25
	v_log_f32_e32 v29, v18
	v_rcp_f32_e32 v10, v10
	v_mul_f32_e32 v11, 0xbfb8aa3b, v11
	v_mul_f32_e32 v14, v14, v28
	v_mul_f32_e32 v15, v15, v28
	v_exp_f32_e32 v11, v11
	v_max_f32_e32 v14, 0xc2a00000, v14
	v_max_f32_e32 v15, 0xc2a00000, v15
	v_mul_f32_e32 v14, 0xbfb8aa3b, v14
	v_mul_f32_e32 v15, 0xbfb8aa3b, v15
	v_cvt_pk_f16_f32 v18, v22, v23
	v_cvt_pk_f16_f32 v19, v24, v25
	v_cvt_pk_f16_f32 v20, v26, v21
	v_exp_f32_e32 v14, v14
	v_exp_f32_e32 v15, v15
	v_cvt_pk_f16_f32 v21, v27, v29
	v_fma_f32 v10, v171, v10, v132
	s_waitcnt lgkmcnt(0)
	v_subrev_u32_e32 v242, s82, v242
	global_store_dwordx4 v242, v[238:241], s[82:83]
	ds_bpermute_b32 v232, v244, v18
	ds_bpermute_b32 v233, v244, v19
	ds_bpermute_b32 v234, v244, v20
	ds_bpermute_b32 v235, v244, v21
	ds_bpermute_b32 v236, v244, v30
	v_add_f32_e32 v14, 1.0, v14
	v_add_f32_e32 v15, 1.0, v15
	v_log_f32_e32 v18, v10
	v_add_f32_e32 v10, 1.0, v11
	v_mul_f32_e32 v11, v12, v28
	v_max_f32_e32 v11, 0xc2a00000, v11
	v_mul_f32_e32 v11, 0xbfb8aa3b, v11
	v_exp_f32_e32 v11, v11
	v_rcp_f32_e32 v14, v14
	v_rcp_f32_e32 v15, v15
	v_mul_f32_e32 v16, v16, v28
	v_mul_f32_e32 v17, v17, v28
	v_rcp_f32_e32 v10, v10
	v_mul_f32_e32 v12, v13, v28
	v_add_f32_e32 v11, 1.0, v11
	v_fma_f32 v14, v180, v14, v136
	v_fma_f32 v15, v179, v15, v137
	v_max_f32_e32 v16, 0xc2a00000, v16
	v_max_f32_e32 v17, 0xc2a00000, v17
	v_max_f32_e32 v12, 0xc2a00000, v12
	v_rcp_f32_e32 v11, v11
	v_log_f32_e32 v14, v14
	v_mul_f32_e32 v16, 0xbfb8aa3b, v16
	v_mul_f32_e32 v17, 0xbfb8aa3b, v17
	v_log_f32_e32 v15, v15
	v_mul_f32_e32 v12, 0xbfb8aa3b, v12
	v_exp_f32_e32 v16, v16
	v_exp_f32_e32 v17, v17
	v_exp_f32_e32 v12, v12
	v_mul_f32_e32 v6, v6, v28
	v_fma_f32 v10, v170, v10, v133
	v_max_f32_e32 v6, 0xc2a00000, v6
	v_log_f32_e32 v13, v10
	v_fma_f32 v10, v169, v11, v134
	v_mul_f32_e32 v6, 0xbfb8aa3b, v6
	v_log_f32_e32 v19, v10
	v_cvt_pk_f16_f32 v10, v14, v15
	v_exp_f32_e32 v14, v6
	v_mul_f32_e32 v6, v7, v28
	v_mul_f32_e32 v8, v8, v28
	v_mul_f32_e32 v9, v9, v28
	v_mul_f32_e32 v2, v2, v28
	v_mul_f32_e32 v3, v3, v28
	v_mul_f32_e32 v4, v4, v28
	v_mul_f32_e32 v5, v5, v28
	v_add_f32_e32 v16, 1.0, v16
	v_add_f32_e32 v17, 1.0, v17
	v_add_f32_e32 v12, 1.0, v12
	v_max_f32_e32 v6, 0xc2a00000, v6
	v_max_f32_e32 v8, 0xc2a00000, v8
	v_max_f32_e32 v9, 0xc2a00000, v9
	v_max_f32_e32 v2, 0xc2a00000, v2
	v_max_f32_e32 v3, 0xc2a00000, v3
	v_max_f32_e32 v4, 0xc2a00000, v4
	v_max_f32_e32 v5, 0xc2a00000, v5
	v_rcp_f32_e32 v16, v16
	v_rcp_f32_e32 v17, v17
	v_rcp_f32_e32 v12, v12
	v_mul_f32_e32 v6, 0xbfb8aa3b, v6
	v_mul_f32_e32 v8, 0xbfb8aa3b, v8
	v_mul_f32_e32 v9, 0xbfb8aa3b, v9
	v_mul_f32_e32 v2, 0xbfb8aa3b, v2
	v_mul_f32_e32 v3, 0xbfb8aa3b, v3
	v_mul_f32_e32 v4, 0xbfb8aa3b, v4
	v_mul_f32_e32 v5, 0xbfb8aa3b, v5
	v_exp_f32_e32 v15, v6
	v_exp_f32_e32 v8, v8
	v_exp_f32_e32 v9, v9
	v_exp_f32_e32 v2, v2
	v_exp_f32_e32 v3, v3
	v_exp_f32_e32 v4, v4
	v_exp_f32_e32 v5, v5
	v_fma_f32 v16, v178, v16, v138
	v_fmac_f32_e32 v139, v177, v17
	v_fmac_f32_e32 v135, v155, v12
	v_log_f32_e32 v16, v16
	v_log_f32_e32 v17, v139
	v_log_f32_e32 v20, v135
	v_add_f32_e32 v14, 1.0, v14
	v_add_f32_e32 v15, 1.0, v15
	v_add_f32_e32 v8, 1.0, v8
	v_add_f32_e32 v9, 1.0, v9
	v_add_f32_e32 v2, 1.0, v2
	v_add_f32_e32 v3, 1.0, v3
	v_add_f32_e32 v4, 1.0, v4
	v_add_f32_e32 v5, 1.0, v5
	s_mov_b64 s[14:15], 0xb0000
	v_rcp_f32_e32 v14, v14
	v_rcp_f32_e32 v15, v15
	v_rcp_f32_e32 v8, v8
	v_rcp_f32_e32 v9, v9
	v_rcp_f32_e32 v2, v2
	v_rcp_f32_e32 v3, v3
	v_rcp_f32_e32 v4, v4
	v_rcp_f32_e32 v5, v5
	v_lshl_add_u64 v[136:137], v[166:167], 0, s[14:15]
	s_mov_b32 s14, 0xb0000
	v_add_co_u32_e32 v6, vcc, s14, v166
	v_cvt_pk_f16_f32 v11, v16, v17
	v_cvt_pk_f16_f32 v12, v18, v13
	v_cvt_pk_f16_f32 v13, v19, v20
	v_addc_co_u32_e32 v7, vcc, 0, v167, vcc
	s_waitcnt lgkmcnt(0)
	v_subrev_u32_e32 v236, s82, v236
	global_store_dwordx4 v236, v[232:235], s[82:83] offset:64
	ds_bpermute_b32 v238, v244, v10
	ds_bpermute_b32 v239, v244, v11
	ds_bpermute_b32 v240, v244, v12
	ds_bpermute_b32 v241, v244, v13
	ds_bpermute_b32 v242, v244, v6
	v_fma_f32 v6, v153, v14, v128
	v_fma_f32 v7, v168, v15, v129
	v_fma_f32 v8, v121, v8, v130
	v_fmac_f32_e32 v131, v122, v9
	v_fma_f32 v2, v123, v2, v124
	v_fma_f32 v3, v120, v3, v125
	v_fma_f32 v4, v118, v4, v126
	v_fmac_f32_e32 v127, v119, v5
	v_log_f32_e32 v6, v6
	v_log_f32_e32 v7, v7
	v_log_f32_e32 v8, v8
	v_log_f32_e32 v9, v131
	v_log_f32_e32 v2, v2
	v_log_f32_e32 v3, v3
	v_log_f32_e32 v4, v4
	v_log_f32_e32 v5, v127
	v_cvt_pk_f16_f32 v196, v181, v182
	v_cvt_pk_f16_f32 v132, v6, v7
	v_cvt_pk_f16_f32 v133, v8, v9
	v_cvt_pk_f16_f32 v134, v2, v3
	v_cvt_pk_f16_f32 v135, v4, v5
	s_waitcnt lgkmcnt(0)
	v_subrev_u32_e32 v242, s82, v242
	global_store_dwordx4 v242, v[238:241], s[82:83]
	ds_bpermute_b32 v232, v244, v194
	ds_bpermute_b32 v233, v244, v195
	ds_bpermute_b32 v234, v244, v196
	ds_bpermute_b32 v235, v244, v197
	ds_bpermute_b32 v236, v244, v166
	s_andn2_b64 vcc, exec, s[38:39]
	s_mov_b64 s[28:29], -1
	s_waitcnt lgkmcnt(0)
	v_subrev_u32_e32 v236, s82, v236
	global_store_dwordx4 v236, v[232:235], s[82:83] offset:64
	ds_bpermute_b32 v238, v244, v132
	ds_bpermute_b32 v239, v244, v133
	ds_bpermute_b32 v240, v244, v134
	ds_bpermute_b32 v241, v244, v135
	ds_bpermute_b32 v242, v244, v136
	s_waitcnt lgkmcnt(0)
	v_subrev_u32_e32 v242, s82, v242
	global_store_dwordx4 v242, v[238:241], s[82:83] offset:64
	s_cbranch_vccnz .LBB0_495

.LBB0_1082:
	v_mbcnt_lo_u32_b32 v244, -1, 0
	v_mbcnt_hi_u32_b32 v244, -1, v244
	v_lshrrev_b32_e32 v245, 2, v244
	v_and_b32_e32 v244, 3, v244
	v_lshl_add_u32 v244, v244, 4, v245
	v_lshlrev_b32_e32 v244, 2, v244
	v_pk_mul_f32 v[148:149], v[118:119], v[118:119]
	v_pk_mul_f32 v[150:151], v[126:127], v[126:127]
	v_pk_fma_f32 v[148:149], v[116:117], v[116:117], v[148:149]
	v_pk_fma_f32 v[150:151], v[124:125], v[124:125], v[150:151]
	v_lshl_add_u32 v144, s46, 8, v1
	v_pk_add_f32 v[152:153], v[148:149], v[150:151]
	v_cvt_pk_bf16_f32 v149, v118, v119
	v_cvt_pk_bf16_f32 v150, v124, v125
	v_pk_mul_f32 v[118:119], v[122:123], v[122:123]
	v_pk_mul_f32 v[124:125], v[130:131], v[130:131]
	v_pk_fma_f32 v[118:119], v[120:121], v[120:121], v[118:119]
	v_pk_fma_f32 v[124:125], v[128:129], v[128:129], v[124:125]
	s_lshl_b32 s16, s46, 5
	v_pk_add_f32 v[118:119], v[118:119], v[124:125]
	s_lshl_b32 s46, s48, 2
	v_pk_add_f32 v[124:125], v[152:153], v[118:119]
	s_or_b32 s17, s46, s12
	v_add_f32_e32 v124, v124, v125
	ds_swizzle_b32 v125, v124 offset:swizzle(SWAP,16)
	s_add_i32 s16, s17, s16
	s_ashr_i32 s17, s16, 31
	s_lshl_b64 s[16:17], s[16:17], 15
	v_cvt_pk_bf16_f32 v148, v116, v117
	v_lshl_add_u64 v[116:117], v[138:139], 0, s[16:17]
	v_cvt_pk_bf16_f32 v118, v120, v121
	v_cvt_pk_bf16_f32 v119, v122, v123
	v_cvt_pk_bf16_f32 v120, v128, v129
	v_cvt_pk_bf16_f32 v121, v130, v131
	ds_bpermute_b32 v232, v244, v118
	ds_bpermute_b32 v233, v244, v119
	ds_bpermute_b32 v234, v244, v120
	ds_bpermute_b32 v235, v244, v121
	ds_bpermute_b32 v236, v244, v116
	s_ashr_i32 s47, s46, 31
	v_cvt_pk_bf16_f32 v151, v126, v127
	s_waitcnt lgkmcnt(0)
	v_subrev_u32_e32 v236, s82, v236
	global_store_dwordx4 v236, v[232:235], s[82:83] offset:64
	ds_bpermute_b32 v238, v244, v148
	ds_bpermute_b32 v239, v244, v149
	ds_bpermute_b32 v240, v244, v150
	ds_bpermute_b32 v241, v244, v151
	ds_bpermute_b32 v242, v244, v116
	s_waitcnt lgkmcnt(0)
	v_add_f32_e32 v118, v124, v125
	v_mov_b32_e32 v119, v118
	s_nop 1
	v_permlane32_swap_b32_e32 v118, v119
	s_waitcnt lgkmcnt(0)
	v_subrev_u32_e32 v242, s82, v242
	global_store_dwordx4 v242, v[238:241], s[82:83]
	s_and_saveexec_b64 s[48:49], s[38:39]
	s_cbranch_execz .LBB0_1084
	v_ashrrev_i32_e32 v145, 31, v144
	v_add_f32_e32 v120, v118, v119
	v_lshlrev_b64 v[118:119], 7, v[144:145]
	v_lshl_add_u64 v[118:119], s[8:9], 0, v[118:119]
	v_lshl_add_u64 v[118:119], s[46:47], 2, v[118:119]
	s_lshl_b32 s24, s12, 2
	v_lshl_add_u64 v[118:119], v[118:119], 0, s[24:25]
	global_store_dword v[118:119], v120, off
.LBB0_1084:
	s_or_b64 exec, exec, s[48:49]
	v_pk_mul_f32 v[118:119], v[100:101], v[100:101]
	v_pk_mul_f32 v[120:121], v[104:105], v[104:105]
	v_pk_fma_f32 v[118:119], v[98:99], v[98:99], v[118:119]
	v_cvt_pk_bf16_f32 v98, v98, v99
	v_cvt_pk_bf16_f32 v99, v100, v101
	v_cvt_pk_bf16_f32 v100, v102, v103
	v_cvt_pk_bf16_f32 v101, v104, v105
	ds_bpermute_b32 v232, v244, v98
	ds_bpermute_b32 v233, v244, v99
	ds_bpermute_b32 v234, v244, v100
	ds_bpermute_b32 v235, v244, v101
	ds_bpermute_b32 v236, v244, v116
	v_pk_fma_f32 v[120:121], v[102:103], v[102:103], v[120:121]
	s_nop 0
	v_pk_mul_f32 v[98:99], v[108:109], v[108:109]
	v_pk_mul_f32 v[100:101], v[112:113], v[112:113]
	v_pk_fma_f32 v[98:99], v[106:107], v[106:107], v[98:99]
	v_pk_fma_f32 v[100:101], v[110:111], v[110:111], v[100:101]
	v_pk_add_f32 v[118:119], v[118:119], v[120:121]
	v_pk_add_f32 v[98:99], v[98:99], v[100:101]
	s_nop 0
	v_pk_add_f32 v[100:101], v[118:119], v[98:99]
	v_cvt_pk_bf16_f32 v98, v106, v107
	v_cvt_pk_bf16_f32 v99, v108, v109
	s_nop 0
	v_add_f32_e32 v102, v100, v101
	ds_swizzle_b32 v103, v102 offset:swizzle(SWAP,16)
	v_cvt_pk_bf16_f32 v100, v110, v111
	v_cvt_pk_bf16_f32 v101, v112, v113
	s_waitcnt lgkmcnt(0)
	v_subrev_u32_e32 v236, s82, v236
	global_store_dwordx4 v236, v[232:235], s[82:83] offset:2048
	ds_bpermute_b32 v238, v244, v98
	ds_bpermute_b32 v239, v244, v99
	ds_bpermute_b32 v240, v244, v100
	ds_bpermute_b32 v241, v244, v101
	ds_bpermute_b32 v242, v244, v116
	s_waitcnt lgkmcnt(0)
	s_nop 0
	v_add_f32_e32 v98, v102, v103
	v_mov_b32_e32 v99, v98
	s_nop 1
	v_permlane32_swap_b32_e32 v98, v99
	s_waitcnt lgkmcnt(0)
	v_subrev_u32_e32 v242, s82, v242
	global_store_dwordx4 v242, v[238:241], s[82:83] offset:2112
	s_and_saveexec_b64 s[48:49], s[38:39]
	s_cbranch_execz .LBB0_1086
	v_or_b32_e32 v100, 16, v144
	v_ashrrev_i32_e32 v101, 31, v100
	v_add_f32_e32 v102, v98, v99
	v_lshlrev_b64 v[98:99], 7, v[100:101]
	v_lshl_add_u64 v[98:99], s[8:9], 0, v[98:99]
	v_lshl_add_u64 v[98:99], s[46:47], 2, v[98:99]
	s_lshl_b32 s24, s12, 2
	v_lshl_add_u64 v[98:99], v[98:99], 0, s[24:25]
	global_store_dword v[98:99], v102, off
.LBB0_1086:
	s_or_b64 exec, exec, s[48:49]
	v_pk_mul_f32 v[98:99], v[84:85], v[84:85]
	v_pk_mul_f32 v[100:101], v[92:93], v[92:93]
	v_pk_fma_f32 v[98:99], v[82:83], v[82:83], v[98:99]
	v_pk_fma_f32 v[100:101], v[90:91], v[90:91], v[100:101]
	s_nop 0
	v_pk_add_f32 v[102:103], v[98:99], v[100:101]
	v_cvt_pk_bf16_f32 v99, v84, v85
	v_cvt_pk_bf16_f32 v100, v90, v91
	v_pk_mul_f32 v[84:85], v[88:89], v[88:89]
	v_pk_mul_f32 v[90:91], v[96:97], v[96:97]
	v_pk_fma_f32 v[84:85], v[86:87], v[86:87], v[84:85]
	v_pk_fma_f32 v[90:91], v[94:95], v[94:95], v[90:91]
	v_cvt_pk_bf16_f32 v98, v82, v83
	v_add_co_u32_e32 v82, vcc, s73, v116
	v_pk_add_f32 v[84:85], v[84:85], v[90:91]
	s_nop 0
	v_addc_co_u32_e32 v83, vcc, 0, v117, vcc
	v_pk_add_f32 v[90:91], v[102:103], v[84:85]
	v_cvt_pk_bf16_f32 v84, v86, v87
	v_cvt_pk_bf16_f32 v85, v88, v89
	v_cvt_pk_bf16_f32 v86, v94, v95
	v_cvt_pk_bf16_f32 v87, v96, v97
	ds_bpermute_b32 v232, v244, v84
	ds_bpermute_b32 v233, v244, v85
	ds_bpermute_b32 v234, v244, v86
	ds_bpermute_b32 v235, v244, v87
	ds_bpermute_b32 v236, v244, v82
	v_add_f32_e32 v90, v90, v91
	ds_swizzle_b32 v91, v90 offset:swizzle(SWAP,16)
	v_cvt_pk_bf16_f32 v101, v92, v93
	s_waitcnt lgkmcnt(0)
	v_subrev_u32_e32 v236, s82, v236
	global_store_dwordx4 v236, v[232:235], s[82:83] offset:64
	ds_bpermute_b32 v238, v244, v98
	ds_bpermute_b32 v239, v244, v99
	ds_bpermute_b32 v240, v244, v100
	ds_bpermute_b32 v241, v244, v101
	ds_bpermute_b32 v242, v244, v82
	s_waitcnt lgkmcnt(0)
	v_add_f32_e32 v84, v90, v91
	v_mov_b32_e32 v85, v84
	s_nop 1
	v_permlane32_swap_b32_e32 v84, v85
	s_waitcnt lgkmcnt(0)
	v_subrev_u32_e32 v242, s82, v242
	global_store_dwordx4 v242, v[238:241], s[82:83]
	s_and_saveexec_b64 s[48:49], s[38:39]
	s_cbranch_execz .LBB0_1088
	v_or_b32_e32 v86, 32, v144
	v_ashrrev_i32_e32 v87, 31, v86
	v_add_f32_e32 v88, v84, v85
	v_lshlrev_b64 v[84:85], 7, v[86:87]
	v_lshl_add_u64 v[84:85], s[8:9], 0, v[84:85]
	v_lshl_add_u64 v[84:85], s[46:47], 2, v[84:85]
	s_lshl_b32 s24, s12, 2
	v_lshl_add_u64 v[84:85], v[84:85], 0, s[24:25]
	global_store_dword v[84:85], v88, off
.LBB0_1088:
	s_or_b64 exec, exec, s[48:49]
	v_pk_mul_f32 v[84:85], v[60:61], v[60:61]
	v_pk_mul_f32 v[86:87], v[72:73], v[72:73]
	v_pk_fma_f32 v[84:85], v[58:59], v[58:59], v[84:85]
	v_cvt_pk_bf16_f32 v58, v58, v59
	v_cvt_pk_bf16_f32 v59, v60, v61
	v_cvt_pk_bf16_f32 v60, v70, v71
	v_cvt_pk_bf16_f32 v61, v72, v73
	ds_bpermute_b32 v232, v244, v58
	ds_bpermute_b32 v233, v244, v59
	ds_bpermute_b32 v234, v244, v60
	ds_bpermute_b32 v235, v244, v61
	ds_bpermute_b32 v236, v244, v82
	v_pk_fma_f32 v[86:87], v[70:71], v[70:71], v[86:87]
	s_nop 0
	v_pk_mul_f32 v[58:59], v[76:77], v[76:77]
	v_pk_mul_f32 v[60:61], v[80:81], v[80:81]
	v_pk_fma_f32 v[58:59], v[74:75], v[74:75], v[58:59]
	v_pk_fma_f32 v[60:61], v[78:79], v[78:79], v[60:61]
	v_pk_add_f32 v[84:85], v[84:85], v[86:87]
	v_pk_add_f32 v[58:59], v[58:59], v[60:61]
	s_nop 0
	v_pk_add_f32 v[60:61], v[84:85], v[58:59]
	v_cvt_pk_bf16_f32 v58, v74, v75
	v_cvt_pk_bf16_f32 v59, v76, v77
	s_nop 0
	v_add_f32_e32 v70, v60, v61
	ds_swizzle_b32 v71, v70 offset:swizzle(SWAP,16)
	v_cvt_pk_bf16_f32 v60, v78, v79
	v_cvt_pk_bf16_f32 v61, v80, v81
	s_waitcnt lgkmcnt(0)
	v_subrev_u32_e32 v236, s82, v236
	global_store_dwordx4 v236, v[232:235], s[82:83] offset:2048
	ds_bpermute_b32 v238, v244, v58
	ds_bpermute_b32 v239, v244, v59
	ds_bpermute_b32 v240, v244, v60
	ds_bpermute_b32 v241, v244, v61
	ds_bpermute_b32 v242, v244, v82
	s_waitcnt lgkmcnt(0)
	s_nop 0
	v_add_f32_e32 v58, v70, v71
	v_mov_b32_e32 v59, v58
	s_nop 1
	v_permlane32_swap_b32_e32 v58, v59
	s_waitcnt lgkmcnt(0)
	v_subrev_u32_e32 v242, s82, v242
	global_store_dwordx4 v242, v[238:241], s[82:83] offset:2112
	s_and_saveexec_b64 s[48:49], s[38:39]
	s_cbranch_execz .LBB0_1090
	v_or_b32_e32 v60, 48, v144
	v_ashrrev_i32_e32 v61, 31, v60
	v_add_f32_e32 v70, v58, v59
	v_lshlrev_b64 v[58:59], 7, v[60:61]
	v_lshl_add_u64 v[58:59], s[8:9], 0, v[58:59]
	v_lshl_add_u64 v[58:59], s[46:47], 2, v[58:59]
	s_lshl_b32 s24, s12, 2
	v_lshl_add_u64 v[58:59], v[58:59], 0, s[24:25]
	global_store_dword v[58:59], v70, off
.LBB0_1090:
	s_or_b64 exec, exec, s[48:49]
	v_pk_mul_f32 v[58:59], v[52:53], v[52:53]
	v_pk_mul_f32 v[60:61], v[64:65], v[64:65]
	v_pk_fma_f32 v[58:59], v[50:51], v[50:51], v[58:59]
	v_pk_fma_f32 v[60:61], v[62:63], v[62:63], v[60:61]
	s_nop 0
	v_pk_add_f32 v[70:71], v[58:59], v[60:61]
	v_cvt_pk_bf16_f32 v58, v50, v51
	v_add_co_u32_e32 v50, vcc, s72, v116
	v_cvt_pk_bf16_f32 v59, v52, v53
	v_cvt_pk_bf16_f32 v60, v62, v63
	v_cvt_pk_bf16_f32 v61, v64, v65
	v_pk_mul_f32 v[52:53], v[56:57], v[56:57]
	s_nop 0
	v_addc_co_u32_e32 v51, vcc, 0, v117, vcc
	ds_bpermute_b32 v232, v244, v58
	ds_bpermute_b32 v233, v244, v59
	ds_bpermute_b32 v234, v244, v60
	ds_bpermute_b32 v235, v244, v61
	ds_bpermute_b32 v236, v244, v50
	v_pk_fma_f32 v[52:53], v[54:55], v[54:55], v[52:53]
	s_nop 0
	v_pk_mul_f32 v[58:59], v[68:69], v[68:69]
	s_nop 0
	v_pk_fma_f32 v[58:59], v[66:67], v[66:67], v[58:59]
	s_nop 0
	v_pk_add_f32 v[52:53], v[52:53], v[58:59]
	s_nop 0
	v_pk_add_f32 v[58:59], v[70:71], v[52:53]
	v_cvt_pk_bf16_f32 v52, v54, v55
	v_cvt_pk_bf16_f32 v53, v56, v57
	v_cvt_pk_bf16_f32 v54, v66, v67
	v_cvt_pk_bf16_f32 v55, v68, v69
	s_waitcnt lgkmcnt(0)
	v_subrev_u32_e32 v236, s82, v236
	global_store_dwordx4 v236, v[232:235], s[82:83]
	ds_bpermute_b32 v238, v244, v52
	ds_bpermute_b32 v239, v244, v53
	ds_bpermute_b32 v240, v244, v54
	ds_bpermute_b32 v241, v244, v55
	ds_bpermute_b32 v242, v244, v50
	v_add_f32_e32 v58, v58, v59
	ds_swizzle_b32 v59, v58 offset:swizzle(SWAP,16)
	s_waitcnt lgkmcnt(0)
	v_add_f32_e32 v52, v58, v59
	v_mov_b32_e32 v53, v52
	s_nop 1
	v_permlane32_swap_b32_e32 v52, v53
	s_waitcnt lgkmcnt(0)
	v_subrev_u32_e32 v242, s82, v242
	global_store_dwordx4 v242, v[238:241], s[82:83] offset:64
	s_and_saveexec_b64 s[48:49], s[38:39]
	s_cbranch_execz .LBB0_1092
	v_ashrrev_i32_e32 v145, 31, v144
	v_add_f32_e32 v54, v52, v53
	v_lshlrev_b64 v[52:53], 7, v[144:145]
	v_lshl_add_u64 v[52:53], s[8:9], 0, v[52:53]
	v_lshl_add_u64 v[52:53], s[46:47], 2, v[52:53]
	s_lshl_b32 s24, s12, 2
	v_lshl_add_u64 v[52:53], v[52:53], 0, s[24:25]
	v_add_co_u32_e32 v52, vcc, 0x4000, v52
	s_nop 1
	v_addc_co_u32_e32 v53, vcc, 0, v53, vcc
	global_store_dword v[52:53], v54, off
.LBB0_1092:
	s_or_b64 exec, exec, s[48:49]
	v_pk_mul_f32 v[52:53], v[36:37], v[36:37]
	v_pk_mul_f32 v[54:55], v[40:41], v[40:41]
	v_pk_fma_f32 v[52:53], v[34:35], v[34:35], v[52:53]
	v_cvt_pk_bf16_f32 v34, v34, v35
	v_cvt_pk_bf16_f32 v35, v36, v37
	v_cvt_pk_bf16_f32 v36, v38, v39
	v_cvt_pk_bf16_f32 v37, v40, v41
	ds_bpermute_b32 v232, v244, v34
	ds_bpermute_b32 v233, v244, v35
	ds_bpermute_b32 v234, v244, v36
	ds_bpermute_b32 v235, v244, v37
	ds_bpermute_b32 v236, v244, v50
	v_pk_fma_f32 v[54:55], v[38:39], v[38:39], v[54:55]
	s_nop 0
	v_pk_mul_f32 v[34:35], v[44:45], v[44:45]
	v_pk_mul_f32 v[36:37], v[48:49], v[48:49]
	v_pk_fma_f32 v[34:35], v[42:43], v[42:43], v[34:35]
	v_pk_fma_f32 v[36:37], v[46:47], v[46:47], v[36:37]
	v_pk_add_f32 v[52:53], v[52:53], v[54:55]
	v_pk_add_f32 v[34:35], v[34:35], v[36:37]
	s_nop 0
	v_pk_add_f32 v[36:37], v[52:53], v[34:35]
	v_cvt_pk_bf16_f32 v34, v42, v43
	v_cvt_pk_bf16_f32 v35, v44, v45
	s_nop 0
	v_add_f32_e32 v38, v36, v37
	ds_swizzle_b32 v39, v38 offset:swizzle(SWAP,16)
	v_cvt_pk_bf16_f32 v36, v46, v47
	v_cvt_pk_bf16_f32 v37, v48, v49
	s_waitcnt lgkmcnt(0)
	v_subrev_u32_e32 v236, s82, v236
	global_store_dwordx4 v236, v[232:235], s[82:83] offset:2048
	ds_bpermute_b32 v238, v244, v34
	ds_bpermute_b32 v239, v244, v35
	ds_bpermute_b32 v240, v244, v36
	ds_bpermute_b32 v241, v244, v37
	ds_bpermute_b32 v242, v244, v50
	s_waitcnt lgkmcnt(0)
	s_nop 0
	v_add_f32_e32 v34, v38, v39
	v_mov_b32_e32 v35, v34
	s_nop 1
	v_permlane32_swap_b32_e32 v34, v35
	s_waitcnt lgkmcnt(0)
	v_subrev_u32_e32 v242, s82, v242
	global_store_dwordx4 v242, v[238:241], s[82:83] offset:2112
	s_and_saveexec_b64 s[48:49], s[38:39]
	s_cbranch_execz .LBB0_1094
	v_ashrrev_i32_e32 v145, 31, v144
	v_add_f32_e32 v36, v34, v35
	v_lshlrev_b64 v[34:35], 7, v[144:145]
	v_lshl_add_u64 v[34:35], s[8:9], 0, v[34:35]
	v_lshl_add_u64 v[34:35], s[46:47], 2, v[34:35]
	s_lshl_b32 s24, s12, 2
	v_lshl_add_u64 v[34:35], v[34:35], 0, s[24:25]
	v_add_co_u32_e32 v34, vcc, 0x4000, v34
	s_nop 1
	v_addc_co_u32_e32 v35, vcc, 0, v35, vcc
	global_store_dword v[34:35], v36, off offset:2048
.LBB0_1094:
	s_or_b64 exec, exec, s[48:49]
	v_pk_mul_f32 v[34:35], v[20:21], v[20:21]
	v_pk_mul_f32 v[36:37], v[28:29], v[28:29]
	v_pk_fma_f32 v[34:35], v[18:19], v[18:19], v[34:35]
	v_pk_fma_f32 v[36:37], v[26:27], v[26:27], v[36:37]
	s_nop 0
	v_pk_add_f32 v[38:39], v[34:35], v[36:37]
	v_cvt_pk_bf16_f32 v35, v20, v21
	v_cvt_pk_bf16_f32 v36, v26, v27
	v_pk_mul_f32 v[20:21], v[24:25], v[24:25]
	v_pk_mul_f32 v[26:27], v[32:33], v[32:33]
	v_pk_fma_f32 v[20:21], v[22:23], v[22:23], v[20:21]
	v_pk_fma_f32 v[26:27], v[30:31], v[30:31], v[26:27]
	v_cvt_pk_bf16_f32 v34, v18, v19
	v_add_co_u32_e32 v18, vcc, s31, v116
	v_pk_add_f32 v[20:21], v[20:21], v[26:27]
	s_nop 0
	v_addc_co_u32_e32 v19, vcc, 0, v117, vcc
	v_pk_add_f32 v[26:27], v[38:39], v[20:21]
	v_cvt_pk_bf16_f32 v20, v22, v23
	v_cvt_pk_bf16_f32 v21, v24, v25
	v_cvt_pk_bf16_f32 v22, v30, v31
	v_cvt_pk_bf16_f32 v23, v32, v33
	ds_bpermute_b32 v232, v244, v20
	ds_bpermute_b32 v233, v244, v21
	ds_bpermute_b32 v234, v244, v22
	ds_bpermute_b32 v235, v244, v23
	ds_bpermute_b32 v236, v244, v18
	v_add_f32_e32 v26, v26, v27
	ds_swizzle_b32 v27, v26 offset:swizzle(SWAP,16)
	v_cvt_pk_bf16_f32 v37, v28, v29
	s_waitcnt lgkmcnt(0)
	v_subrev_u32_e32 v236, s82, v236
	global_store_dwordx4 v236, v[232:235], s[82:83] offset:64
	ds_bpermute_b32 v238, v244, v34
	ds_bpermute_b32 v239, v244, v35
	ds_bpermute_b32 v240, v244, v36
	ds_bpermute_b32 v241, v244, v37
	ds_bpermute_b32 v242, v244, v18
	s_waitcnt lgkmcnt(0)
	v_add_f32_e32 v20, v26, v27
	v_mov_b32_e32 v21, v20
	s_nop 1
	v_permlane32_swap_b32_e32 v20, v21
	s_waitcnt lgkmcnt(0)
	v_subrev_u32_e32 v242, s82, v242
	global_store_dwordx4 v242, v[238:241], s[82:83]
	s_and_saveexec_b64 s[48:49], s[38:39]
	s_cbranch_execz .LBB0_1096
	v_ashrrev_i32_e32 v145, 31, v144
	v_add_f32_e32 v22, v20, v21
	v_lshlrev_b64 v[20:21], 7, v[144:145]
	v_lshl_add_u64 v[20:21], s[8:9], 0, v[20:21]
	v_lshl_add_u64 v[20:21], s[46:47], 2, v[20:21]
	s_lshl_b32 s24, s12, 2
	v_lshl_add_u64 v[20:21], v[20:21], 0, s[24:25]
	v_add_co_u32_e32 v20, vcc, 0x5000, v20
	s_nop 1
	v_addc_co_u32_e32 v21, vcc, 0, v21, vcc
	global_store_dword v[20:21], v22, off
.LBB0_1096:
	s_or_b64 exec, exec, s[48:49]
	v_pk_mul_f32 v[20:21], v[4:5], v[4:5]
	v_pk_mul_f32 v[22:23], v[8:9], v[8:9]
	v_pk_fma_f32 v[20:21], v[2:3], v[2:3], v[20:21]
	v_cvt_pk_bf16_f32 v2, v2, v3
	v_cvt_pk_bf16_f32 v3, v4, v5
	v_cvt_pk_bf16_f32 v4, v6, v7
	v_cvt_pk_bf16_f32 v5, v8, v9
	ds_bpermute_b32 v232, v244, v2
	ds_bpermute_b32 v233, v244, v3
	ds_bpermute_b32 v234, v244, v4
	ds_bpermute_b32 v235, v244, v5
	ds_bpermute_b32 v236, v244, v18
	v_pk_fma_f32 v[22:23], v[6:7], v[6:7], v[22:23]
	s_nop 0
	v_pk_mul_f32 v[2:3], v[12:13], v[12:13]
	v_pk_mul_f32 v[4:5], v[16:17], v[16:17]
	v_pk_fma_f32 v[2:3], v[10:11], v[10:11], v[2:3]
	v_pk_fma_f32 v[4:5], v[14:15], v[14:15], v[4:5]
	v_pk_add_f32 v[20:21], v[20:21], v[22:23]
	v_pk_add_f32 v[2:3], v[2:3], v[4:5]
	s_nop 0
	v_pk_add_f32 v[4:5], v[20:21], v[2:3]
	v_cvt_pk_bf16_f32 v2, v10, v11
	v_cvt_pk_bf16_f32 v3, v12, v13
	s_nop 0
	v_add_f32_e32 v6, v4, v5
	ds_swizzle_b32 v7, v6 offset:swizzle(SWAP,16)
	v_cvt_pk_bf16_f32 v4, v14, v15
	v_cvt_pk_bf16_f32 v5, v16, v17
	s_waitcnt lgkmcnt(0)
	v_subrev_u32_e32 v236, s82, v236
	global_store_dwordx4 v236, v[232:235], s[82:83] offset:2048
	ds_bpermute_b32 v238, v244, v2
	ds_bpermute_b32 v239, v244, v3
	ds_bpermute_b32 v240, v244, v4
	ds_bpermute_b32 v241, v244, v5
	ds_bpermute_b32 v242, v244, v18
	s_waitcnt lgkmcnt(0)
	s_nop 0
	v_add_f32_e32 v2, v6, v7
	v_mov_b32_e32 v3, v2
	s_nop 1
	v_permlane32_swap_b32_e32 v2, v3
	s_waitcnt lgkmcnt(0)
	v_subrev_u32_e32 v242, s82, v242
	global_store_dwordx4 v242, v[238:241], s[82:83] offset:2112
	s_and_saveexec_b64 s[48:49], s[38:39]
	s_cbranch_execz .LBB0_1098
	v_ashrrev_i32_e32 v145, 31, v144
	v_add_f32_e32 v4, v2, v3
	v_lshlrev_b64 v[2:3], 7, v[144:145]
	v_lshl_add_u64 v[2:3], s[8:9], 0, v[2:3]
	v_lshl_add_u64 v[2:3], s[46:47], 2, v[2:3]
	s_lshl_b32 s24, s12, 2
	v_lshl_add_u64 v[2:3], v[2:3], 0, s[24:25]
	v_add_co_u32_e32 v2, vcc, 0x5000, v2
	s_nop 1
	v_addc_co_u32_e32 v3, vcc, 0, v3, vcc
	global_store_dword v[2:3], v4, off offset:2048

.LBB0_1233:
	v_mbcnt_lo_u32_b32 v244, -1, 0
	v_mbcnt_hi_u32_b32 v244, -1, v244
	v_lshrrev_b32_e32 v245, 2, v244
	v_and_b32_e32 v244, 3, v244
	v_lshl_add_u32 v244, v244, 4, v245
	v_lshlrev_b32_e32 v244, 2, v244
	v_lshl_add_u32 v148, s59, 10, v146
	ds_read2_b32 v[150:151], v148 offset1:16
	s_lshl_b32 s17, s58, 2
	v_med3_f32 v124, v124, 0, v193
	v_med3_f32 v125, v125, 0, v193
	s_lshl_b32 s16, s44, 7
	s_or_b32 s17, s17, s45
	s_waitcnt lgkmcnt(0)
	v_mul_f32_e32 v150, v150, v150
	v_pk_mul_f32 v[124:125], v[124:125], v[124:125]
	s_add_i32 s16, s17, s16
	v_pk_mul_f32 v[152:153], v[124:125], v[150:151] op_sel_hi:[1,0]
	v_med3_f32 v124, v130, 0, v193
	v_med3_f32 v125, v131, 0, v193
	s_ashr_i32 s17, s16, 31
	v_med3_f32 v128, v128, 0, v193
	v_med3_f32 v129, v129, 0, v193
	v_med3_f32 v126, v126, 0, v193
	v_med3_f32 v127, v127, 0, v193
	v_pk_mul_f32 v[124:125], v[124:125], v[124:125]
	s_lshl_b64 s[16:17], s[16:17], 15
	v_pk_mul_f32 v[128:129], v[128:129], v[128:129]
	v_pk_mul_f32 v[130:131], v[124:125], v[150:151] op_sel_hi:[1,0]
	v_pk_mul_f32 v[124:125], v[126:127], v[126:127]
	v_med3_f32 v116, v116, 0, v193
	v_med3_f32 v117, v117, 0, v193
	v_lshl_add_u64 v[144:145], v[138:139], 0, s[16:17]
	v_pk_mul_f32 v[128:129], v[128:129], v[150:151] op_sel_hi:[1,0]
	v_pk_mul_f32 v[154:155], v[124:125], v[150:151] op_sel_hi:[1,0]
	v_cvt_pk_bf16_f32 v124, v128, v129
	v_cvt_pk_bf16_f32 v125, v130, v131
	v_pk_mul_f32 v[116:117], v[116:117], v[116:117]
	v_cvt_pk_bf16_f32 v126, v152, v153
	v_cvt_pk_bf16_f32 v127, v154, v155
	ds_bpermute_b32 v232, v244, v124
	ds_bpermute_b32 v233, v244, v125
	ds_bpermute_b32 v234, v244, v126
	ds_bpermute_b32 v235, v244, v127
	ds_bpermute_b32 v236, v244, v144
	v_med3_f32 v120, v120, 0, v193
	v_med3_f32 v121, v121, 0, v193
	v_pk_mul_f32 v[124:125], v[116:117], v[150:151] op_sel_hi:[1,0]
	v_med3_f32 v116, v122, 0, v193
	v_med3_f32 v117, v123, 0, v193
	v_med3_f32 v118, v118, 0, v193
	v_med3_f32 v119, v119, 0, v193
	v_pk_mul_f32 v[116:117], v[116:117], v[116:117]
	v_pk_mul_f32 v[120:121], v[120:121], v[120:121]
	v_pk_mul_f32 v[122:123], v[116:117], v[150:151] op_sel_hi:[1,0]
	v_pk_mul_f32 v[116:117], v[118:119], v[118:119]
	v_pk_mul_f32 v[120:121], v[120:121], v[150:151] op_sel_hi:[1,0]
	v_pk_mul_f32 v[126:127], v[116:117], v[150:151] op_sel_hi:[1,0]
	v_cvt_pk_bf16_f32 v116, v120, v121
	v_med3_f32 v106, v106, 0, v193
	v_med3_f32 v107, v107, 0, v193
	v_cvt_pk_bf16_f32 v117, v122, v123
	v_cvt_pk_bf16_f32 v118, v124, v125
	v_cvt_pk_bf16_f32 v119, v126, v127
	s_waitcnt lgkmcnt(0)
	v_subrev_u32_e32 v236, s82, v236
	global_store_dwordx4 v236, v[232:235], s[82:83]
	ds_bpermute_b32 v238, v244, v116
	ds_bpermute_b32 v239, v244, v117
	ds_bpermute_b32 v240, v244, v118
	ds_bpermute_b32 v241, v244, v119
	ds_bpermute_b32 v242, v244, v144
	v_pk_mul_f32 v[106:107], v[106:107], v[106:107]
	v_med3_f32 v110, v110, 0, v193
	v_mul_f32_e32 v116, v151, v151
	v_pk_mul_f32 v[118:119], v[106:107], v[116:117] op_sel_hi:[1,0]
	v_med3_f32 v106, v112, 0, v193
	v_med3_f32 v107, v113, 0, v193
	v_med3_f32 v111, v111, 0, v193
	v_med3_f32 v108, v108, 0, v193
	v_med3_f32 v109, v109, 0, v193
	v_pk_mul_f32 v[106:107], v[106:107], v[106:107]
	v_pk_mul_f32 v[110:111], v[110:111], v[110:111]
	v_pk_mul_f32 v[112:113], v[106:107], v[116:117] op_sel_hi:[1,0]
	v_pk_mul_f32 v[106:107], v[108:109], v[108:109]
	v_med3_f32 v98, v98, 0, v193
	v_med3_f32 v99, v99, 0, v193
	v_pk_mul_f32 v[110:111], v[110:111], v[116:117] op_sel_hi:[1,0]
	v_pk_mul_f32 v[120:121], v[106:107], v[116:117] op_sel_hi:[1,0]
	v_cvt_pk_bf16_f32 v106, v110, v111
	v_cvt_pk_bf16_f32 v107, v112, v113
	v_pk_mul_f32 v[98:99], v[98:99], v[98:99]
	v_cvt_pk_bf16_f32 v108, v118, v119
	v_cvt_pk_bf16_f32 v109, v120, v121
	s_waitcnt lgkmcnt(0)
	v_subrev_u32_e32 v242, s82, v242
	global_store_dwordx4 v242, v[238:241], s[82:83] offset:64
	ds_bpermute_b32 v232, v244, v106
	ds_bpermute_b32 v233, v244, v107
	ds_bpermute_b32 v234, v244, v108
	ds_bpermute_b32 v235, v244, v109
	ds_bpermute_b32 v236, v244, v144
	v_med3_f32 v102, v102, 0, v193
	v_med3_f32 v103, v103, 0, v193
	v_pk_mul_f32 v[106:107], v[98:99], v[116:117] op_sel_hi:[1,0]
	v_med3_f32 v98, v104, 0, v193
	v_med3_f32 v99, v105, 0, v193
	v_pk_mul_f32 v[102:103], v[102:103], v[102:103]
	v_med3_f32 v100, v100, 0, v193
	v_med3_f32 v101, v101, 0, v193
	v_pk_mul_f32 v[98:99], v[98:99], v[98:99]
	v_pk_mul_f32 v[102:103], v[102:103], v[116:117] op_sel_hi:[1,0]
	v_pk_mul_f32 v[104:105], v[98:99], v[116:117] op_sel_hi:[1,0]
	v_pk_mul_f32 v[98:99], v[100:101], v[100:101]
	v_med3_f32 v90, v90, 0, v193
	v_pk_mul_f32 v[108:109], v[98:99], v[116:117] op_sel_hi:[1,0]
	v_cvt_pk_bf16_f32 v98, v102, v103
	ds_read2_b32 v[102:103], v148 offset0:32 offset1:48
	v_med3_f32 v91, v91, 0, v193
	v_cvt_pk_bf16_f32 v99, v104, v105
	v_cvt_pk_bf16_f32 v100, v106, v107
	v_cvt_pk_bf16_f32 v101, v108, v109
	s_waitcnt lgkmcnt(0)
	v_subrev_u32_e32 v236, s82, v236
	global_store_dwordx4 v236, v[232:235], s[82:83] offset:2048
	ds_bpermute_b32 v238, v244, v98
	ds_bpermute_b32 v239, v244, v99
	ds_bpermute_b32 v240, v244, v100
	ds_bpermute_b32 v241, v244, v101
	ds_bpermute_b32 v242, v244, v144
	v_pk_mul_f32 v[90:91], v[90:91], v[90:91]
	v_med3_f32 v94, v94, 0, v193
	s_waitcnt lgkmcnt(0)
	v_mul_f32_e32 v98, v102, v102
	v_med3_f32 v95, v95, 0, v193
	v_pk_mul_f32 v[100:101], v[90:91], v[98:99] op_sel_hi:[1,0]
	v_med3_f32 v90, v96, 0, v193
	v_med3_f32 v91, v97, 0, v193
	v_pk_mul_f32 v[94:95], v[94:95], v[94:95]
	v_med3_f32 v92, v92, 0, v193
	v_med3_f32 v93, v93, 0, v193
	v_pk_mul_f32 v[90:91], v[90:91], v[90:91]
	v_pk_mul_f32 v[94:95], v[94:95], v[98:99] op_sel_hi:[1,0]
	v_pk_mul_f32 v[96:97], v[90:91], v[98:99] op_sel_hi:[1,0]
	v_pk_mul_f32 v[90:91], v[92:93], v[92:93]
	v_med3_f32 v82, v82, 0, v193
	v_pk_mul_f32 v[104:105], v[90:91], v[98:99] op_sel_hi:[1,0]
	v_cvt_pk_bf16_f32 v90, v94, v95
	v_add_co_u32_e32 v94, vcc, s73, v144
	v_med3_f32 v83, v83, 0, v193
	v_cvt_pk_bf16_f32 v91, v96, v97
	s_nop 0
	v_addc_co_u32_e32 v95, vcc, 0, v145, vcc
	v_pk_mul_f32 v[82:83], v[82:83], v[82:83]
	v_cvt_pk_bf16_f32 v92, v100, v101
	v_cvt_pk_bf16_f32 v93, v104, v105
	s_waitcnt lgkmcnt(0)
	v_subrev_u32_e32 v242, s82, v242
	global_store_dwordx4 v242, v[238:241], s[82:83] offset:2112
	ds_bpermute_b32 v232, v244, v90
	ds_bpermute_b32 v233, v244, v91
	ds_bpermute_b32 v234, v244, v92
	ds_bpermute_b32 v235, v244, v93
	ds_bpermute_b32 v236, v244, v94
	v_med3_f32 v86, v86, 0, v193
	v_med3_f32 v87, v87, 0, v193
	v_pk_mul_f32 v[90:91], v[82:83], v[98:99] op_sel_hi:[1,0]
	v_med3_f32 v82, v88, 0, v193
	v_med3_f32 v83, v89, 0, v193
	v_med3_f32 v84, v84, 0, v193
	v_med3_f32 v85, v85, 0, v193
	v_pk_mul_f32 v[82:83], v[82:83], v[82:83]
	v_pk_mul_f32 v[86:87], v[86:87], v[86:87]
	v_pk_mul_f32 v[88:89], v[82:83], v[98:99] op_sel_hi:[1,0]
	v_pk_mul_f32 v[82:83], v[84:85], v[84:85]
	v_pk_mul_f32 v[86:87], v[86:87], v[98:99] op_sel_hi:[1,0]
	v_pk_mul_f32 v[92:93], v[82:83], v[98:99] op_sel_hi:[1,0]
	v_cvt_pk_bf16_f32 v82, v86, v87
	v_med3_f32 v74, v74, 0, v193
	v_med3_f32 v75, v75, 0, v193
	v_cvt_pk_bf16_f32 v83, v88, v89
	v_cvt_pk_bf16_f32 v84, v90, v91
	v_cvt_pk_bf16_f32 v85, v92, v93
	s_waitcnt lgkmcnt(0)
	v_subrev_u32_e32 v236, s82, v236
	global_store_dwordx4 v236, v[232:235], s[82:83]
	ds_bpermute_b32 v238, v244, v82
	ds_bpermute_b32 v239, v244, v83
	ds_bpermute_b32 v240, v244, v84
	ds_bpermute_b32 v241, v244, v85
	ds_bpermute_b32 v242, v244, v94
	v_pk_mul_f32 v[74:75], v[74:75], v[74:75]
	v_med3_f32 v78, v78, 0, v193
	v_mul_f32_e32 v82, v103, v103
	v_pk_mul_f32 v[84:85], v[74:75], v[82:83] op_sel_hi:[1,0]
	v_med3_f32 v74, v80, 0, v193
	v_med3_f32 v75, v81, 0, v193
	v_med3_f32 v79, v79, 0, v193
	v_med3_f32 v76, v76, 0, v193
	v_med3_f32 v77, v77, 0, v193
	v_pk_mul_f32 v[74:75], v[74:75], v[74:75]
	v_pk_mul_f32 v[78:79], v[78:79], v[78:79]
	v_pk_mul_f32 v[80:81], v[74:75], v[82:83] op_sel_hi:[1,0]
	v_pk_mul_f32 v[74:75], v[76:77], v[76:77]
	v_med3_f32 v66, v66, 0, v193
	v_med3_f32 v67, v67, 0, v193
	v_pk_mul_f32 v[78:79], v[78:79], v[82:83] op_sel_hi:[1,0]
	v_pk_mul_f32 v[86:87], v[74:75], v[82:83] op_sel_hi:[1,0]
	v_cvt_pk_bf16_f32 v74, v78, v79
	v_cvt_pk_bf16_f32 v75, v80, v81
	v_pk_mul_f32 v[66:67], v[66:67], v[66:67]
	v_cvt_pk_bf16_f32 v76, v84, v85
	v_cvt_pk_bf16_f32 v77, v86, v87
	s_waitcnt lgkmcnt(0)
	v_subrev_u32_e32 v242, s82, v242
	global_store_dwordx4 v242, v[238:241], s[82:83] offset:64
	ds_bpermute_b32 v232, v244, v74
	ds_bpermute_b32 v233, v244, v75
	ds_bpermute_b32 v234, v244, v76
	ds_bpermute_b32 v235, v244, v77
	ds_bpermute_b32 v236, v244, v94
	v_med3_f32 v70, v70, 0, v193
	v_med3_f32 v71, v71, 0, v193
	v_pk_mul_f32 v[74:75], v[66:67], v[82:83] op_sel_hi:[1,0]
	v_med3_f32 v66, v72, 0, v193
	v_med3_f32 v67, v73, 0, v193
	v_pk_mul_f32 v[70:71], v[70:71], v[70:71]
	v_med3_f32 v68, v68, 0, v193
	v_med3_f32 v69, v69, 0, v193
	v_pk_mul_f32 v[66:67], v[66:67], v[66:67]
	v_pk_mul_f32 v[70:71], v[70:71], v[82:83] op_sel_hi:[1,0]
	v_pk_mul_f32 v[72:73], v[66:67], v[82:83] op_sel_hi:[1,0]
	v_pk_mul_f32 v[66:67], v[68:69], v[68:69]
	v_med3_f32 v64, v64, 0, v193
	v_pk_mul_f32 v[76:77], v[66:67], v[82:83] op_sel_hi:[1,0]
	v_cvt_pk_bf16_f32 v66, v70, v71
	ds_read2_b32 v[70:71], v148 offset0:128 offset1:144
	v_med3_f32 v65, v65, 0, v193
	v_cvt_pk_bf16_f32 v67, v72, v73
	v_cvt_pk_bf16_f32 v68, v74, v75
	v_cvt_pk_bf16_f32 v69, v76, v77
	s_waitcnt lgkmcnt(0)
	v_subrev_u32_e32 v236, s82, v236
	global_store_dwordx4 v236, v[232:235], s[82:83] offset:2048
	ds_bpermute_b32 v238, v244, v66
	ds_bpermute_b32 v239, v244, v67
	ds_bpermute_b32 v240, v244, v68
	ds_bpermute_b32 v241, v244, v69
	ds_bpermute_b32 v242, v244, v94
	v_med3_f32 v60, v60, 0, v193
	v_med3_f32 v61, v61, 0, v193
	s_waitcnt lgkmcnt(0)
	v_mul_f32_e32 v66, v70, v70
	v_pk_mul_f32 v[64:65], v[64:65], v[64:65]
	v_med3_f32 v62, v62, 0, v193
	v_med3_f32 v63, v63, 0, v193
	v_med3_f32 v58, v58, 0, v193
	v_med3_f32 v59, v59, 0, v193
	v_pk_mul_f32 v[64:65], v[64:65], v[66:67] op_sel_hi:[1,0]
	v_pk_mul_f32 v[60:61], v[60:61], v[60:61]
	v_pk_mul_f32 v[62:63], v[62:63], v[62:63]
	v_pk_mul_f32 v[58:59], v[58:59], v[58:59]
	v_pk_mul_f32 v[68:69], v[60:61], v[66:67] op_sel_hi:[1,0]
	v_cvt_pk_bf16_f32 v61, v64, v65
	v_add_co_u32_e32 v64, vcc, s72, v144
	v_pk_mul_f32 v[62:63], v[62:63], v[66:67] op_sel_hi:[1,0]
	v_pk_mul_f32 v[58:59], v[58:59], v[66:67] op_sel_hi:[1,0]
	v_addc_co_u32_e32 v65, vcc, 0, v145, vcc
	v_cvt_pk_bf16_f32 v60, v62, v63
	v_cvt_pk_bf16_f32 v62, v58, v59
	v_add_co_u32_e32 v58, vcc, s31, v144
	v_med3_f32 v50, v50, 0, v193
	v_med3_f32 v51, v51, 0, v193
	v_addc_co_u32_e32 v59, vcc, 0, v145, vcc
	v_pk_mul_f32 v[50:51], v[50:51], v[50:51]
	v_cvt_pk_bf16_f32 v63, v68, v69
	s_waitcnt lgkmcnt(0)
	v_subrev_u32_e32 v242, s82, v242
	global_store_dwordx4 v242, v[238:241], s[82:83] offset:2112
	ds_bpermute_b32 v232, v244, v60
	ds_bpermute_b32 v233, v244, v61
	ds_bpermute_b32 v234, v244, v62
	ds_bpermute_b32 v235, v244, v63
	ds_bpermute_b32 v236, v244, v58
	v_med3_f32 v54, v54, 0, v193
	v_med3_f32 v55, v55, 0, v193
	v_pk_mul_f32 v[60:61], v[50:51], v[66:67] op_sel_hi:[1,0]
	v_med3_f32 v50, v56, 0, v193
	v_med3_f32 v51, v57, 0, v193
	v_med3_f32 v52, v52, 0, v193
	v_med3_f32 v53, v53, 0, v193
	v_pk_mul_f32 v[50:51], v[50:51], v[50:51]
	v_pk_mul_f32 v[54:55], v[54:55], v[54:55]
	v_pk_mul_f32 v[56:57], v[50:51], v[66:67] op_sel_hi:[1,0]
	v_pk_mul_f32 v[50:51], v[52:53], v[52:53]
	v_pk_mul_f32 v[54:55], v[54:55], v[66:67] op_sel_hi:[1,0]
	v_pk_mul_f32 v[62:63], v[50:51], v[66:67] op_sel_hi:[1,0]
	v_cvt_pk_bf16_f32 v50, v54, v55
	v_med3_f32 v42, v42, 0, v193
	v_med3_f32 v43, v43, 0, v193
	v_cvt_pk_bf16_f32 v51, v56, v57
	v_cvt_pk_bf16_f32 v52, v60, v61
	v_cvt_pk_bf16_f32 v53, v62, v63
	s_waitcnt lgkmcnt(0)
	v_subrev_u32_e32 v236, s82, v236
	global_store_dwordx4 v236, v[232:235], s[82:83] offset:-4096
	ds_bpermute_b32 v238, v244, v50
	ds_bpermute_b32 v239, v244, v51
	ds_bpermute_b32 v240, v244, v52
	ds_bpermute_b32 v241, v244, v53
	ds_bpermute_b32 v242, v244, v64
	v_pk_mul_f32 v[42:43], v[42:43], v[42:43]
	v_med3_f32 v46, v46, 0, v193
	v_mul_f32_e32 v50, v71, v71
	v_pk_mul_f32 v[52:53], v[42:43], v[50:51] op_sel_hi:[1,0]
	v_med3_f32 v42, v48, 0, v193
	v_med3_f32 v43, v49, 0, v193
	v_med3_f32 v47, v47, 0, v193
	v_med3_f32 v44, v44, 0, v193
	v_med3_f32 v45, v45, 0, v193
	v_pk_mul_f32 v[42:43], v[42:43], v[42:43]
	v_pk_mul_f32 v[46:47], v[46:47], v[46:47]
	v_pk_mul_f32 v[48:49], v[42:43], v[50:51] op_sel_hi:[1,0]
	v_pk_mul_f32 v[42:43], v[44:45], v[44:45]
	v_med3_f32 v34, v34, 0, v193
	v_med3_f32 v35, v35, 0, v193
	v_pk_mul_f32 v[46:47], v[46:47], v[50:51] op_sel_hi:[1,0]
	v_pk_mul_f32 v[54:55], v[42:43], v[50:51] op_sel_hi:[1,0]
	v_cvt_pk_bf16_f32 v42, v46, v47
	v_cvt_pk_bf16_f32 v43, v48, v49
	v_pk_mul_f32 v[34:35], v[34:35], v[34:35]
	v_cvt_pk_bf16_f32 v44, v52, v53
	v_cvt_pk_bf16_f32 v45, v54, v55
	s_waitcnt lgkmcnt(0)
	v_subrev_u32_e32 v242, s82, v242
	global_store_dwordx4 v242, v[238:241], s[82:83] offset:64
	ds_bpermute_b32 v232, v244, v42
	ds_bpermute_b32 v233, v244, v43
	ds_bpermute_b32 v234, v244, v44
	ds_bpermute_b32 v235, v244, v45
	ds_bpermute_b32 v236, v244, v64
	v_med3_f32 v38, v38, 0, v193
	v_med3_f32 v39, v39, 0, v193
	v_pk_mul_f32 v[42:43], v[34:35], v[50:51] op_sel_hi:[1,0]
	v_med3_f32 v34, v40, 0, v193
	v_med3_f32 v35, v41, 0, v193
	v_pk_mul_f32 v[38:39], v[38:39], v[38:39]
	v_med3_f32 v36, v36, 0, v193
	v_med3_f32 v37, v37, 0, v193
	v_pk_mul_f32 v[34:35], v[34:35], v[34:35]
	v_pk_mul_f32 v[38:39], v[38:39], v[50:51] op_sel_hi:[1,0]
	v_pk_mul_f32 v[40:41], v[34:35], v[50:51] op_sel_hi:[1,0]
	v_pk_mul_f32 v[34:35], v[36:37], v[36:37]
	v_med3_f32 v26, v26, 0, v193
	v_pk_mul_f32 v[44:45], v[34:35], v[50:51] op_sel_hi:[1,0]
	v_cvt_pk_bf16_f32 v34, v38, v39
	ds_read2_b32 v[38:39], v148 offset0:160 offset1:176
	v_med3_f32 v27, v27, 0, v193
	v_cvt_pk_bf16_f32 v35, v40, v41
	v_cvt_pk_bf16_f32 v36, v42, v43
	v_cvt_pk_bf16_f32 v37, v44, v45
	s_waitcnt lgkmcnt(0)
	v_subrev_u32_e32 v236, s82, v236
	global_store_dwordx4 v236, v[232:235], s[82:83] offset:2048
	ds_bpermute_b32 v238, v244, v34
	ds_bpermute_b32 v239, v244, v35
	ds_bpermute_b32 v240, v244, v36
	ds_bpermute_b32 v241, v244, v37
	ds_bpermute_b32 v242, v244, v64
	v_pk_mul_f32 v[26:27], v[26:27], v[26:27]
	v_med3_f32 v30, v30, 0, v193
	s_waitcnt lgkmcnt(0)
	v_mul_f32_e32 v34, v38, v38
	v_pk_mul_f32 v[36:37], v[26:27], v[34:35] op_sel_hi:[1,0]
	v_med3_f32 v26, v32, 0, v193
	v_med3_f32 v27, v33, 0, v193
	v_med3_f32 v31, v31, 0, v193
	v_med3_f32 v28, v28, 0, v193
	v_med3_f32 v29, v29, 0, v193
	v_pk_mul_f32 v[26:27], v[26:27], v[26:27]
	v_pk_mul_f32 v[30:31], v[30:31], v[30:31]
	v_pk_mul_f32 v[32:33], v[26:27], v[34:35] op_sel_hi:[1,0]
	v_pk_mul_f32 v[26:27], v[28:29], v[28:29]
	v_med3_f32 v18, v18, 0, v193
	v_med3_f32 v19, v19, 0, v193
	v_pk_mul_f32 v[30:31], v[30:31], v[34:35] op_sel_hi:[1,0]
	v_pk_mul_f32 v[40:41], v[26:27], v[34:35] op_sel_hi:[1,0]
	v_cvt_pk_bf16_f32 v26, v30, v31
	v_cvt_pk_bf16_f32 v27, v32, v33
	v_pk_mul_f32 v[18:19], v[18:19], v[18:19]
	v_cvt_pk_bf16_f32 v28, v36, v37
	v_cvt_pk_bf16_f32 v29, v40, v41
	s_waitcnt lgkmcnt(0)
	v_subrev_u32_e32 v242, s82, v242
	global_store_dwordx4 v242, v[238:241], s[82:83] offset:2112
	ds_bpermute_b32 v232, v244, v26
	ds_bpermute_b32 v233, v244, v27
	ds_bpermute_b32 v234, v244, v28
	ds_bpermute_b32 v235, v244, v29
	ds_bpermute_b32 v236, v244, v58
	v_med3_f32 v22, v22, 0, v193
	v_med3_f32 v23, v23, 0, v193
	v_pk_mul_f32 v[26:27], v[18:19], v[34:35] op_sel_hi:[1,0]
	v_med3_f32 v18, v24, 0, v193
	v_med3_f32 v19, v25, 0, v193
	v_med3_f32 v20, v20, 0, v193
	v_med3_f32 v21, v21, 0, v193
	v_pk_mul_f32 v[18:19], v[18:19], v[18:19]
	v_pk_mul_f32 v[22:23], v[22:23], v[22:23]
	v_pk_mul_f32 v[24:25], v[18:19], v[34:35] op_sel_hi:[1,0]
	v_pk_mul_f32 v[18:19], v[20:21], v[20:21]
	v_pk_mul_f32 v[22:23], v[22:23], v[34:35] op_sel_hi:[1,0]
	v_pk_mul_f32 v[28:29], v[18:19], v[34:35] op_sel_hi:[1,0]
	v_cvt_pk_bf16_f32 v18, v22, v23
	v_med3_f32 v10, v10, 0, v193
	v_med3_f32 v11, v11, 0, v193
	v_cvt_pk_bf16_f32 v19, v24, v25
	v_cvt_pk_bf16_f32 v20, v26, v27
	v_cvt_pk_bf16_f32 v21, v28, v29
	s_waitcnt lgkmcnt(0)
	v_subrev_u32_e32 v236, s82, v236
	global_store_dwordx4 v236, v[232:235], s[82:83]
	ds_bpermute_b32 v238, v244, v18
	ds_bpermute_b32 v239, v244, v19
	ds_bpermute_b32 v240, v244, v20
	ds_bpermute_b32 v241, v244, v21
	ds_bpermute_b32 v242, v244, v58
	v_pk_mul_f32 v[10:11], v[10:11], v[10:11]
	v_med3_f32 v14, v14, 0, v193
	v_mul_f32_e32 v18, v39, v39
	v_pk_mul_f32 v[20:21], v[10:11], v[18:19] op_sel_hi:[1,0]
	v_med3_f32 v10, v16, 0, v193
	v_med3_f32 v11, v17, 0, v193
	v_med3_f32 v15, v15, 0, v193
	v_med3_f32 v12, v12, 0, v193
	v_med3_f32 v13, v13, 0, v193
	v_pk_mul_f32 v[10:11], v[10:11], v[10:11]
	v_pk_mul_f32 v[14:15], v[14:15], v[14:15]
	v_pk_mul_f32 v[16:17], v[10:11], v[18:19] op_sel_hi:[1,0]
	v_pk_mul_f32 v[10:11], v[12:13], v[12:13]
	v_med3_f32 v2, v2, 0, v193
	v_med3_f32 v3, v3, 0, v193
	v_pk_mul_f32 v[14:15], v[14:15], v[18:19] op_sel_hi:[1,0]
	v_pk_mul_f32 v[22:23], v[10:11], v[18:19] op_sel_hi:[1,0]
	v_cvt_pk_bf16_f32 v10, v14, v15
	v_cvt_pk_bf16_f32 v11, v16, v17
	v_pk_mul_f32 v[2:3], v[2:3], v[2:3]
	v_cvt_pk_bf16_f32 v12, v20, v21
	v_cvt_pk_bf16_f32 v13, v22, v23
	s_waitcnt lgkmcnt(0)
	v_subrev_u32_e32 v242, s82, v242
	global_store_dwordx4 v242, v[238:241], s[82:83] offset:64
	ds_bpermute_b32 v232, v244, v10
	ds_bpermute_b32 v233, v244, v11
	ds_bpermute_b32 v234, v244, v12
	ds_bpermute_b32 v235, v244, v13
	ds_bpermute_b32 v236, v244, v58
	v_med3_f32 v6, v6, 0, v193
	v_med3_f32 v7, v7, 0, v193
	v_pk_mul_f32 v[10:11], v[2:3], v[18:19] op_sel_hi:[1,0]
	v_med3_f32 v2, v8, 0, v193
	v_med3_f32 v3, v9, 0, v193
	v_med3_f32 v4, v4, 0, v193
	v_med3_f32 v5, v5, 0, v193
	v_pk_mul_f32 v[2:3], v[2:3], v[2:3]
	v_pk_mul_f32 v[6:7], v[6:7], v[6:7]
	v_pk_mul_f32 v[8:9], v[2:3], v[18:19] op_sel_hi:[1,0]
	v_pk_mul_f32 v[2:3], v[4:5], v[4:5]
	s_andn2_b64 vcc, exec, s[38:39]
	s_mov_b64 s[38:39], -1
	v_pk_mul_f32 v[6:7], v[6:7], v[18:19] op_sel_hi:[1,0]
	v_pk_mul_f32 v[12:13], v[2:3], v[18:19] op_sel_hi:[1,0]
	v_cvt_pk_bf16_f32 v2, v6, v7
	v_cvt_pk_bf16_f32 v3, v8, v9
	v_cvt_pk_bf16_f32 v4, v10, v11
	s_nop 0
	v_cvt_pk_bf16_f32 v5, v12, v13
	s_waitcnt lgkmcnt(0)
	v_subrev_u32_e32 v236, s82, v236
	global_store_dwordx4 v236, v[232:235], s[82:83] offset:2048
	ds_bpermute_b32 v238, v244, v2
	ds_bpermute_b32 v239, v244, v3
	ds_bpermute_b32 v240, v244, v4
	ds_bpermute_b32 v241, v244, v5
	ds_bpermute_b32 v242, v244, v58
	s_waitcnt lgkmcnt(0)
	v_subrev_u32_e32 v242, s82, v242
	global_store_dwordx4 v242, v[238:241], s[82:83] offset:2112
	s_cbranch_vccnz .LBB0_1222
	s_andn2_b64 vcc, exec, s[0:1]
	s_cbranch_vccnz .LBB0_1221
	s_barrier
	s_branch .LBB0_1221

.LBB0_1337:
	v_mbcnt_lo_u32_b32 v244, -1, 0
	v_mbcnt_hi_u32_b32 v244, -1, v244
	v_lshrrev_b32_e32 v245, 2, v244
	v_and_b32_e32 v244, 3, v244
	v_lshl_add_u32 v244, v244, 4, v245
	v_lshlrev_b32_e32 v244, 2, v244
	v_pk_mul_f32 v[148:149], v[118:119], v[118:119]
	v_pk_mul_f32 v[150:151], v[126:127], v[126:127]
	v_pk_fma_f32 v[148:149], v[116:117], v[116:117], v[148:149]
	v_pk_fma_f32 v[150:151], v[124:125], v[124:125], v[150:151]
	v_lshl_add_u32 v144, s46, 8, v1
	v_pk_add_f32 v[152:153], v[148:149], v[150:151]
	v_cvt_pk_bf16_f32 v149, v118, v119
	v_cvt_pk_bf16_f32 v150, v124, v125
	v_pk_mul_f32 v[118:119], v[122:123], v[122:123]
	v_pk_mul_f32 v[124:125], v[130:131], v[130:131]
	v_pk_fma_f32 v[118:119], v[120:121], v[120:121], v[118:119]
	v_pk_fma_f32 v[124:125], v[128:129], v[128:129], v[124:125]
	s_lshl_b32 s16, s46, 5
	v_pk_add_f32 v[118:119], v[118:119], v[124:125]
	s_lshl_b32 s46, s48, 2
	v_pk_add_f32 v[124:125], v[152:153], v[118:119]
	s_or_b32 s17, s46, s14
	v_add_f32_e32 v124, v124, v125
	ds_swizzle_b32 v125, v124 offset:swizzle(SWAP,16)
	s_add_i32 s16, s17, s16
	s_ashr_i32 s17, s16, 31
	s_lshl_b64 s[16:17], s[16:17], 15
	v_cvt_pk_bf16_f32 v148, v116, v117
	v_lshl_add_u64 v[116:117], v[138:139], 0, s[16:17]
	v_cvt_pk_bf16_f32 v118, v120, v121
	v_cvt_pk_bf16_f32 v119, v122, v123
	v_cvt_pk_bf16_f32 v120, v128, v129
	v_cvt_pk_bf16_f32 v121, v130, v131
	ds_bpermute_b32 v232, v244, v118
	ds_bpermute_b32 v233, v244, v119
	ds_bpermute_b32 v234, v244, v120
	ds_bpermute_b32 v235, v244, v121
	ds_bpermute_b32 v236, v244, v116
	s_ashr_i32 s47, s46, 31
	v_cvt_pk_bf16_f32 v151, v126, v127
	s_waitcnt lgkmcnt(0)
	v_subrev_u32_e32 v236, s82, v236
	global_store_dwordx4 v236, v[232:235], s[82:83] offset:64
	ds_bpermute_b32 v238, v244, v148
	ds_bpermute_b32 v239, v244, v149
	ds_bpermute_b32 v240, v244, v150
	ds_bpermute_b32 v241, v244, v151
	ds_bpermute_b32 v242, v244, v116
	s_waitcnt lgkmcnt(0)
	v_add_f32_e32 v118, v124, v125
	v_mov_b32_e32 v119, v118
	s_nop 1
	v_permlane32_swap_b32_e32 v118, v119
	s_waitcnt lgkmcnt(0)
	v_subrev_u32_e32 v242, s82, v242
	global_store_dwordx4 v242, v[238:241], s[82:83]
	s_and_saveexec_b64 s[48:49], s[38:39]
	s_cbranch_execz .LBB0_1339
	v_ashrrev_i32_e32 v145, 31, v144
	v_add_f32_e32 v120, v118, v119
	v_lshlrev_b64 v[118:119], 7, v[144:145]
	v_lshl_add_u64 v[118:119], s[8:9], 0, v[118:119]
	v_lshl_add_u64 v[118:119], s[46:47], 2, v[118:119]
	s_lshl_b32 s24, s14, 2
	v_lshl_add_u64 v[118:119], v[118:119], 0, s[24:25]
	global_store_dword v[118:119], v120, off
.LBB0_1339:
	s_or_b64 exec, exec, s[48:49]
	v_pk_mul_f32 v[118:119], v[100:101], v[100:101]
	v_pk_mul_f32 v[120:121], v[104:105], v[104:105]
	v_pk_fma_f32 v[118:119], v[98:99], v[98:99], v[118:119]
	v_cvt_pk_bf16_f32 v98, v98, v99
	v_cvt_pk_bf16_f32 v99, v100, v101
	v_cvt_pk_bf16_f32 v100, v102, v103
	v_cvt_pk_bf16_f32 v101, v104, v105
	ds_bpermute_b32 v232, v244, v98
	ds_bpermute_b32 v233, v244, v99
	ds_bpermute_b32 v234, v244, v100
	ds_bpermute_b32 v235, v244, v101
	ds_bpermute_b32 v236, v244, v116
	v_pk_fma_f32 v[120:121], v[102:103], v[102:103], v[120:121]
	s_nop 0
	v_pk_mul_f32 v[98:99], v[108:109], v[108:109]
	v_pk_mul_f32 v[100:101], v[112:113], v[112:113]
	v_pk_fma_f32 v[98:99], v[106:107], v[106:107], v[98:99]
	v_pk_fma_f32 v[100:101], v[110:111], v[110:111], v[100:101]
	v_pk_add_f32 v[118:119], v[118:119], v[120:121]
	v_pk_add_f32 v[98:99], v[98:99], v[100:101]
	s_nop 0
	v_pk_add_f32 v[100:101], v[118:119], v[98:99]
	v_cvt_pk_bf16_f32 v98, v106, v107
	v_cvt_pk_bf16_f32 v99, v108, v109
	s_nop 0
	v_add_f32_e32 v102, v100, v101
	ds_swizzle_b32 v103, v102 offset:swizzle(SWAP,16)
	v_cvt_pk_bf16_f32 v100, v110, v111
	v_cvt_pk_bf16_f32 v101, v112, v113
	s_waitcnt lgkmcnt(0)
	v_subrev_u32_e32 v236, s82, v236
	global_store_dwordx4 v236, v[232:235], s[82:83] offset:2048
	ds_bpermute_b32 v238, v244, v98
	ds_bpermute_b32 v239, v244, v99
	ds_bpermute_b32 v240, v244, v100
	ds_bpermute_b32 v241, v244, v101
	ds_bpermute_b32 v242, v244, v116
	s_waitcnt lgkmcnt(0)
	s_nop 0
	v_add_f32_e32 v98, v102, v103
	v_mov_b32_e32 v99, v98
	s_nop 1
	v_permlane32_swap_b32_e32 v98, v99
	s_waitcnt lgkmcnt(0)
	v_subrev_u32_e32 v242, s82, v242
	global_store_dwordx4 v242, v[238:241], s[82:83] offset:2112
	s_and_saveexec_b64 s[48:49], s[38:39]
	s_cbranch_execz .LBB0_1341
	v_or_b32_e32 v100, 16, v144
	v_ashrrev_i32_e32 v101, 31, v100
	v_add_f32_e32 v102, v98, v99
	v_lshlrev_b64 v[98:99], 7, v[100:101]
	v_lshl_add_u64 v[98:99], s[8:9], 0, v[98:99]
	v_lshl_add_u64 v[98:99], s[46:47], 2, v[98:99]
	s_lshl_b32 s24, s14, 2
	v_lshl_add_u64 v[98:99], v[98:99], 0, s[24:25]
	global_store_dword v[98:99], v102, off
.LBB0_1341:
	s_or_b64 exec, exec, s[48:49]
	v_pk_mul_f32 v[98:99], v[84:85], v[84:85]
	v_pk_mul_f32 v[100:101], v[92:93], v[92:93]
	v_pk_fma_f32 v[98:99], v[82:83], v[82:83], v[98:99]
	v_pk_fma_f32 v[100:101], v[90:91], v[90:91], v[100:101]
	s_nop 0
	v_pk_add_f32 v[102:103], v[98:99], v[100:101]
	v_cvt_pk_bf16_f32 v99, v84, v85
	v_cvt_pk_bf16_f32 v100, v90, v91
	v_pk_mul_f32 v[84:85], v[88:89], v[88:89]
	v_pk_mul_f32 v[90:91], v[96:97], v[96:97]
	v_pk_fma_f32 v[84:85], v[86:87], v[86:87], v[84:85]
	v_pk_fma_f32 v[90:91], v[94:95], v[94:95], v[90:91]
	v_cvt_pk_bf16_f32 v98, v82, v83
	v_add_co_u32_e32 v82, vcc, s73, v116
	v_pk_add_f32 v[84:85], v[84:85], v[90:91]
	s_nop 0
	v_addc_co_u32_e32 v83, vcc, 0, v117, vcc
	v_pk_add_f32 v[90:91], v[102:103], v[84:85]
	v_cvt_pk_bf16_f32 v84, v86, v87
	v_cvt_pk_bf16_f32 v85, v88, v89
	v_cvt_pk_bf16_f32 v86, v94, v95
	v_cvt_pk_bf16_f32 v87, v96, v97
	ds_bpermute_b32 v232, v244, v84
	ds_bpermute_b32 v233, v244, v85
	ds_bpermute_b32 v234, v244, v86
	ds_bpermute_b32 v235, v244, v87
	ds_bpermute_b32 v236, v244, v82
	v_add_f32_e32 v90, v90, v91
	ds_swizzle_b32 v91, v90 offset:swizzle(SWAP,16)
	v_cvt_pk_bf16_f32 v101, v92, v93
	s_waitcnt lgkmcnt(0)
	v_subrev_u32_e32 v236, s82, v236
	global_store_dwordx4 v236, v[232:235], s[82:83] offset:64
	ds_bpermute_b32 v238, v244, v98
	ds_bpermute_b32 v239, v244, v99
	ds_bpermute_b32 v240, v244, v100
	ds_bpermute_b32 v241, v244, v101
	ds_bpermute_b32 v242, v244, v82
	s_waitcnt lgkmcnt(0)
	v_add_f32_e32 v84, v90, v91
	v_mov_b32_e32 v85, v84
	s_nop 1
	v_permlane32_swap_b32_e32 v84, v85
	s_waitcnt lgkmcnt(0)
	v_subrev_u32_e32 v242, s82, v242
	global_store_dwordx4 v242, v[238:241], s[82:83]
	s_and_saveexec_b64 s[48:49], s[38:39]
	s_cbranch_execz .LBB0_1343
	v_or_b32_e32 v86, 32, v144
	v_ashrrev_i32_e32 v87, 31, v86
	v_add_f32_e32 v88, v84, v85
	v_lshlrev_b64 v[84:85], 7, v[86:87]
	v_lshl_add_u64 v[84:85], s[8:9], 0, v[84:85]
	v_lshl_add_u64 v[84:85], s[46:47], 2, v[84:85]
	s_lshl_b32 s24, s14, 2
	v_lshl_add_u64 v[84:85], v[84:85], 0, s[24:25]
	global_store_dword v[84:85], v88, off
.LBB0_1343:
	s_or_b64 exec, exec, s[48:49]
	v_pk_mul_f32 v[84:85], v[60:61], v[60:61]
	v_pk_mul_f32 v[86:87], v[72:73], v[72:73]
	v_pk_fma_f32 v[84:85], v[58:59], v[58:59], v[84:85]
	v_cvt_pk_bf16_f32 v58, v58, v59
	v_cvt_pk_bf16_f32 v59, v60, v61
	v_cvt_pk_bf16_f32 v60, v70, v71
	v_cvt_pk_bf16_f32 v61, v72, v73
	ds_bpermute_b32 v232, v244, v58
	ds_bpermute_b32 v233, v244, v59
	ds_bpermute_b32 v234, v244, v60
	ds_bpermute_b32 v235, v244, v61
	ds_bpermute_b32 v236, v244, v82
	v_pk_fma_f32 v[86:87], v[70:71], v[70:71], v[86:87]
	s_nop 0
	v_pk_mul_f32 v[58:59], v[76:77], v[76:77]
	v_pk_mul_f32 v[60:61], v[80:81], v[80:81]
	v_pk_fma_f32 v[58:59], v[74:75], v[74:75], v[58:59]
	v_pk_fma_f32 v[60:61], v[78:79], v[78:79], v[60:61]
	v_pk_add_f32 v[84:85], v[84:85], v[86:87]
	v_pk_add_f32 v[58:59], v[58:59], v[60:61]
	s_nop 0
	v_pk_add_f32 v[60:61], v[84:85], v[58:59]
	v_cvt_pk_bf16_f32 v58, v74, v75
	v_cvt_pk_bf16_f32 v59, v76, v77
	s_nop 0
	v_add_f32_e32 v70, v60, v61
	ds_swizzle_b32 v71, v70 offset:swizzle(SWAP,16)
	v_cvt_pk_bf16_f32 v60, v78, v79
	v_cvt_pk_bf16_f32 v61, v80, v81
	s_waitcnt lgkmcnt(0)
	v_subrev_u32_e32 v236, s82, v236
	global_store_dwordx4 v236, v[232:235], s[82:83] offset:2048
	ds_bpermute_b32 v238, v244, v58
	ds_bpermute_b32 v239, v244, v59
	ds_bpermute_b32 v240, v244, v60
	ds_bpermute_b32 v241, v244, v61
	ds_bpermute_b32 v242, v244, v82
	s_waitcnt lgkmcnt(0)
	s_nop 0
	v_add_f32_e32 v58, v70, v71
	v_mov_b32_e32 v59, v58
	s_nop 1
	v_permlane32_swap_b32_e32 v58, v59
	s_waitcnt lgkmcnt(0)
	v_subrev_u32_e32 v242, s82, v242
	global_store_dwordx4 v242, v[238:241], s[82:83] offset:2112
	s_and_saveexec_b64 s[48:49], s[38:39]
	s_cbranch_execz .LBB0_1345
	v_or_b32_e32 v60, 48, v144
	v_ashrrev_i32_e32 v61, 31, v60
	v_add_f32_e32 v70, v58, v59
	v_lshlrev_b64 v[58:59], 7, v[60:61]
	v_lshl_add_u64 v[58:59], s[8:9], 0, v[58:59]
	v_lshl_add_u64 v[58:59], s[46:47], 2, v[58:59]
	s_lshl_b32 s24, s14, 2
	v_lshl_add_u64 v[58:59], v[58:59], 0, s[24:25]
	global_store_dword v[58:59], v70, off
.LBB0_1345:
	s_or_b64 exec, exec, s[48:49]
	v_pk_mul_f32 v[58:59], v[52:53], v[52:53]
	v_pk_mul_f32 v[60:61], v[64:65], v[64:65]
	v_pk_fma_f32 v[58:59], v[50:51], v[50:51], v[58:59]
	v_pk_fma_f32 v[60:61], v[62:63], v[62:63], v[60:61]
	s_nop 0
	v_pk_add_f32 v[70:71], v[58:59], v[60:61]
	v_cvt_pk_bf16_f32 v58, v50, v51
	v_add_co_u32_e32 v50, vcc, s72, v116
	v_cvt_pk_bf16_f32 v59, v52, v53
	v_cvt_pk_bf16_f32 v60, v62, v63
	v_cvt_pk_bf16_f32 v61, v64, v65
	v_pk_mul_f32 v[52:53], v[56:57], v[56:57]
	s_nop 0
	v_addc_co_u32_e32 v51, vcc, 0, v117, vcc
	ds_bpermute_b32 v232, v244, v58
	ds_bpermute_b32 v233, v244, v59
	ds_bpermute_b32 v234, v244, v60
	ds_bpermute_b32 v235, v244, v61
	ds_bpermute_b32 v236, v244, v50
	v_pk_fma_f32 v[52:53], v[54:55], v[54:55], v[52:53]
	s_nop 0
	v_pk_mul_f32 v[58:59], v[68:69], v[68:69]
	s_nop 0
	v_pk_fma_f32 v[58:59], v[66:67], v[66:67], v[58:59]
	s_nop 0
	v_pk_add_f32 v[52:53], v[52:53], v[58:59]
	s_nop 0
	v_pk_add_f32 v[58:59], v[70:71], v[52:53]
	v_cvt_pk_bf16_f32 v52, v54, v55
	v_cvt_pk_bf16_f32 v53, v56, v57
	v_cvt_pk_bf16_f32 v54, v66, v67
	v_cvt_pk_bf16_f32 v55, v68, v69
	s_waitcnt lgkmcnt(0)
	v_subrev_u32_e32 v236, s82, v236
	global_store_dwordx4 v236, v[232:235], s[82:83]
	ds_bpermute_b32 v238, v244, v52
	ds_bpermute_b32 v239, v244, v53
	ds_bpermute_b32 v240, v244, v54
	ds_bpermute_b32 v241, v244, v55
	ds_bpermute_b32 v242, v244, v50
	v_add_f32_e32 v58, v58, v59
	ds_swizzle_b32 v59, v58 offset:swizzle(SWAP,16)
	s_waitcnt lgkmcnt(0)
	v_add_f32_e32 v52, v58, v59
	v_mov_b32_e32 v53, v52
	s_nop 1
	v_permlane32_swap_b32_e32 v52, v53
	s_waitcnt lgkmcnt(0)
	v_subrev_u32_e32 v242, s82, v242
	global_store_dwordx4 v242, v[238:241], s[82:83] offset:64
	s_and_saveexec_b64 s[48:49], s[38:39]
	s_cbranch_execz .LBB0_1347
	v_ashrrev_i32_e32 v145, 31, v144
	v_add_f32_e32 v54, v52, v53
	v_lshlrev_b64 v[52:53], 7, v[144:145]
	v_lshl_add_u64 v[52:53], s[8:9], 0, v[52:53]
	v_lshl_add_u64 v[52:53], s[46:47], 2, v[52:53]
	s_lshl_b32 s24, s14, 2
	v_lshl_add_u64 v[52:53], v[52:53], 0, s[24:25]
	v_add_co_u32_e32 v52, vcc, 0x4000, v52
	s_nop 1
	v_addc_co_u32_e32 v53, vcc, 0, v53, vcc
	global_store_dword v[52:53], v54, off
.LBB0_1347:
	s_or_b64 exec, exec, s[48:49]
	v_pk_mul_f32 v[52:53], v[36:37], v[36:37]
	v_pk_mul_f32 v[54:55], v[40:41], v[40:41]
	v_pk_fma_f32 v[52:53], v[34:35], v[34:35], v[52:53]
	v_cvt_pk_bf16_f32 v34, v34, v35
	v_cvt_pk_bf16_f32 v35, v36, v37
	v_cvt_pk_bf16_f32 v36, v38, v39
	v_cvt_pk_bf16_f32 v37, v40, v41
	ds_bpermute_b32 v232, v244, v34
	ds_bpermute_b32 v233, v244, v35
	ds_bpermute_b32 v234, v244, v36
	ds_bpermute_b32 v235, v244, v37
	ds_bpermute_b32 v236, v244, v50
	v_pk_fma_f32 v[54:55], v[38:39], v[38:39], v[54:55]
	s_nop 0
	v_pk_mul_f32 v[34:35], v[44:45], v[44:45]
	v_pk_mul_f32 v[36:37], v[48:49], v[48:49]
	v_pk_fma_f32 v[34:35], v[42:43], v[42:43], v[34:35]
	v_pk_fma_f32 v[36:37], v[46:47], v[46:47], v[36:37]
	v_pk_add_f32 v[52:53], v[52:53], v[54:55]
	v_pk_add_f32 v[34:35], v[34:35], v[36:37]
	s_nop 0
	v_pk_add_f32 v[36:37], v[52:53], v[34:35]
	v_cvt_pk_bf16_f32 v34, v42, v43
	v_cvt_pk_bf16_f32 v35, v44, v45
	s_nop 0
	v_add_f32_e32 v38, v36, v37
	ds_swizzle_b32 v39, v38 offset:swizzle(SWAP,16)
	v_cvt_pk_bf16_f32 v36, v46, v47
	v_cvt_pk_bf16_f32 v37, v48, v49
	s_waitcnt lgkmcnt(0)
	v_subrev_u32_e32 v236, s82, v236
	global_store_dwordx4 v236, v[232:235], s[82:83] offset:2048
	ds_bpermute_b32 v238, v244, v34
	ds_bpermute_b32 v239, v244, v35
	ds_bpermute_b32 v240, v244, v36
	ds_bpermute_b32 v241, v244, v37
	ds_bpermute_b32 v242, v244, v50
	s_waitcnt lgkmcnt(0)
	s_nop 0
	v_add_f32_e32 v34, v38, v39
	v_mov_b32_e32 v35, v34
	s_nop 1
	v_permlane32_swap_b32_e32 v34, v35
	s_waitcnt lgkmcnt(0)
	v_subrev_u32_e32 v242, s82, v242
	global_store_dwordx4 v242, v[238:241], s[82:83] offset:2112
	s_and_saveexec_b64 s[48:49], s[38:39]
	s_cbranch_execz .LBB0_1349
	v_ashrrev_i32_e32 v145, 31, v144
	v_add_f32_e32 v36, v34, v35
	v_lshlrev_b64 v[34:35], 7, v[144:145]
	v_lshl_add_u64 v[34:35], s[8:9], 0, v[34:35]
	v_lshl_add_u64 v[34:35], s[46:47], 2, v[34:35]
	s_lshl_b32 s24, s14, 2
	v_lshl_add_u64 v[34:35], v[34:35], 0, s[24:25]
	v_add_co_u32_e32 v34, vcc, 0x4000, v34
	s_nop 1
	v_addc_co_u32_e32 v35, vcc, 0, v35, vcc
	global_store_dword v[34:35], v36, off offset:2048
.LBB0_1349:
	s_or_b64 exec, exec, s[48:49]
	v_pk_mul_f32 v[34:35], v[20:21], v[20:21]
	v_pk_mul_f32 v[36:37], v[28:29], v[28:29]
	v_pk_fma_f32 v[34:35], v[18:19], v[18:19], v[34:35]
	v_pk_fma_f32 v[36:37], v[26:27], v[26:27], v[36:37]
	s_nop 0
	v_pk_add_f32 v[38:39], v[34:35], v[36:37]
	v_cvt_pk_bf16_f32 v35, v20, v21
	v_cvt_pk_bf16_f32 v36, v26, v27
	v_pk_mul_f32 v[20:21], v[24:25], v[24:25]
	v_pk_mul_f32 v[26:27], v[32:33], v[32:33]
	v_pk_fma_f32 v[20:21], v[22:23], v[22:23], v[20:21]
	v_pk_fma_f32 v[26:27], v[30:31], v[30:31], v[26:27]
	v_cvt_pk_bf16_f32 v34, v18, v19
	v_add_co_u32_e32 v18, vcc, s31, v116
	v_pk_add_f32 v[20:21], v[20:21], v[26:27]
	s_nop 0
	v_addc_co_u32_e32 v19, vcc, 0, v117, vcc
	v_pk_add_f32 v[26:27], v[38:39], v[20:21]
	v_cvt_pk_bf16_f32 v20, v22, v23
	v_cvt_pk_bf16_f32 v21, v24, v25
	v_cvt_pk_bf16_f32 v22, v30, v31
	v_cvt_pk_bf16_f32 v23, v32, v33
	ds_bpermute_b32 v232, v244, v20
	ds_bpermute_b32 v233, v244, v21
	ds_bpermute_b32 v234, v244, v22
	ds_bpermute_b32 v235, v244, v23
	ds_bpermute_b32 v236, v244, v18
	v_add_f32_e32 v26, v26, v27
	ds_swizzle_b32 v27, v26 offset:swizzle(SWAP,16)
	v_cvt_pk_bf16_f32 v37, v28, v29
	s_waitcnt lgkmcnt(0)
	v_subrev_u32_e32 v236, s82, v236
	global_store_dwordx4 v236, v[232:235], s[82:83] offset:64
	ds_bpermute_b32 v238, v244, v34
	ds_bpermute_b32 v239, v244, v35
	ds_bpermute_b32 v240, v244, v36
	ds_bpermute_b32 v241, v244, v37
	ds_bpermute_b32 v242, v244, v18
	s_waitcnt lgkmcnt(0)
	v_add_f32_e32 v20, v26, v27
	v_mov_b32_e32 v21, v20
	s_nop 1
	v_permlane32_swap_b32_e32 v20, v21
	s_waitcnt lgkmcnt(0)
	v_subrev_u32_e32 v242, s82, v242
	global_store_dwordx4 v242, v[238:241], s[82:83]
	s_and_saveexec_b64 s[48:49], s[38:39]
	s_cbranch_execz .LBB0_1351
	v_ashrrev_i32_e32 v145, 31, v144
	v_add_f32_e32 v22, v20, v21
	v_lshlrev_b64 v[20:21], 7, v[144:145]
	v_lshl_add_u64 v[20:21], s[8:9], 0, v[20:21]
	v_lshl_add_u64 v[20:21], s[46:47], 2, v[20:21]
	s_lshl_b32 s24, s14, 2
	v_lshl_add_u64 v[20:21], v[20:21], 0, s[24:25]
	v_add_co_u32_e32 v20, vcc, 0x5000, v20
	s_nop 1
	v_addc_co_u32_e32 v21, vcc, 0, v21, vcc
	global_store_dword v[20:21], v22, off
.LBB0_1351:
	s_or_b64 exec, exec, s[48:49]
	v_pk_mul_f32 v[20:21], v[4:5], v[4:5]
	v_pk_mul_f32 v[22:23], v[8:9], v[8:9]
	v_pk_fma_f32 v[20:21], v[2:3], v[2:3], v[20:21]
	v_cvt_pk_bf16_f32 v2, v2, v3
	v_cvt_pk_bf16_f32 v3, v4, v5
	v_cvt_pk_bf16_f32 v4, v6, v7
	v_cvt_pk_bf16_f32 v5, v8, v9
	ds_bpermute_b32 v232, v244, v2
	ds_bpermute_b32 v233, v244, v3
	ds_bpermute_b32 v234, v244, v4
	ds_bpermute_b32 v235, v244, v5
	ds_bpermute_b32 v236, v244, v18
	v_pk_fma_f32 v[22:23], v[6:7], v[6:7], v[22:23]
	s_nop 0
	v_pk_mul_f32 v[2:3], v[12:13], v[12:13]
	v_pk_mul_f32 v[4:5], v[16:17], v[16:17]
	v_pk_fma_f32 v[2:3], v[10:11], v[10:11], v[2:3]
	v_pk_fma_f32 v[4:5], v[14:15], v[14:15], v[4:5]
	v_pk_add_f32 v[20:21], v[20:21], v[22:23]
	v_pk_add_f32 v[2:3], v[2:3], v[4:5]
	s_nop 0
	v_pk_add_f32 v[4:5], v[20:21], v[2:3]
	v_cvt_pk_bf16_f32 v2, v10, v11
	v_cvt_pk_bf16_f32 v3, v12, v13
	s_nop 0
	v_add_f32_e32 v6, v4, v5
	ds_swizzle_b32 v7, v6 offset:swizzle(SWAP,16)
	v_cvt_pk_bf16_f32 v4, v14, v15
	v_cvt_pk_bf16_f32 v5, v16, v17
	s_waitcnt lgkmcnt(0)
	v_subrev_u32_e32 v236, s82, v236
	global_store_dwordx4 v236, v[232:235], s[82:83] offset:2048
	ds_bpermute_b32 v238, v244, v2
	ds_bpermute_b32 v239, v244, v3
	ds_bpermute_b32 v240, v244, v4
	ds_bpermute_b32 v241, v244, v5
	ds_bpermute_b32 v242, v244, v18
	s_waitcnt lgkmcnt(0)
	s_nop 0
	v_add_f32_e32 v2, v6, v7
	v_mov_b32_e32 v3, v2
	s_nop 1
	v_permlane32_swap_b32_e32 v2, v3
	s_waitcnt lgkmcnt(0)
	v_subrev_u32_e32 v242, s82, v242
	global_store_dwordx4 v242, v[238:241], s[82:83] offset:2112
	s_and_saveexec_b64 s[48:49], s[38:39]
	s_cbranch_execz .LBB0_1353
	v_ashrrev_i32_e32 v145, 31, v144
	v_add_f32_e32 v4, v2, v3
	v_lshlrev_b64 v[2:3], 7, v[144:145]
	v_lshl_add_u64 v[2:3], s[8:9], 0, v[2:3]
	v_lshl_add_u64 v[2:3], s[46:47], 2, v[2:3]
	s_lshl_b32 s24, s14, 2
	v_lshl_add_u64 v[2:3], v[2:3], 0, s[24:25]
	v_add_co_u32_e32 v2, vcc, 0x5000, v2
	s_nop 1
	v_addc_co_u32_e32 v3, vcc, 0, v3, vcc
	global_store_dword v[2:3], v4, off offset:2048
